# GEMM K-loops: loading waves run at priority 2 (above the MFMA waves' priority 1) instead of 0
# speedup vs baseline: 1.0001x; 1.0001x over previous
.LBB0_1025:
	ds_read_b128 v[140:143], v134
	ds_read_b128 v[144:147], v134 offset:1024
	ds_read_b128 v[148:151], v134 offset:2048
	ds_read_b128 v[152:155], v134 offset:3072
	ds_read_b128 v[156:159], v135
	ds_read_b128 v[160:163], v135 offset:1024
	ds_read_b128 v[164:167], v135 offset:2048
	ds_read_b128 v[168:171], v135 offset:3072
	s_add_i32 s13, s12, 0xfffc0080
	s_cmp_eq_u32 s1, 12
	s_cselect_b32 s45, s29, s41
	s_cselect_b32 s44, s28, s40
	s_cselect_b32 s47, s31, s43
	s_cselect_b32 s46, s30, s42
	s_cselect_b32 s13, 0, s13
	s_cselect_b32 s49, s35, s53
	s_cselect_b32 s48, s34, s52
	s_cselect_b32 s51, s63, s5
	s_cselect_b32 s50, s62, s4
	s_mov_b32 m0, s91
	ds_read_b128 v[198:201], v136
	ds_read_b128 v[202:205], v136 offset:1024
	ds_read_b128 v[206:209], v136 offset:2048
	ds_read_b128 v[210:213], v136 offset:3072
	ds_read_b128 v[214:217], v136 offset:4096
	ds_read_b128 v[218:221], v136 offset:5120
	ds_read_b128 v[222:225], v136 offset:6144
	ds_read_b128 v[226:229], v136 offset:7168
	buffer_load_dwordx4 v132, s[40:43], s12 offen lds
	s_mov_b32 m0, s92
	s_nop 0
	buffer_load_dwordx4 v133, s[40:43], s12 offen lds
	s_waitcnt vmcnt(8)
	s_waitcnt lgkmcnt(0)
	s_barrier
	s_setprio 1
	s_waitcnt lgkmcnt(6)
	v_mfma_scale_f32_16x16x128_f8f6f4 v[124:127], v[140:147], v[198:205], v[124:127], v230, v230 op_sel_hi:[0,0,0]
	v_mfma_scale_f32_16x16x128_f8f6f4 v[120:123], v[148:155], v[198:205], v[120:123], v230, v230 op_sel_hi:[0,0,0]
	s_waitcnt lgkmcnt(4)
	v_mfma_scale_f32_16x16x128_f8f6f4 v[108:111], v[140:147], v[206:213], v[108:111], v230, v230 op_sel_hi:[0,0,0]
	v_mfma_scale_f32_16x16x128_f8f6f4 v[104:107], v[148:155], v[206:213], v[104:107], v230, v230 op_sel_hi:[0,0,0]
	s_waitcnt lgkmcnt(2)
	v_mfma_scale_f32_16x16x128_f8f6f4 v[172:175], v[140:147], v[214:221], v[92:95], v230, v230 op_sel_hi:[0,0,0]
	v_mfma_scale_f32_16x16x128_f8f6f4 v[246:249], v[148:155], v[214:221], v[88:91], v230, v230 op_sel_hi:[0,0,0]
	s_waitcnt lgkmcnt(0)
	v_mfma_scale_f32_16x16x128_f8f6f4 v[250:253], v[140:147], v[222:229], v[76:79], v230, v230 op_sel_hi:[0,0,0]
	v_mfma_scale_f32_16x16x128_f8f6f4 v[194:197], v[148:155], v[222:229], v[72:75], v230, v230 op_sel_hi:[0,0,0]
	s_setprio 2
	s_setprio 1
	v_mfma_scale_f32_16x16x128_f8f6f4 v[116:119], v[156:163], v[198:205], v[116:119], v230, v230 op_sel_hi:[0,0,0]
	v_mfma_scale_f32_16x16x128_f8f6f4 v[112:115], v[164:171], v[198:205], v[112:115], v230, v230 op_sel_hi:[0,0,0]
	v_mfma_scale_f32_16x16x128_f8f6f4 v[100:103], v[156:163], v[206:213], v[100:103], v230, v230 op_sel_hi:[0,0,0]
	v_mfma_scale_f32_16x16x128_f8f6f4 v[96:99], v[164:171], v[206:213], v[96:99], v230, v230 op_sel_hi:[0,0,0]
	v_mfma_scale_f32_16x16x128_f8f6f4 v[198:201], v[156:163], v[214:221], v[84:87], v230, v230 op_sel_hi:[0,0,0]
	v_mfma_scale_f32_16x16x128_f8f6f4 v[202:205], v[164:171], v[214:221], v[80:83], v230, v230 op_sel_hi:[0,0,0]
	v_mfma_scale_f32_16x16x128_f8f6f4 v[206:209], v[156:163], v[222:229], v[68:71], v230, v230 op_sel_hi:[0,0,0]
	v_mfma_scale_f32_16x16x128_f8f6f4 v[210:213], v[164:171], v[222:229], v[64:67], v230, v230 op_sel_hi:[0,0,0]
	s_setprio 2
	s_barrier
	s_mov_b32 m0, s69
	s_nop 3
	ds_read_b128 v[64:67], v136 offset:16384
	ds_read_b128 v[68:71], v136 offset:17408
	ds_read_b128 v[72:75], v136 offset:18432
	ds_read_b128 v[76:79], v136 offset:19456
	ds_read_b128 v[80:83], v136 offset:20480
	ds_read_b128 v[84:87], v136 offset:21504
	ds_read_b128 v[88:91], v136 offset:22528
	ds_read_b128 v[92:95], v136 offset:23552
	buffer_load_dwordx4 v245, s[48:51], s13 offen lds
	s_mov_b32 m0, s70
	s_add_i32 s21, s13, 0x40000
	buffer_load_dwordx4 v244, s[48:51], s13 offen lds
	s_mov_b32 m0, s71
	s_nop 0
	buffer_load_dwordx4 v245, s[48:51], s21 offen lds
	s_mov_b32 m0, s72
	s_nop 0
	buffer_load_dwordx4 v244, s[48:51], s21 offen lds
	s_mov_b32 m0, s68
	s_nop 0
	buffer_load_dwordx4 v132, s[44:47], s13 offen lds
	s_mov_b32 m0, s73
	s_nop 0
	buffer_load_dwordx4 v133, s[44:47], s13 offen lds
	s_waitcnt vmcnt(8)
	s_waitcnt lgkmcnt(0)
	s_barrier
	s_setprio 1
	s_waitcnt lgkmcnt(6)
	v_mfma_scale_f32_16x16x128_f8f6f4 v[60:63], v[140:147], v[64:71], v[60:63], v230, v230 op_sel_hi:[0,0,0]
	s_waitcnt lgkmcnt(0)
	v_mfma_scale_f32_16x16x128_f8f6f4 v[16:19], v[140:147], v[88:95], v[16:19], v230, v230 op_sel_hi:[0,0,0]
	v_mfma_scale_f32_16x16x128_f8f6f4 v[214:217], v[148:155], v[64:71], v[12:15], v230, v230 op_sel_hi:[0,0,0]
	v_mfma_scale_f32_16x16x128_f8f6f4 v[218:221], v[140:147], v[72:79], v[48:51], v230, v230 op_sel_hi:[0,0,0]
	v_mfma_scale_f32_16x16x128_f8f6f4 v[222:225], v[148:155], v[72:79], v[44:47], v230, v230 op_sel_hi:[0,0,0]
	v_mfma_scale_f32_16x16x128_f8f6f4 v[226:229], v[140:147], v[80:87], v[32:35], v230, v230 op_sel_hi:[0,0,0]
	v_mfma_scale_f32_16x16x128_f8f6f4 v[178:181], v[148:155], v[80:87], v[28:31], v230, v230 op_sel_hi:[0,0,0]
	v_mfma_scale_f32_16x16x128_f8f6f4 v[182:185], v[148:155], v[88:95], v[8:11], v230, v230 op_sel_hi:[0,0,0]
	s_setprio 2
	s_setprio 1
	v_mfma_scale_f32_16x16x128_f8f6f4 v[56:59], v[156:163], v[64:71], v[56:59], v230, v230 op_sel_hi:[0,0,0]
	v_mfma_scale_f32_16x16x128_f8f6f4 v[52:55], v[164:171], v[64:71], v[52:55], v230, v230 op_sel_hi:[0,0,0]
	v_mfma_scale_f32_16x16x128_f8f6f4 v[186:189], v[156:163], v[72:79], v[40:43], v230, v230 op_sel_hi:[0,0,0]
	v_mfma_scale_f32_16x16x128_f8f6f4 v[190:193], v[164:171], v[72:79], v[36:39], v230, v230 op_sel_hi:[0,0,0]
	v_mfma_scale_f32_16x16x128_f8f6f4 v[236:239], v[156:163], v[80:87], v[24:27], v230, v230 op_sel_hi:[0,0,0]
	v_mfma_scale_f32_16x16x128_f8f6f4 v[240:243], v[164:171], v[80:87], v[20:23], v230, v230 op_sel_hi:[0,0,0]
	v_mfma_scale_f32_16x16x128_f8f6f4 v[232:235], v[156:163], v[88:95], v[4:7], v230, v230 op_sel_hi:[0,0,0]
	v_mfma_scale_f32_16x16x128_f8f6f4 v[128:131], v[164:171], v[88:95], v[0:3], v230, v230 op_sel_hi:[0,0,0]
	s_setprio 2
	s_barrier
	s_nop 4
	ds_read_b128 v[0:3], v137
	ds_read_b128 v[4:7], v137 offset:1024
	ds_read_b128 v[20:23], v137 offset:2048
	ds_read_b128 v[24:27], v137 offset:3072
	ds_read_b128 v[140:143], v138
	ds_read_b128 v[144:147], v138 offset:1024
	ds_read_b128 v[148:151], v138 offset:2048
	ds_read_b128 v[152:155], v138 offset:3072
	s_mov_b32 m0, s76
	ds_read_b128 v[8:11], v136 offset:32768
	ds_read_b128 v[12:15], v136 offset:33792
	ds_read_b128 v[28:31], v136 offset:34816
	ds_read_b128 v[32:35], v136 offset:35840
	ds_read_b128 v[36:39], v136 offset:36864
	ds_read_b128 v[40:43], v136 offset:37888
	ds_read_b128 v[44:47], v136 offset:38912
	ds_read_b128 v[48:51], v136 offset:39936
	buffer_load_dwordx4 v132, s[44:47], s21 offen lds
	s_mov_b32 m0, s77
	s_nop 0
	buffer_load_dwordx4 v133, s[44:47], s21 offen lds
	s_waitcnt vmcnt(8)
	s_waitcnt lgkmcnt(0)
	s_barrier
	s_setprio 1
	s_waitcnt lgkmcnt(6)
	v_mfma_scale_f32_16x16x128_f8f6f4 v[124:127], v[0:7], v[8:15], v[124:127], v230, v230 op_sel_hi:[0,0,0]
	v_mfma_scale_f32_16x16x128_f8f6f4 v[120:123], v[20:27], v[8:15], v[120:123], v230, v230 op_sel_hi:[0,0,0]
	s_waitcnt lgkmcnt(4)
	v_mfma_scale_f32_16x16x128_f8f6f4 v[108:111], v[0:7], v[28:35], v[108:111], v230, v230 op_sel_hi:[0,0,0]
	v_mfma_scale_f32_16x16x128_f8f6f4 v[104:107], v[20:27], v[28:35], v[104:107], v230, v230 op_sel_hi:[0,0,0]
	s_waitcnt lgkmcnt(2)
	v_mfma_scale_f32_16x16x128_f8f6f4 v[92:95], v[0:7], v[36:43], v[172:175], v230, v230 op_sel_hi:[0,0,0]
	v_mfma_scale_f32_16x16x128_f8f6f4 v[88:91], v[20:27], v[36:43], v[246:249], v230, v230 op_sel_hi:[0,0,0]
	s_waitcnt lgkmcnt(0)
	v_mfma_scale_f32_16x16x128_f8f6f4 v[76:79], v[0:7], v[44:51], v[250:253], v230, v230 op_sel_hi:[0,0,0]
	v_mfma_scale_f32_16x16x128_f8f6f4 v[72:75], v[20:27], v[44:51], v[194:197], v230, v230 op_sel_hi:[0,0,0]
	s_setprio 2
	s_setprio 1
	v_mfma_scale_f32_16x16x128_f8f6f4 v[116:119], v[140:147], v[8:15], v[116:119], v230, v230 op_sel_hi:[0,0,0]
	v_mfma_scale_f32_16x16x128_f8f6f4 v[112:115], v[148:155], v[8:15], v[112:115], v230, v230 op_sel_hi:[0,0,0]
	v_mfma_scale_f32_16x16x128_f8f6f4 v[100:103], v[140:147], v[28:35], v[100:103], v230, v230 op_sel_hi:[0,0,0]
	v_mfma_scale_f32_16x16x128_f8f6f4 v[96:99], v[148:155], v[28:35], v[96:99], v230, v230 op_sel_hi:[0,0,0]
	v_mfma_scale_f32_16x16x128_f8f6f4 v[84:87], v[140:147], v[36:43], v[198:201], v230, v230 op_sel_hi:[0,0,0]
	v_mfma_scale_f32_16x16x128_f8f6f4 v[80:83], v[148:155], v[36:43], v[202:205], v230, v230 op_sel_hi:[0,0,0]
	v_mfma_scale_f32_16x16x128_f8f6f4 v[68:71], v[140:147], v[44:51], v[206:209], v230, v230 op_sel_hi:[0,0,0]
	v_mfma_scale_f32_16x16x128_f8f6f4 v[64:67], v[148:155], v[44:51], v[210:213], v230, v230 op_sel_hi:[0,0,0]
	s_setprio 2
	s_barrier
	s_mov_b32 m0, s78
	s_or_b32 s21, s13, 0x80
	ds_read_b128 v[36:39], v136 offset:49152
	ds_read_b128 v[40:43], v136 offset:50176
	ds_read_b128 v[156:159], v136 offset:51200
	ds_read_b128 v[160:163], v136 offset:52224
	ds_read_b128 v[164:167], v136 offset:53248
	ds_read_b128 v[168:171], v136 offset:54272
	ds_read_b128 v[198:201], v136 offset:55296
	ds_read_b128 v[202:205], v136 offset:56320
	buffer_load_dwordx4 v245, s[48:51], s21 offen lds
	s_mov_b32 m0, s79
	s_add_i32 s13, s13, 0x40080
	buffer_load_dwordx4 v244, s[48:51], s21 offen lds
	s_mov_b32 m0, s83
	s_nop 0
	buffer_load_dwordx4 v245, s[48:51], s13 offen lds
	s_mov_b32 m0, s88
	s_nop 0
	buffer_load_dwordx4 v244, s[48:51], s13 offen lds
	s_mov_b32 m0, s80
	s_nop 0
	buffer_load_dwordx4 v132, s[44:47], s21 offen lds
	s_mov_b32 m0, s82
	s_nop 0
	buffer_load_dwordx4 v133, s[44:47], s21 offen lds
	s_waitcnt vmcnt(8)
	s_waitcnt lgkmcnt(0)
	s_barrier
	s_setprio 1
	s_waitcnt lgkmcnt(6)
	v_mfma_scale_f32_16x16x128_f8f6f4 v[60:63], v[0:7], v[36:43], v[60:63], v230, v230 op_sel_hi:[0,0,0]
	v_mfma_scale_f32_16x16x128_f8f6f4 v[12:15], v[20:27], v[36:43], v[214:217], v230, v230 op_sel_hi:[0,0,0]
	s_waitcnt lgkmcnt(4)
	v_mfma_scale_f32_16x16x128_f8f6f4 v[48:51], v[0:7], v[156:163], v[218:221], v230, v230 op_sel_hi:[0,0,0]
	v_mfma_scale_f32_16x16x128_f8f6f4 v[44:47], v[20:27], v[156:163], v[222:225], v230, v230 op_sel_hi:[0,0,0]
	s_waitcnt lgkmcnt(2)
	v_mfma_scale_f32_16x16x128_f8f6f4 v[32:35], v[0:7], v[164:171], v[226:229], v230, v230 op_sel_hi:[0,0,0]
	v_mfma_scale_f32_16x16x128_f8f6f4 v[28:31], v[20:27], v[164:171], v[178:181], v230, v230 op_sel_hi:[0,0,0]
	s_waitcnt lgkmcnt(0)
	v_mfma_scale_f32_16x16x128_f8f6f4 v[16:19], v[0:7], v[198:205], v[16:19], v230, v230 op_sel_hi:[0,0,0]
	v_mfma_scale_f32_16x16x128_f8f6f4 v[8:11], v[20:27], v[198:205], v[182:185], v230, v230 op_sel_hi:[0,0,0]
	s_setprio 2
	s_setprio 1
	v_mfma_scale_f32_16x16x128_f8f6f4 v[56:59], v[140:147], v[36:43], v[56:59], v230, v230 op_sel_hi:[0,0,0]
	v_mfma_scale_f32_16x16x128_f8f6f4 v[52:55], v[148:155], v[36:43], v[52:55], v230, v230 op_sel_hi:[0,0,0]
	v_mfma_scale_f32_16x16x128_f8f6f4 v[40:43], v[140:147], v[156:163], v[186:189], v230, v230 op_sel_hi:[0,0,0]
	v_mfma_scale_f32_16x16x128_f8f6f4 v[36:39], v[148:155], v[156:163], v[190:193], v230, v230 op_sel_hi:[0,0,0]
	v_mfma_scale_f32_16x16x128_f8f6f4 v[24:27], v[140:147], v[164:171], v[236:239], v230, v230 op_sel_hi:[0,0,0]
	v_mfma_scale_f32_16x16x128_f8f6f4 v[20:23], v[148:155], v[164:171], v[240:243], v230, v230 op_sel_hi:[0,0,0]
	v_mfma_scale_f32_16x16x128_f8f6f4 v[4:7], v[140:147], v[198:205], v[232:235], v230, v230 op_sel_hi:[0,0,0]
	v_mfma_scale_f32_16x16x128_f8f6f4 v[0:3], v[148:155], v[198:205], v[128:131], v230, v230 op_sel_hi:[0,0,0]
	s_setprio 2
	s_barrier
	s_add_i32 s1, s1, 2
	s_addk_i32 s12, 0x100
	s_cmp_gt_u32 s1, 13
	s_cbranch_scc0 .LBB0_1025
	s_and_b64 vcc, exec, s[18:19]
	s_cbranch_vccz .LBB0_1028
	s_barrier

.LBB0_1051:
	v_add_u32_e32 v140, 0x10000, v150
	v_add_u32_e32 v144, 0x14000, v150
	ds_read_b128 v[120:123], v140
	ds_read_b128 v[124:127], v140 offset:1024
	ds_read_b128 v[136:139], v140 offset:2048
	ds_read_b128 v[140:143], v140 offset:3072
	ds_read_b128 v[152:155], v144
	ds_read_b128 v[156:159], v144 offset:1024
	ds_read_b128 v[160:163], v144 offset:2048
	ds_read_b128 v[164:167], v144 offset:3072
	s_add_i32 s38, s31, 0xfffc0080
	s_cmp_eq_u32 s29, 12
	s_cselect_b32 s45, s35, s41
	s_cselect_b32 s44, s34, s40
	s_cselect_b32 s47, s9, s43
	s_cselect_b32 s46, s8, s42
	s_cselect_b32 s38, 0, s38
	s_cselect_b32 s49, s3, s53
	s_cselect_b32 s48, s2, s52
	s_cselect_b32 s51, s13, s1
	s_cselect_b32 s50, s12, s0
	s_mov_b32 m0, s89
	ds_read_b128 v[168:171], v151
	ds_read_b128 v[172:175], v151 offset:1024
	ds_read_b128 v[198:201], v151 offset:2048
	ds_read_b128 v[202:205], v151 offset:3072
	ds_read_b128 v[206:209], v151 offset:4096
	ds_read_b128 v[210:213], v151 offset:5120
	ds_read_b128 v[214:217], v151 offset:6144
	ds_read_b128 v[218:221], v151 offset:7168
	buffer_load_dwordx4 v148, s[40:43], s31 offen lds
	s_mov_b32 m0, s88
	s_nop 0
	buffer_load_dwordx4 v149, s[40:43], s31 offen lds
	s_waitcnt vmcnt(8)
	s_waitcnt lgkmcnt(0)
	s_barrier
	s_setprio 1
	s_waitcnt lgkmcnt(6)
	v_mfma_scale_f32_16x16x128_f8f6f4 v[132:135], v[120:127], v[168:175], v[132:135], v230, v230 op_sel_hi:[0,0,0]
	v_mfma_scale_f32_16x16x128_f8f6f4 v[128:131], v[136:143], v[168:175], v[128:131], v230, v230 op_sel_hi:[0,0,0]
	s_waitcnt lgkmcnt(4)
	v_mfma_scale_f32_16x16x128_f8f6f4 v[108:111], v[120:127], v[198:205], v[108:111], v230, v230 op_sel_hi:[0,0,0]
	v_mfma_scale_f32_16x16x128_f8f6f4 v[104:107], v[136:143], v[198:205], v[104:107], v230, v230 op_sel_hi:[0,0,0]
	s_waitcnt lgkmcnt(2)
	v_mfma_scale_f32_16x16x128_f8f6f4 v[178:181], v[120:127], v[206:213], v[92:95], v230, v230 op_sel_hi:[0,0,0]
	v_mfma_scale_f32_16x16x128_f8f6f4 v[182:185], v[136:143], v[206:213], v[88:91], v230, v230 op_sel_hi:[0,0,0]
	s_waitcnt lgkmcnt(0)
	v_mfma_scale_f32_16x16x128_f8f6f4 v[186:189], v[120:127], v[214:221], v[76:79], v230, v230 op_sel_hi:[0,0,0]
	v_mfma_scale_f32_16x16x128_f8f6f4 v[190:193], v[136:143], v[214:221], v[72:75], v230, v230 op_sel_hi:[0,0,0]
	s_setprio 2
	s_setprio 1
	v_mfma_scale_f32_16x16x128_f8f6f4 v[116:119], v[152:159], v[168:175], v[116:119], v230, v230 op_sel_hi:[0,0,0]
	v_mfma_scale_f32_16x16x128_f8f6f4 v[112:115], v[160:167], v[168:175], v[112:115], v230, v230 op_sel_hi:[0,0,0]
	v_mfma_scale_f32_16x16x128_f8f6f4 v[100:103], v[152:159], v[198:205], v[100:103], v230, v230 op_sel_hi:[0,0,0]
	v_mfma_scale_f32_16x16x128_f8f6f4 v[96:99], v[160:167], v[198:205], v[96:99], v230, v230 op_sel_hi:[0,0,0]
	v_mfma_scale_f32_16x16x128_f8f6f4 v[168:171], v[152:159], v[206:213], v[84:87], v230, v230 op_sel_hi:[0,0,0]
	v_mfma_scale_f32_16x16x128_f8f6f4 v[172:175], v[160:167], v[206:213], v[80:83], v230, v230 op_sel_hi:[0,0,0]
	v_mfma_scale_f32_16x16x128_f8f6f4 v[194:197], v[152:159], v[214:221], v[68:71], v230, v230 op_sel_hi:[0,0,0]
	v_mfma_scale_f32_16x16x128_f8f6f4 v[198:201], v[160:167], v[214:221], v[64:67], v230, v230 op_sel_hi:[0,0,0]
	s_setprio 2
	s_barrier
	s_mov_b32 m0, s77
	s_nop 3
	ds_read_b128 v[64:67], v151 offset:16384
	ds_read_b128 v[68:71], v151 offset:17408
	ds_read_b128 v[72:75], v151 offset:18432
	ds_read_b128 v[76:79], v151 offset:19456
	ds_read_b128 v[80:83], v151 offset:20480
	ds_read_b128 v[84:87], v151 offset:21504
	ds_read_b128 v[88:91], v151 offset:22528
	ds_read_b128 v[92:95], v151 offset:23552
	buffer_load_dwordx4 v146, s[48:51], s38 offen lds
	s_mov_b32 m0, s64
	s_add_i32 s39, s38, 0x40000
	buffer_load_dwordx4 v147, s[48:51], s38 offen lds
	s_mov_b32 m0, s65
	s_nop 0
	buffer_load_dwordx4 v146, s[48:51], s39 offen lds
	s_mov_b32 m0, s22
	s_nop 0
	buffer_load_dwordx4 v147, s[48:51], s39 offen lds
	s_mov_b32 m0, s92
	s_nop 0
	buffer_load_dwordx4 v148, s[44:47], s38 offen lds
	s_mov_b32 m0, s23
	s_nop 0
	buffer_load_dwordx4 v149, s[44:47], s38 offen lds
	s_waitcnt vmcnt(8)
	s_waitcnt lgkmcnt(0)
	s_barrier
	s_setprio 1
	s_waitcnt lgkmcnt(6)
	v_mfma_scale_f32_16x16x128_f8f6f4 v[60:63], v[120:127], v[64:71], v[60:63], v230, v230 op_sel_hi:[0,0,0]
	v_mfma_scale_f32_16x16x128_f8f6f4 v[16:19], v[136:143], v[64:71], v[16:19], v230, v230 op_sel_hi:[0,0,0]
	s_waitcnt lgkmcnt(4)
	v_mfma_scale_f32_16x16x128_f8f6f4 v[202:205], v[120:127], v[72:79], v[48:51], v230, v230 op_sel_hi:[0,0,0]
	v_mfma_scale_f32_16x16x128_f8f6f4 v[206:209], v[136:143], v[72:79], v[44:47], v230, v230 op_sel_hi:[0,0,0]
	s_waitcnt lgkmcnt(2)
	v_mfma_scale_f32_16x16x128_f8f6f4 v[210:213], v[120:127], v[80:87], v[32:35], v230, v230 op_sel_hi:[0,0,0]
	v_mfma_scale_f32_16x16x128_f8f6f4 v[214:217], v[136:143], v[80:87], v[28:31], v230, v230 op_sel_hi:[0,0,0]
	s_waitcnt lgkmcnt(0)
	v_mfma_scale_f32_16x16x128_f8f6f4 v[218:221], v[120:127], v[88:95], v[12:15], v230, v230 op_sel_hi:[0,0,0]
	v_mfma_scale_f32_16x16x128_f8f6f4 v[222:225], v[136:143], v[88:95], v[8:11], v230, v230 op_sel_hi:[0,0,0]
	s_setprio 2
	s_setprio 1
	v_mfma_scale_f32_16x16x128_f8f6f4 v[56:59], v[152:159], v[64:71], v[56:59], v230, v230 op_sel_hi:[0,0,0]
	v_mfma_scale_f32_16x16x128_f8f6f4 v[52:55], v[160:167], v[64:71], v[52:55], v230, v230 op_sel_hi:[0,0,0]
	v_mfma_scale_f32_16x16x128_f8f6f4 v[226:229], v[152:159], v[72:79], v[40:43], v230, v230 op_sel_hi:[0,0,0]
	v_mfma_scale_f32_16x16x128_f8f6f4 v[232:235], v[160:167], v[72:79], v[36:39], v230, v230 op_sel_hi:[0,0,0]
	v_mfma_scale_f32_16x16x128_f8f6f4 v[236:239], v[152:159], v[80:87], v[24:27], v230, v230 op_sel_hi:[0,0,0]
	v_mfma_scale_f32_16x16x128_f8f6f4 v[240:243], v[160:167], v[80:87], v[20:23], v230, v230 op_sel_hi:[0,0,0]
	v_mfma_scale_f32_16x16x128_f8f6f4 v[244:247], v[152:159], v[88:95], v[4:7], v230, v230 op_sel_hi:[0,0,0]
	v_mfma_scale_f32_16x16x128_f8f6f4 v[248:251], v[160:167], v[88:95], v[0:3], v230, v230 op_sel_hi:[0,0,0]
	s_setprio 2
	s_barrier
	v_add_u32_e32 v8, 0x18000, v150
	s_nop 3
	ds_read_b128 v[0:3], v8
	ds_read_b128 v[4:7], v8 offset:1024
	ds_read_b128 v[20:23], v8 offset:2048
	ds_read_b128 v[24:27], v8 offset:3072
	v_add_u32_e32 v8, 0x1c000, v150
	ds_read_b128 v[120:123], v8
	ds_read_b128 v[124:127], v8 offset:1024
	ds_read_b128 v[136:139], v8 offset:2048
	ds_read_b128 v[140:143], v8 offset:3072
	s_mov_b32 m0, s33
	ds_read_b128 v[8:11], v151 offset:32768
	ds_read_b128 v[12:15], v151 offset:33792
	ds_read_b128 v[28:31], v151 offset:34816
	ds_read_b128 v[32:35], v151 offset:35840
	ds_read_b128 v[36:39], v151 offset:36864
	ds_read_b128 v[40:43], v151 offset:37888
	ds_read_b128 v[44:47], v151 offset:38912
	ds_read_b128 v[48:51], v151 offset:39936
	buffer_load_dwordx4 v148, s[44:47], s39 offen lds
	s_mov_b32 m0, s96
	s_nop 0
	buffer_load_dwordx4 v149, s[44:47], s39 offen lds
	s_waitcnt vmcnt(8)
	s_waitcnt lgkmcnt(0)
	s_barrier
	s_setprio 1
	s_waitcnt lgkmcnt(6)
	v_mfma_scale_f32_16x16x128_f8f6f4 v[132:135], v[0:7], v[8:15], v[132:135], v230, v230 op_sel_hi:[0,0,0]
	v_mfma_scale_f32_16x16x128_f8f6f4 v[128:131], v[20:27], v[8:15], v[128:131], v230, v230 op_sel_hi:[0,0,0]
	s_waitcnt lgkmcnt(4)
	v_mfma_scale_f32_16x16x128_f8f6f4 v[108:111], v[0:7], v[28:35], v[108:111], v230, v230 op_sel_hi:[0,0,0]
	v_mfma_scale_f32_16x16x128_f8f6f4 v[104:107], v[20:27], v[28:35], v[104:107], v230, v230 op_sel_hi:[0,0,0]
	s_waitcnt lgkmcnt(2)
	v_mfma_scale_f32_16x16x128_f8f6f4 v[92:95], v[0:7], v[36:43], v[178:181], v230, v230 op_sel_hi:[0,0,0]
	v_mfma_scale_f32_16x16x128_f8f6f4 v[88:91], v[20:27], v[36:43], v[182:185], v230, v230 op_sel_hi:[0,0,0]
	s_waitcnt lgkmcnt(0)
	v_mfma_scale_f32_16x16x128_f8f6f4 v[76:79], v[0:7], v[44:51], v[186:189], v230, v230 op_sel_hi:[0,0,0]
	v_mfma_scale_f32_16x16x128_f8f6f4 v[72:75], v[20:27], v[44:51], v[190:193], v230, v230 op_sel_hi:[0,0,0]
	s_setprio 2
	s_setprio 1
	v_mfma_scale_f32_16x16x128_f8f6f4 v[116:119], v[120:127], v[8:15], v[116:119], v230, v230 op_sel_hi:[0,0,0]
	v_mfma_scale_f32_16x16x128_f8f6f4 v[112:115], v[136:143], v[8:15], v[112:115], v230, v230 op_sel_hi:[0,0,0]
	v_mfma_scale_f32_16x16x128_f8f6f4 v[100:103], v[120:127], v[28:35], v[100:103], v230, v230 op_sel_hi:[0,0,0]
	v_mfma_scale_f32_16x16x128_f8f6f4 v[96:99], v[136:143], v[28:35], v[96:99], v230, v230 op_sel_hi:[0,0,0]
	v_mfma_scale_f32_16x16x128_f8f6f4 v[84:87], v[120:127], v[36:43], v[168:171], v230, v230 op_sel_hi:[0,0,0]
	v_mfma_scale_f32_16x16x128_f8f6f4 v[80:83], v[136:143], v[36:43], v[172:175], v230, v230 op_sel_hi:[0,0,0]
	v_mfma_scale_f32_16x16x128_f8f6f4 v[68:71], v[120:127], v[44:51], v[194:197], v230, v230 op_sel_hi:[0,0,0]
	v_mfma_scale_f32_16x16x128_f8f6f4 v[64:67], v[136:143], v[44:51], v[198:201], v230, v230 op_sel_hi:[0,0,0]
	s_setprio 2
	s_barrier
	s_mov_b32 m0, s69
	s_or_b32 s39, s38, 0x80
	ds_read_b128 v[36:39], v151 offset:49152
	ds_read_b128 v[40:43], v151 offset:50176
	ds_read_b128 v[152:155], v151 offset:51200
	ds_read_b128 v[156:159], v151 offset:52224
	ds_read_b128 v[160:163], v151 offset:53248
	ds_read_b128 v[164:167], v151 offset:54272
	ds_read_b128 v[168:171], v151 offset:55296
	ds_read_b128 v[172:175], v151 offset:56320
	buffer_load_dwordx4 v146, s[48:51], s39 offen lds
	s_mov_b32 m0, s61
	s_add_i32 s38, s38, 0x40080
	buffer_load_dwordx4 v147, s[48:51], s39 offen lds
	s_mov_b32 m0, s83
	s_nop 0
	buffer_load_dwordx4 v146, s[48:51], s38 offen lds
	s_mov_b32 m0, s82
	s_nop 0
	buffer_load_dwordx4 v147, s[48:51], s38 offen lds
	s_mov_b32 m0, s71
	s_nop 0
	buffer_load_dwordx4 v148, s[44:47], s39 offen lds
	s_mov_b32 m0, s70
	s_nop 0
	buffer_load_dwordx4 v149, s[44:47], s39 offen lds
	s_waitcnt vmcnt(8)
	s_waitcnt lgkmcnt(0)
	s_barrier
	s_setprio 1
	s_waitcnt lgkmcnt(6)
	v_mfma_scale_f32_16x16x128_f8f6f4 v[60:63], v[0:7], v[36:43], v[60:63], v230, v230 op_sel_hi:[0,0,0]
	v_mfma_scale_f32_16x16x128_f8f6f4 v[16:19], v[20:27], v[36:43], v[16:19], v230, v230 op_sel_hi:[0,0,0]
	s_waitcnt lgkmcnt(4)
	v_mfma_scale_f32_16x16x128_f8f6f4 v[48:51], v[0:7], v[152:159], v[202:205], v230, v230 op_sel_hi:[0,0,0]
	v_mfma_scale_f32_16x16x128_f8f6f4 v[44:47], v[20:27], v[152:159], v[206:209], v230, v230 op_sel_hi:[0,0,0]
	s_waitcnt lgkmcnt(2)
	v_mfma_scale_f32_16x16x128_f8f6f4 v[32:35], v[0:7], v[160:167], v[210:213], v230, v230 op_sel_hi:[0,0,0]
	v_mfma_scale_f32_16x16x128_f8f6f4 v[28:31], v[20:27], v[160:167], v[214:217], v230, v230 op_sel_hi:[0,0,0]
	s_waitcnt lgkmcnt(0)
	v_mfma_scale_f32_16x16x128_f8f6f4 v[12:15], v[0:7], v[168:175], v[218:221], v230, v230 op_sel_hi:[0,0,0]
	v_mfma_scale_f32_16x16x128_f8f6f4 v[8:11], v[20:27], v[168:175], v[222:225], v230, v230 op_sel_hi:[0,0,0]
	s_setprio 2
	s_setprio 1
	v_mfma_scale_f32_16x16x128_f8f6f4 v[56:59], v[120:127], v[36:43], v[56:59], v230, v230 op_sel_hi:[0,0,0]
	v_mfma_scale_f32_16x16x128_f8f6f4 v[52:55], v[136:143], v[36:43], v[52:55], v230, v230 op_sel_hi:[0,0,0]
	v_mfma_scale_f32_16x16x128_f8f6f4 v[40:43], v[120:127], v[152:159], v[226:229], v230, v230 op_sel_hi:[0,0,0]
	v_mfma_scale_f32_16x16x128_f8f6f4 v[36:39], v[136:143], v[152:159], v[232:235], v230, v230 op_sel_hi:[0,0,0]
	v_mfma_scale_f32_16x16x128_f8f6f4 v[24:27], v[120:127], v[160:167], v[236:239], v230, v230 op_sel_hi:[0,0,0]
	v_mfma_scale_f32_16x16x128_f8f6f4 v[20:23], v[136:143], v[160:167], v[240:243], v230, v230 op_sel_hi:[0,0,0]
	v_mfma_scale_f32_16x16x128_f8f6f4 v[4:7], v[120:127], v[168:175], v[244:247], v230, v230 op_sel_hi:[0,0,0]
	v_mfma_scale_f32_16x16x128_f8f6f4 v[0:3], v[136:143], v[168:175], v[248:251], v230, v230 op_sel_hi:[0,0,0]
	s_setprio 2
	s_barrier
	s_add_i32 s29, s29, 2
	s_addk_i32 s31, 0x100
	s_cmp_gt_u32 s29, 13
	s_cbranch_scc0 .LBB0_1051
	s_and_b64 vcc, exec, s[62:63]
	s_cbranch_vccz .LBB0_1054
	s_barrier

.LBB0_1187:
	v_add_u32_e32 v140, 0x10000, v148
	v_add_u32_e32 v162, 0x14000, v148
	ds_read_b128 v[128:131], v140
	ds_read_b128 v[132:135], v140 offset:1024
	ds_read_b128 v[136:139], v140 offset:2048
	ds_read_b128 v[140:143], v140 offset:3072
	ds_read_b128 v[150:153], v162
	ds_read_b128 v[154:157], v162 offset:1024
	ds_read_b128 v[158:161], v162 offset:2048
	ds_read_b128 v[162:165], v162 offset:3072
	s_add_i32 s19, s13, 0xfffc0080
	s_cmp_eq_u32 s12, 12
	s_cselect_b32 s45, s23, s41
	s_cselect_b32 s44, s22, s40
	s_cselect_b32 s47, s29, s43
	s_cselect_b32 s46, s28, s42
	s_cselect_b32 s19, 0, s19
	s_cselect_b32 s49, s31, s53
	s_cselect_b32 s48, s30, s52
	s_cselect_b32 s51, s35, s5
	s_cselect_b32 s50, s34, s4
	s_mov_b32 m0, s83
	ds_read_b128 v[166:169], v149
	ds_read_b128 v[170:173], v149 offset:1024
	ds_read_b128 v[198:201], v149 offset:2048
	ds_read_b128 v[202:205], v149 offset:3072
	ds_read_b128 v[206:209], v149 offset:4096
	ds_read_b128 v[210:213], v149 offset:5120
	ds_read_b128 v[214:217], v149 offset:6144
	ds_read_b128 v[218:221], v149 offset:7168
	buffer_load_dwordx4 v146, s[40:43], s13 offen lds
	s_mov_b32 m0, s91
	s_nop 0
	buffer_load_dwordx4 v147, s[40:43], s13 offen lds
	s_waitcnt vmcnt(8)
	s_waitcnt lgkmcnt(0)
	s_barrier
	s_setprio 1
	s_waitcnt lgkmcnt(6)
	v_mfma_scale_f32_16x16x128_f8f6f4 v[124:127], v[128:135], v[166:173], v[124:127], v230, v230 op_sel_hi:[0,0,0]
	v_mfma_scale_f32_16x16x128_f8f6f4 v[120:123], v[136:143], v[166:173], v[120:123], v230, v230 op_sel_hi:[0,0,0]
	s_waitcnt lgkmcnt(4)
	v_mfma_scale_f32_16x16x128_f8f6f4 v[108:111], v[128:135], v[198:205], v[108:111], v230, v230 op_sel_hi:[0,0,0]
	v_mfma_scale_f32_16x16x128_f8f6f4 v[104:107], v[136:143], v[198:205], v[104:107], v230, v230 op_sel_hi:[0,0,0]
	s_waitcnt lgkmcnt(2)
	v_mfma_scale_f32_16x16x128_f8f6f4 v[178:181], v[128:135], v[206:213], v[92:95], v230, v230 op_sel_hi:[0,0,0]
	v_mfma_scale_f32_16x16x128_f8f6f4 v[182:185], v[136:143], v[206:213], v[88:91], v230, v230 op_sel_hi:[0,0,0]
	s_waitcnt lgkmcnt(0)
	v_mfma_scale_f32_16x16x128_f8f6f4 v[186:189], v[128:135], v[214:221], v[76:79], v230, v230 op_sel_hi:[0,0,0]
	v_mfma_scale_f32_16x16x128_f8f6f4 v[190:193], v[136:143], v[214:221], v[72:75], v230, v230 op_sel_hi:[0,0,0]
	s_setprio 2
	s_setprio 1
	v_mfma_scale_f32_16x16x128_f8f6f4 v[116:119], v[150:157], v[166:173], v[116:119], v230, v230 op_sel_hi:[0,0,0]
	v_mfma_scale_f32_16x16x128_f8f6f4 v[112:115], v[158:165], v[166:173], v[112:115], v230, v230 op_sel_hi:[0,0,0]
	v_mfma_scale_f32_16x16x128_f8f6f4 v[100:103], v[150:157], v[198:205], v[100:103], v230, v230 op_sel_hi:[0,0,0]
	v_mfma_scale_f32_16x16x128_f8f6f4 v[96:99], v[158:165], v[198:205], v[96:99], v230, v230 op_sel_hi:[0,0,0]
	v_mfma_scale_f32_16x16x128_f8f6f4 v[166:169], v[150:157], v[206:213], v[84:87], v230, v230 op_sel_hi:[0,0,0]
	v_mfma_scale_f32_16x16x128_f8f6f4 v[170:173], v[158:165], v[206:213], v[80:83], v230, v230 op_sel_hi:[0,0,0]
	v_mfma_scale_f32_16x16x128_f8f6f4 v[194:197], v[150:157], v[214:221], v[68:71], v230, v230 op_sel_hi:[0,0,0]
	v_mfma_scale_f32_16x16x128_f8f6f4 v[198:201], v[158:165], v[214:221], v[64:67], v230, v230 op_sel_hi:[0,0,0]
	s_setprio 2
	s_barrier
	s_mov_b32 m0, s66
	s_nop 3
	ds_read_b128 v[64:67], v149 offset:16384
	ds_read_b128 v[68:71], v149 offset:17408
	ds_read_b128 v[72:75], v149 offset:18432
	ds_read_b128 v[76:79], v149 offset:19456
	ds_read_b128 v[80:83], v149 offset:20480
	ds_read_b128 v[84:87], v149 offset:21504
	ds_read_b128 v[88:91], v149 offset:22528
	ds_read_b128 v[92:95], v149 offset:23552
	buffer_load_dwordx4 v144, s[48:51], s19 offen lds
	s_mov_b32 m0, s67
	s_add_i32 s21, s19, 0x40000
	buffer_load_dwordx4 v145, s[48:51], s19 offen lds
	s_mov_b32 m0, s68
	s_nop 0
	buffer_load_dwordx4 v144, s[48:51], s21 offen lds
	s_mov_b32 m0, s69
	s_nop 0
	buffer_load_dwordx4 v145, s[48:51], s21 offen lds
	s_mov_b32 m0, s63
	s_nop 0
	buffer_load_dwordx4 v146, s[44:47], s19 offen lds
	s_mov_b32 m0, s70
	s_nop 0
	buffer_load_dwordx4 v147, s[44:47], s19 offen lds
	s_waitcnt vmcnt(8)
	s_waitcnt lgkmcnt(0)
	s_barrier
	s_setprio 1
	s_waitcnt lgkmcnt(6)
	v_mfma_scale_f32_16x16x128_f8f6f4 v[60:63], v[128:135], v[64:71], v[60:63], v230, v230 op_sel_hi:[0,0,0]
	v_mfma_scale_f32_16x16x128_f8f6f4 v[0:3], v[136:143], v[64:71], v[0:3], v230, v230 op_sel_hi:[0,0,0]
	s_waitcnt lgkmcnt(4)
	v_mfma_scale_f32_16x16x128_f8f6f4 v[202:205], v[128:135], v[72:79], v[48:51], v230, v230 op_sel_hi:[0,0,0]
	v_mfma_scale_f32_16x16x128_f8f6f4 v[206:209], v[136:143], v[72:79], v[44:47], v230, v230 op_sel_hi:[0,0,0]
	s_waitcnt lgkmcnt(2)
	v_mfma_scale_f32_16x16x128_f8f6f4 v[210:213], v[128:135], v[80:87], v[32:35], v230, v230 op_sel_hi:[0,0,0]
	v_mfma_scale_f32_16x16x128_f8f6f4 v[214:217], v[136:143], v[80:87], v[28:31], v230, v230 op_sel_hi:[0,0,0]
	s_waitcnt lgkmcnt(0)
	v_mfma_scale_f32_16x16x128_f8f6f4 v[218:221], v[128:135], v[88:95], v[16:19], v230, v230 op_sel_hi:[0,0,0]
	v_mfma_scale_f32_16x16x128_f8f6f4 v[222:225], v[136:143], v[88:95], v[12:15], v230, v230 op_sel_hi:[0,0,0]
	s_setprio 2
	s_setprio 1
	v_mfma_scale_f32_16x16x128_f8f6f4 v[56:59], v[150:157], v[64:71], v[56:59], v230, v230 op_sel_hi:[0,0,0]
	v_mfma_scale_f32_16x16x128_f8f6f4 v[52:55], v[158:165], v[64:71], v[52:55], v230, v230 op_sel_hi:[0,0,0]
	v_mfma_scale_f32_16x16x128_f8f6f4 v[226:229], v[150:157], v[72:79], v[40:43], v230, v230 op_sel_hi:[0,0,0]
	v_mfma_scale_f32_16x16x128_f8f6f4 v[232:235], v[158:165], v[72:79], v[36:39], v230, v230 op_sel_hi:[0,0,0]
	v_mfma_scale_f32_16x16x128_f8f6f4 v[236:239], v[150:157], v[80:87], v[24:27], v230, v230 op_sel_hi:[0,0,0]
	v_mfma_scale_f32_16x16x128_f8f6f4 v[240:243], v[158:165], v[80:87], v[20:23], v230, v230 op_sel_hi:[0,0,0]
	v_mfma_scale_f32_16x16x128_f8f6f4 v[244:247], v[150:157], v[88:95], v[8:11], v230, v230 op_sel_hi:[0,0,0]
	v_mfma_scale_f32_16x16x128_f8f6f4 v[248:251], v[158:165], v[88:95], v[4:7], v230, v230 op_sel_hi:[0,0,0]
	s_setprio 2
	s_barrier
	v_add_u32_e32 v12, 0x18000, v148
	s_nop 3
	ds_read_b128 v[4:7], v12
	ds_read_b128 v[8:11], v12 offset:1024
	ds_read_b128 v[20:23], v12 offset:2048
	ds_read_b128 v[24:27], v12 offset:3072
	v_add_u32_e32 v12, 0x1c000, v148
	ds_read_b128 v[128:131], v12
	ds_read_b128 v[132:135], v12 offset:1024
	ds_read_b128 v[136:139], v12 offset:2048
	ds_read_b128 v[140:143], v12 offset:3072
	s_mov_b32 m0, s71
	ds_read_b128 v[12:15], v149 offset:32768
	ds_read_b128 v[16:19], v149 offset:33792
	ds_read_b128 v[28:31], v149 offset:34816
	ds_read_b128 v[32:35], v149 offset:35840
	ds_read_b128 v[36:39], v149 offset:36864
	ds_read_b128 v[40:43], v149 offset:37888
	ds_read_b128 v[44:47], v149 offset:38912
	ds_read_b128 v[48:51], v149 offset:39936
	buffer_load_dwordx4 v146, s[44:47], s21 offen lds
	s_mov_b32 m0, s72
	s_nop 0
	buffer_load_dwordx4 v147, s[44:47], s21 offen lds
	s_waitcnt vmcnt(8)
	s_waitcnt lgkmcnt(0)
	s_barrier
	s_setprio 1
	s_waitcnt lgkmcnt(6)
	v_mfma_scale_f32_16x16x128_f8f6f4 v[124:127], v[4:11], v[12:19], v[124:127], v230, v230 op_sel_hi:[0,0,0]
	v_mfma_scale_f32_16x16x128_f8f6f4 v[120:123], v[20:27], v[12:19], v[120:123], v230, v230 op_sel_hi:[0,0,0]
	s_waitcnt lgkmcnt(4)
	v_mfma_scale_f32_16x16x128_f8f6f4 v[108:111], v[4:11], v[28:35], v[108:111], v230, v230 op_sel_hi:[0,0,0]
	v_mfma_scale_f32_16x16x128_f8f6f4 v[104:107], v[20:27], v[28:35], v[104:107], v230, v230 op_sel_hi:[0,0,0]
	s_waitcnt lgkmcnt(2)
	v_mfma_scale_f32_16x16x128_f8f6f4 v[92:95], v[4:11], v[36:43], v[178:181], v230, v230 op_sel_hi:[0,0,0]
	v_mfma_scale_f32_16x16x128_f8f6f4 v[88:91], v[20:27], v[36:43], v[182:185], v230, v230 op_sel_hi:[0,0,0]
	s_waitcnt lgkmcnt(0)
	v_mfma_scale_f32_16x16x128_f8f6f4 v[76:79], v[4:11], v[44:51], v[186:189], v230, v230 op_sel_hi:[0,0,0]
	v_mfma_scale_f32_16x16x128_f8f6f4 v[72:75], v[20:27], v[44:51], v[190:193], v230, v230 op_sel_hi:[0,0,0]
	s_setprio 2
	s_setprio 1
	v_mfma_scale_f32_16x16x128_f8f6f4 v[116:119], v[128:135], v[12:19], v[116:119], v230, v230 op_sel_hi:[0,0,0]
	v_mfma_scale_f32_16x16x128_f8f6f4 v[112:115], v[136:143], v[12:19], v[112:115], v230, v230 op_sel_hi:[0,0,0]
	v_mfma_scale_f32_16x16x128_f8f6f4 v[100:103], v[128:135], v[28:35], v[100:103], v230, v230 op_sel_hi:[0,0,0]
	v_mfma_scale_f32_16x16x128_f8f6f4 v[96:99], v[136:143], v[28:35], v[96:99], v230, v230 op_sel_hi:[0,0,0]
	v_mfma_scale_f32_16x16x128_f8f6f4 v[84:87], v[128:135], v[36:43], v[166:169], v230, v230 op_sel_hi:[0,0,0]
	v_mfma_scale_f32_16x16x128_f8f6f4 v[80:83], v[136:143], v[36:43], v[170:173], v230, v230 op_sel_hi:[0,0,0]
	v_mfma_scale_f32_16x16x128_f8f6f4 v[68:71], v[128:135], v[44:51], v[194:197], v230, v230 op_sel_hi:[0,0,0]
	v_mfma_scale_f32_16x16x128_f8f6f4 v[64:67], v[136:143], v[44:51], v[198:201], v230, v230 op_sel_hi:[0,0,0]
	s_setprio 2
	s_barrier
	s_mov_b32 m0, s76
	s_or_b32 s21, s19, 0x80
	ds_read_b128 v[36:39], v149 offset:49152
	ds_read_b128 v[40:43], v149 offset:50176
	ds_read_b128 v[150:153], v149 offset:51200
	ds_read_b128 v[154:157], v149 offset:52224
	ds_read_b128 v[158:161], v149 offset:53248
	ds_read_b128 v[162:165], v149 offset:54272
	ds_read_b128 v[166:169], v149 offset:55296
	ds_read_b128 v[170:173], v149 offset:56320
	buffer_load_dwordx4 v144, s[48:51], s21 offen lds
	s_mov_b32 m0, s77
	s_add_i32 s19, s19, 0x40080
	buffer_load_dwordx4 v145, s[48:51], s21 offen lds
	s_mov_b32 m0, s80
	s_nop 0
	buffer_load_dwordx4 v144, s[48:51], s19 offen lds
	s_mov_b32 m0, s82
	s_nop 0
	buffer_load_dwordx4 v145, s[48:51], s19 offen lds
	s_mov_b32 m0, s78
	s_nop 0
	buffer_load_dwordx4 v146, s[44:47], s21 offen lds
	s_mov_b32 m0, s79
	s_nop 0
	buffer_load_dwordx4 v147, s[44:47], s21 offen lds
	s_waitcnt vmcnt(8)
	s_waitcnt lgkmcnt(0)
	s_barrier
	s_setprio 1
	s_waitcnt lgkmcnt(6)
	v_mfma_scale_f32_16x16x128_f8f6f4 v[60:63], v[4:11], v[36:43], v[60:63], v230, v230 op_sel_hi:[0,0,0]
	v_mfma_scale_f32_16x16x128_f8f6f4 v[0:3], v[20:27], v[36:43], v[0:3], v230, v230 op_sel_hi:[0,0,0]
	s_waitcnt lgkmcnt(4)
	v_mfma_scale_f32_16x16x128_f8f6f4 v[48:51], v[4:11], v[150:157], v[202:205], v230, v230 op_sel_hi:[0,0,0]
	v_mfma_scale_f32_16x16x128_f8f6f4 v[44:47], v[20:27], v[150:157], v[206:209], v230, v230 op_sel_hi:[0,0,0]
	s_waitcnt lgkmcnt(2)
	v_mfma_scale_f32_16x16x128_f8f6f4 v[32:35], v[4:11], v[158:165], v[210:213], v230, v230 op_sel_hi:[0,0,0]
	v_mfma_scale_f32_16x16x128_f8f6f4 v[28:31], v[20:27], v[158:165], v[214:217], v230, v230 op_sel_hi:[0,0,0]
	s_waitcnt lgkmcnt(0)
	v_mfma_scale_f32_16x16x128_f8f6f4 v[16:19], v[4:11], v[166:173], v[218:221], v230, v230 op_sel_hi:[0,0,0]
	v_mfma_scale_f32_16x16x128_f8f6f4 v[12:15], v[20:27], v[166:173], v[222:225], v230, v230 op_sel_hi:[0,0,0]
	s_setprio 2
	s_setprio 1
	v_mfma_scale_f32_16x16x128_f8f6f4 v[56:59], v[128:135], v[36:43], v[56:59], v230, v230 op_sel_hi:[0,0,0]
	v_mfma_scale_f32_16x16x128_f8f6f4 v[52:55], v[136:143], v[36:43], v[52:55], v230, v230 op_sel_hi:[0,0,0]
	v_mfma_scale_f32_16x16x128_f8f6f4 v[40:43], v[128:135], v[150:157], v[226:229], v230, v230 op_sel_hi:[0,0,0]
	v_mfma_scale_f32_16x16x128_f8f6f4 v[36:39], v[136:143], v[150:157], v[232:235], v230, v230 op_sel_hi:[0,0,0]
	v_mfma_scale_f32_16x16x128_f8f6f4 v[24:27], v[128:135], v[158:165], v[236:239], v230, v230 op_sel_hi:[0,0,0]
	v_mfma_scale_f32_16x16x128_f8f6f4 v[20:23], v[136:143], v[158:165], v[240:243], v230, v230 op_sel_hi:[0,0,0]
	v_mfma_scale_f32_16x16x128_f8f6f4 v[8:11], v[128:135], v[166:173], v[244:247], v230, v230 op_sel_hi:[0,0,0]
	v_mfma_scale_f32_16x16x128_f8f6f4 v[4:7], v[136:143], v[166:173], v[248:251], v230, v230 op_sel_hi:[0,0,0]
	s_setprio 2
	s_barrier
	s_add_i32 s12, s12, 2
	s_addk_i32 s13, 0x100
	s_cmp_gt_u32 s12, 13
	s_cbranch_scc0 .LBB0_1187
	s_and_b64 vcc, exec, s[8:9]
	s_cbranch_vccz .LBB0_1190
	s_barrier

.LBB0_1217:
	v_add_u32_e32 v132, 0x10000, v150
	v_add_u32_e32 v144, 0x14000, v150
	ds_read_b128 v[112:115], v132
	ds_read_b128 v[116:119], v132 offset:1024
	ds_read_b128 v[128:131], v132 offset:2048
	ds_read_b128 v[132:135], v132 offset:3072
	ds_read_b128 v[152:155], v144
	ds_read_b128 v[156:159], v144 offset:1024
	ds_read_b128 v[160:163], v144 offset:2048
	ds_read_b128 v[164:167], v144 offset:3072
	s_add_i32 s19, s13, 0xfff80080
	s_cmp_eq_u32 s12, 28
	s_cselect_b32 s45, s21, s41
	s_cselect_b32 s44, s20, s40
	s_cselect_b32 s47, s23, s43
	s_cselect_b32 s46, s22, s42
	s_cselect_b32 s19, 0, s19
	s_cselect_b32 s49, s29, s53
	s_cselect_b32 s48, s28, s52
	s_cselect_b32 s51, s31, s5
	s_cselect_b32 s50, s30, s4
	s_mov_b32 m0, s83
	ds_read_b128 v[168:171], v151
	ds_read_b128 v[172:175], v151 offset:1024
	ds_read_b128 v[178:181], v151 offset:2048
	ds_read_b128 v[182:185], v151 offset:3072
	ds_read_b128 v[186:189], v151 offset:4096
	ds_read_b128 v[190:193], v151 offset:5120
	ds_read_b128 v[194:197], v151 offset:6144
	ds_read_b128 v[198:201], v151 offset:7168
	buffer_load_dwordx4 v148, s[40:43], s13 offen lds
	s_mov_b32 m0, s90
	s_nop 0
	buffer_load_dwordx4 v149, s[40:43], s13 offen lds
	s_waitcnt vmcnt(8)
	s_waitcnt lgkmcnt(0)
	s_barrier
	s_setprio 1
	s_waitcnt lgkmcnt(7)
	v_mfma_f32_16x16x32_bf16 v[140:143], v[112:115], v[168:171], v[140:143]
	v_mfma_f32_16x16x32_bf16 v[136:139], v[128:131], v[168:171], v[136:139]
	s_waitcnt lgkmcnt(5)
	v_mfma_f32_16x16x32_bf16 v[108:111], v[112:115], v[178:181], v[108:111]
	v_mfma_f32_16x16x32_bf16 v[104:107], v[128:131], v[178:181], v[104:107]
	s_waitcnt lgkmcnt(3)
	v_mfma_f32_16x16x32_bf16 v[92:95], v[112:115], v[186:189], v[92:95]
	v_mfma_f32_16x16x32_bf16 v[88:91], v[128:131], v[186:189], v[88:91]
	s_waitcnt lgkmcnt(1)
	v_mfma_f32_16x16x32_bf16 v[76:79], v[112:115], v[194:197], v[76:79]
	v_mfma_f32_16x16x32_bf16 v[72:75], v[128:131], v[194:197], v[72:75]
	v_mfma_f32_16x16x32_bf16 v[140:143], v[116:119], v[172:175], v[140:143]
	v_mfma_f32_16x16x32_bf16 v[136:139], v[132:135], v[172:175], v[136:139]
	v_mfma_f32_16x16x32_bf16 v[108:111], v[116:119], v[182:185], v[108:111]
	v_mfma_f32_16x16x32_bf16 v[104:107], v[132:135], v[182:185], v[104:107]
	v_mfma_f32_16x16x32_bf16 v[92:95], v[116:119], v[190:193], v[92:95]
	v_mfma_f32_16x16x32_bf16 v[88:91], v[132:135], v[190:193], v[88:91]
	s_waitcnt lgkmcnt(0)
	v_mfma_f32_16x16x32_bf16 v[76:79], v[116:119], v[198:201], v[76:79]
	v_mfma_f32_16x16x32_bf16 v[72:75], v[132:135], v[198:201], v[72:75]
	s_setprio 2
	s_setprio 1
	v_mfma_f32_16x16x32_bf16 v[124:127], v[152:155], v[168:171], v[124:127]
	v_mfma_f32_16x16x32_bf16 v[120:123], v[160:163], v[168:171], v[120:123]
	v_mfma_f32_16x16x32_bf16 v[100:103], v[152:155], v[178:181], v[100:103]
	v_mfma_f32_16x16x32_bf16 v[96:99], v[160:163], v[178:181], v[96:99]
	v_mfma_f32_16x16x32_bf16 v[84:87], v[152:155], v[186:189], v[84:87]
	v_mfma_f32_16x16x32_bf16 v[80:83], v[160:163], v[186:189], v[80:83]
	v_mfma_f32_16x16x32_bf16 v[68:71], v[152:155], v[194:197], v[68:71]
	v_mfma_f32_16x16x32_bf16 v[64:67], v[160:163], v[194:197], v[64:67]
	v_mfma_f32_16x16x32_bf16 v[124:127], v[156:159], v[172:175], v[124:127]
	v_mfma_f32_16x16x32_bf16 v[120:123], v[164:167], v[172:175], v[120:123]
	v_mfma_f32_16x16x32_bf16 v[100:103], v[156:159], v[182:185], v[100:103]
	v_mfma_f32_16x16x32_bf16 v[96:99], v[164:167], v[182:185], v[96:99]
	v_mfma_f32_16x16x32_bf16 v[84:87], v[156:159], v[190:193], v[84:87]
	v_mfma_f32_16x16x32_bf16 v[80:83], v[164:167], v[190:193], v[80:83]
	v_mfma_f32_16x16x32_bf16 v[68:71], v[156:159], v[198:201], v[68:71]
	v_mfma_f32_16x16x32_bf16 v[64:67], v[164:167], v[198:201], v[64:67]
	s_setprio 2
	s_barrier
	s_mov_b32 m0, s65
	ds_read_b128 v[168:171], v151 offset:16384
	ds_read_b128 v[172:175], v151 offset:17408
	ds_read_b128 v[178:181], v151 offset:18432
	ds_read_b128 v[182:185], v151 offset:19456
	ds_read_b128 v[186:189], v151 offset:20480
	ds_read_b128 v[190:193], v151 offset:21504
	ds_read_b128 v[194:197], v151 offset:22528
	ds_read_b128 v[198:201], v151 offset:23552
	buffer_load_dwordx4 v146, s[48:51], s19 offen lds
	s_mov_b32 m0, s66
	s_add_i32 s35, s19, 0x1000
	buffer_load_dwordx4 v147, s[48:51], s19 offen lds
	s_mov_b32 m0, s67
	s_nop 0
	buffer_load_dwordx4 v146, s[48:51], s35 offen lds
	s_mov_b32 m0, s68
	s_nop 0
	buffer_load_dwordx4 v147, s[48:51], s35 offen lds
	s_mov_b32 m0, s64
	s_nop 0
	buffer_load_dwordx4 v148, s[44:47], s19 offen lds
	s_mov_b32 m0, s69
	s_nop 0
	buffer_load_dwordx4 v149, s[44:47], s19 offen lds
	s_waitcnt vmcnt(8)
	s_waitcnt lgkmcnt(0)
	s_barrier
	s_setprio 1
	s_waitcnt lgkmcnt(7)
	v_mfma_f32_16x16x32_bf16 v[60:63], v[112:115], v[168:171], v[60:63]
	v_mfma_f32_16x16x32_bf16 v[0:3], v[128:131], v[168:171], v[0:3]
	s_waitcnt lgkmcnt(5)
	v_mfma_f32_16x16x32_bf16 v[48:51], v[112:115], v[178:181], v[48:51]
	v_mfma_f32_16x16x32_bf16 v[44:47], v[128:131], v[178:181], v[44:47]
	s_waitcnt lgkmcnt(3)
	v_mfma_f32_16x16x32_bf16 v[32:35], v[112:115], v[186:189], v[32:35]
	v_mfma_f32_16x16x32_bf16 v[28:31], v[128:131], v[186:189], v[28:31]
	s_waitcnt lgkmcnt(1)
	v_mfma_f32_16x16x32_bf16 v[16:19], v[112:115], v[194:197], v[16:19]
	v_mfma_f32_16x16x32_bf16 v[12:15], v[128:131], v[194:197], v[12:15]
	v_mfma_f32_16x16x32_bf16 v[60:63], v[116:119], v[172:175], v[60:63]
	v_mfma_f32_16x16x32_bf16 v[0:3], v[132:135], v[172:175], v[0:3]
	v_mfma_f32_16x16x32_bf16 v[48:51], v[116:119], v[182:185], v[48:51]
	v_mfma_f32_16x16x32_bf16 v[44:47], v[132:135], v[182:185], v[44:47]
	v_mfma_f32_16x16x32_bf16 v[32:35], v[116:119], v[190:193], v[32:35]
	v_mfma_f32_16x16x32_bf16 v[28:31], v[132:135], v[190:193], v[28:31]
	s_waitcnt lgkmcnt(0)
	v_mfma_f32_16x16x32_bf16 v[16:19], v[116:119], v[198:201], v[16:19]
	v_mfma_f32_16x16x32_bf16 v[12:15], v[132:135], v[198:201], v[12:15]
	s_setprio 2
	s_setprio 1
	v_mfma_f32_16x16x32_bf16 v[56:59], v[152:155], v[168:171], v[56:59]
	v_mfma_f32_16x16x32_bf16 v[52:55], v[160:163], v[168:171], v[52:55]
	v_mfma_f32_16x16x32_bf16 v[40:43], v[152:155], v[178:181], v[40:43]
	v_mfma_f32_16x16x32_bf16 v[36:39], v[160:163], v[178:181], v[36:39]
	v_mfma_f32_16x16x32_bf16 v[24:27], v[152:155], v[186:189], v[24:27]
	v_mfma_f32_16x16x32_bf16 v[20:23], v[160:163], v[186:189], v[20:23]
	v_mfma_f32_16x16x32_bf16 v[8:11], v[152:155], v[194:197], v[8:11]
	v_mfma_f32_16x16x32_bf16 v[4:7], v[160:163], v[194:197], v[4:7]
	v_mfma_f32_16x16x32_bf16 v[56:59], v[156:159], v[172:175], v[56:59]
	v_mfma_f32_16x16x32_bf16 v[52:55], v[164:167], v[172:175], v[52:55]
	v_mfma_f32_16x16x32_bf16 v[40:43], v[156:159], v[182:185], v[40:43]
	v_mfma_f32_16x16x32_bf16 v[36:39], v[164:167], v[182:185], v[36:39]
	v_mfma_f32_16x16x32_bf16 v[24:27], v[156:159], v[190:193], v[24:27]
	v_mfma_f32_16x16x32_bf16 v[20:23], v[164:167], v[190:193], v[20:23]
	v_mfma_f32_16x16x32_bf16 v[8:11], v[156:159], v[198:201], v[8:11]
	v_mfma_f32_16x16x32_bf16 v[4:7], v[164:167], v[198:201], v[4:7]
	s_setprio 2
	s_barrier
	v_add_u32_e32 v132, 0x18000, v150
	v_add_u32_e32 v144, 0x1c000, v150
	ds_read_b128 v[112:115], v132
	ds_read_b128 v[116:119], v132 offset:1024
	ds_read_b128 v[128:131], v132 offset:2048
	ds_read_b128 v[132:135], v132 offset:3072
	ds_read_b128 v[152:155], v144
	ds_read_b128 v[156:159], v144 offset:1024
	ds_read_b128 v[160:163], v144 offset:2048
	ds_read_b128 v[164:167], v144 offset:3072
	s_add_i32 s35, s19, 0x80000
	s_mov_b32 m0, s70
	ds_read_b128 v[168:171], v151 offset:32768
	ds_read_b128 v[172:175], v151 offset:33792
	ds_read_b128 v[178:181], v151 offset:34816
	ds_read_b128 v[182:185], v151 offset:35840
	ds_read_b128 v[186:189], v151 offset:36864
	ds_read_b128 v[190:193], v151 offset:37888
	ds_read_b128 v[194:197], v151 offset:38912
	ds_read_b128 v[198:201], v151 offset:39936
	buffer_load_dwordx4 v148, s[44:47], s35 offen lds
	s_mov_b32 m0, s71
	s_nop 0
	buffer_load_dwordx4 v149, s[44:47], s35 offen lds
	s_waitcnt vmcnt(8)
	s_waitcnt lgkmcnt(0)
	s_barrier
	s_setprio 1
	s_waitcnt lgkmcnt(7)
	v_mfma_f32_16x16x32_bf16 v[140:143], v[112:115], v[168:171], v[140:143]
	v_mfma_f32_16x16x32_bf16 v[136:139], v[128:131], v[168:171], v[136:139]
	s_waitcnt lgkmcnt(5)
	v_mfma_f32_16x16x32_bf16 v[108:111], v[112:115], v[178:181], v[108:111]
	v_mfma_f32_16x16x32_bf16 v[104:107], v[128:131], v[178:181], v[104:107]
	s_waitcnt lgkmcnt(3)
	v_mfma_f32_16x16x32_bf16 v[92:95], v[112:115], v[186:189], v[92:95]
	v_mfma_f32_16x16x32_bf16 v[88:91], v[128:131], v[186:189], v[88:91]
	s_waitcnt lgkmcnt(1)
	v_mfma_f32_16x16x32_bf16 v[76:79], v[112:115], v[194:197], v[76:79]
	v_mfma_f32_16x16x32_bf16 v[72:75], v[128:131], v[194:197], v[72:75]
	v_mfma_f32_16x16x32_bf16 v[140:143], v[116:119], v[172:175], v[140:143]
	v_mfma_f32_16x16x32_bf16 v[136:139], v[132:135], v[172:175], v[136:139]
	v_mfma_f32_16x16x32_bf16 v[108:111], v[116:119], v[182:185], v[108:111]
	v_mfma_f32_16x16x32_bf16 v[104:107], v[132:135], v[182:185], v[104:107]
	v_mfma_f32_16x16x32_bf16 v[92:95], v[116:119], v[190:193], v[92:95]
	v_mfma_f32_16x16x32_bf16 v[88:91], v[132:135], v[190:193], v[88:91]
	s_waitcnt lgkmcnt(0)
	v_mfma_f32_16x16x32_bf16 v[76:79], v[116:119], v[198:201], v[76:79]
	v_mfma_f32_16x16x32_bf16 v[72:75], v[132:135], v[198:201], v[72:75]
	s_setprio 2
	s_setprio 1
	v_mfma_f32_16x16x32_bf16 v[124:127], v[152:155], v[168:171], v[124:127]
	v_mfma_f32_16x16x32_bf16 v[120:123], v[160:163], v[168:171], v[120:123]
	v_mfma_f32_16x16x32_bf16 v[100:103], v[152:155], v[178:181], v[100:103]
	v_mfma_f32_16x16x32_bf16 v[96:99], v[160:163], v[178:181], v[96:99]
	v_mfma_f32_16x16x32_bf16 v[84:87], v[152:155], v[186:189], v[84:87]
	v_mfma_f32_16x16x32_bf16 v[80:83], v[160:163], v[186:189], v[80:83]
	v_mfma_f32_16x16x32_bf16 v[68:71], v[152:155], v[194:197], v[68:71]
	v_mfma_f32_16x16x32_bf16 v[64:67], v[160:163], v[194:197], v[64:67]
	v_mfma_f32_16x16x32_bf16 v[124:127], v[156:159], v[172:175], v[124:127]
	v_mfma_f32_16x16x32_bf16 v[120:123], v[164:167], v[172:175], v[120:123]
	v_mfma_f32_16x16x32_bf16 v[100:103], v[156:159], v[182:185], v[100:103]
	v_mfma_f32_16x16x32_bf16 v[96:99], v[164:167], v[182:185], v[96:99]
	v_mfma_f32_16x16x32_bf16 v[84:87], v[156:159], v[190:193], v[84:87]
	v_mfma_f32_16x16x32_bf16 v[80:83], v[164:167], v[190:193], v[80:83]
	v_mfma_f32_16x16x32_bf16 v[68:71], v[156:159], v[198:201], v[68:71]
	v_mfma_f32_16x16x32_bf16 v[64:67], v[164:167], v[198:201], v[64:67]
	s_setprio 2
	s_barrier
	s_mov_b32 m0, s76
	s_or_b32 s35, s19, 0x80
	ds_read_b128 v[168:171], v151 offset:49152
	ds_read_b128 v[172:175], v151 offset:50176
	ds_read_b128 v[178:181], v151 offset:51200
	ds_read_b128 v[182:185], v151 offset:52224
	ds_read_b128 v[186:189], v151 offset:53248
	ds_read_b128 v[190:193], v151 offset:54272
	ds_read_b128 v[194:197], v151 offset:55296
	ds_read_b128 v[198:201], v151 offset:56320
	buffer_load_dwordx4 v146, s[48:51], s35 offen lds
	s_mov_b32 m0, s77
	s_addk_i32 s19, 0x1080
	buffer_load_dwordx4 v147, s[48:51], s35 offen lds
	s_mov_b32 m0, s80
	s_nop 0
	buffer_load_dwordx4 v146, s[48:51], s19 offen lds
	s_mov_b32 m0, s82
	s_nop 0
	buffer_load_dwordx4 v147, s[48:51], s19 offen lds
	s_mov_b32 m0, s78
	s_nop 0
	buffer_load_dwordx4 v148, s[44:47], s35 offen lds
	s_mov_b32 m0, s79
	s_nop 0
	buffer_load_dwordx4 v149, s[44:47], s35 offen lds
	s_waitcnt vmcnt(8)
	s_waitcnt lgkmcnt(0)
	s_barrier
	s_setprio 1
	s_waitcnt lgkmcnt(7)
	v_mfma_f32_16x16x32_bf16 v[60:63], v[112:115], v[168:171], v[60:63]
	v_mfma_f32_16x16x32_bf16 v[0:3], v[128:131], v[168:171], v[0:3]
	s_waitcnt lgkmcnt(5)
	v_mfma_f32_16x16x32_bf16 v[48:51], v[112:115], v[178:181], v[48:51]
	v_mfma_f32_16x16x32_bf16 v[44:47], v[128:131], v[178:181], v[44:47]
	s_waitcnt lgkmcnt(3)
	v_mfma_f32_16x16x32_bf16 v[32:35], v[112:115], v[186:189], v[32:35]
	v_mfma_f32_16x16x32_bf16 v[28:31], v[128:131], v[186:189], v[28:31]
	s_waitcnt lgkmcnt(1)
	v_mfma_f32_16x16x32_bf16 v[16:19], v[112:115], v[194:197], v[16:19]
	v_mfma_f32_16x16x32_bf16 v[12:15], v[128:131], v[194:197], v[12:15]
	v_mfma_f32_16x16x32_bf16 v[60:63], v[116:119], v[172:175], v[60:63]
	v_mfma_f32_16x16x32_bf16 v[0:3], v[132:135], v[172:175], v[0:3]
	v_mfma_f32_16x16x32_bf16 v[48:51], v[116:119], v[182:185], v[48:51]
	v_mfma_f32_16x16x32_bf16 v[44:47], v[132:135], v[182:185], v[44:47]
	v_mfma_f32_16x16x32_bf16 v[32:35], v[116:119], v[190:193], v[32:35]
	v_mfma_f32_16x16x32_bf16 v[28:31], v[132:135], v[190:193], v[28:31]
	s_waitcnt lgkmcnt(0)
	v_mfma_f32_16x16x32_bf16 v[16:19], v[116:119], v[198:201], v[16:19]
	v_mfma_f32_16x16x32_bf16 v[12:15], v[132:135], v[198:201], v[12:15]
	s_setprio 2
	s_setprio 1
	v_mfma_f32_16x16x32_bf16 v[56:59], v[152:155], v[168:171], v[56:59]
	v_mfma_f32_16x16x32_bf16 v[52:55], v[160:163], v[168:171], v[52:55]
	v_mfma_f32_16x16x32_bf16 v[40:43], v[152:155], v[178:181], v[40:43]
	v_mfma_f32_16x16x32_bf16 v[36:39], v[160:163], v[178:181], v[36:39]
	v_mfma_f32_16x16x32_bf16 v[24:27], v[152:155], v[186:189], v[24:27]
	v_mfma_f32_16x16x32_bf16 v[20:23], v[160:163], v[186:189], v[20:23]
	v_mfma_f32_16x16x32_bf16 v[8:11], v[152:155], v[194:197], v[8:11]
	v_mfma_f32_16x16x32_bf16 v[4:7], v[160:163], v[194:197], v[4:7]
	v_mfma_f32_16x16x32_bf16 v[56:59], v[156:159], v[172:175], v[56:59]
	v_mfma_f32_16x16x32_bf16 v[52:55], v[164:167], v[172:175], v[52:55]
	v_mfma_f32_16x16x32_bf16 v[40:43], v[156:159], v[182:185], v[40:43]
	v_mfma_f32_16x16x32_bf16 v[36:39], v[164:167], v[182:185], v[36:39]
	v_mfma_f32_16x16x32_bf16 v[24:27], v[156:159], v[190:193], v[24:27]
	v_mfma_f32_16x16x32_bf16 v[20:23], v[164:167], v[190:193], v[20:23]
	v_mfma_f32_16x16x32_bf16 v[8:11], v[156:159], v[198:201], v[8:11]
	v_mfma_f32_16x16x32_bf16 v[4:7], v[164:167], v[198:201], v[4:7]
	s_setprio 2
	s_barrier
	s_add_i32 s12, s12, 2
	s_addk_i32 s13, 0x100
	s_cmp_gt_u32 s12, 29
	s_cbranch_scc0 .LBB0_1217
	s_and_b64 vcc, exec, s[8:9]
	s_cbranch_vccz .LBB0_1220
	s_barrier

.LBB0_1396:
	v_add_u32_e32 v140, 0x10000, v164
	v_add_u32_e32 v156, 0x14000, v164
	ds_read_b128 v[128:131], v140
	ds_read_b128 v[132:135], v140 offset:1024
	ds_read_b128 v[136:139], v140 offset:2048
	ds_read_b128 v[140:143], v140 offset:3072
	ds_read_b128 v[144:147], v156
	ds_read_b128 v[148:151], v156 offset:1024
	ds_read_b128 v[152:155], v156 offset:2048
	ds_read_b128 v[156:159], v156 offset:3072
	s_add_i32 s2, s83, 0xfff60080
	s_cmp_eq_u32 s88, 38
	s_cselect_b32 s3, 0, s2
	s_cselect_b32 s45, s39, s41
	s_cselect_b32 s44, s38, s40
	s_cselect_b32 s47, s71, s43
	s_cselect_b32 s46, s70, s42
	s_cselect_b32 s49, s73, s53
	s_cselect_b32 s48, s72, s52
	s_cselect_b32 s51, s77, s1
	s_cselect_b32 s50, s76, s0
	s_or_b32 s2, s3, 0x80
	s_mov_b32 m0, s75
	ds_read_b128 v[166:169], v165
	ds_read_b128 v[170:173], v165 offset:1024
	ds_read_b128 v[178:181], v165 offset:2048
	ds_read_b128 v[182:185], v165 offset:3072
	ds_read_b128 v[186:189], v165 offset:4096
	ds_read_b128 v[190:193], v165 offset:5120
	ds_read_b128 v[194:197], v165 offset:6144
	ds_read_b128 v[198:201], v165 offset:7168
	buffer_load_dwordx4 v162, s[40:43], s83 offen lds
	s_mov_b32 m0, s78
	s_nop 0
	buffer_load_dwordx4 v163, s[40:43], s83 offen lds
	s_waitcnt vmcnt(8)
	s_waitcnt lgkmcnt(0)
	s_barrier
	s_setprio 1
	s_waitcnt lgkmcnt(7)
	v_mfma_f32_16x16x32_bf16 v[124:127], v[128:131], v[166:169], v[124:127]
	v_mfma_f32_16x16x32_bf16 v[120:123], v[136:139], v[166:169], v[120:123]
	s_waitcnt lgkmcnt(5)
	v_mfma_f32_16x16x32_bf16 v[108:111], v[128:131], v[178:181], v[108:111]
	v_mfma_f32_16x16x32_bf16 v[104:107], v[136:139], v[178:181], v[104:107]
	s_waitcnt lgkmcnt(3)
	v_mfma_f32_16x16x32_bf16 v[92:95], v[128:131], v[186:189], v[92:95]
	v_mfma_f32_16x16x32_bf16 v[88:91], v[136:139], v[186:189], v[88:91]
	s_waitcnt lgkmcnt(1)
	v_mfma_f32_16x16x32_bf16 v[76:79], v[128:131], v[194:197], v[76:79]
	v_mfma_f32_16x16x32_bf16 v[72:75], v[136:139], v[194:197], v[72:75]
	v_mfma_f32_16x16x32_bf16 v[124:127], v[132:135], v[170:173], v[124:127]
	v_mfma_f32_16x16x32_bf16 v[120:123], v[140:143], v[170:173], v[120:123]
	v_mfma_f32_16x16x32_bf16 v[108:111], v[132:135], v[182:185], v[108:111]
	v_mfma_f32_16x16x32_bf16 v[104:107], v[140:143], v[182:185], v[104:107]
	v_mfma_f32_16x16x32_bf16 v[92:95], v[132:135], v[190:193], v[92:95]
	v_mfma_f32_16x16x32_bf16 v[88:91], v[140:143], v[190:193], v[88:91]
	s_waitcnt lgkmcnt(0)
	v_mfma_f32_16x16x32_bf16 v[76:79], v[132:135], v[198:201], v[76:79]
	v_mfma_f32_16x16x32_bf16 v[72:75], v[140:143], v[198:201], v[72:75]
	s_setprio 2
	s_setprio 1
	v_mfma_f32_16x16x32_bf16 v[116:119], v[144:147], v[166:169], v[116:119]
	v_mfma_f32_16x16x32_bf16 v[112:115], v[152:155], v[166:169], v[112:115]
	v_mfma_f32_16x16x32_bf16 v[100:103], v[144:147], v[178:181], v[100:103]
	v_mfma_f32_16x16x32_bf16 v[96:99], v[152:155], v[178:181], v[96:99]
	v_mfma_f32_16x16x32_bf16 v[84:87], v[144:147], v[186:189], v[84:87]
	v_mfma_f32_16x16x32_bf16 v[80:83], v[152:155], v[186:189], v[80:83]
	v_mfma_f32_16x16x32_bf16 v[68:71], v[144:147], v[194:197], v[68:71]
	v_mfma_f32_16x16x32_bf16 v[64:67], v[152:155], v[194:197], v[64:67]
	v_mfma_f32_16x16x32_bf16 v[116:119], v[148:151], v[170:173], v[116:119]
	v_mfma_f32_16x16x32_bf16 v[112:115], v[156:159], v[170:173], v[112:115]
	v_mfma_f32_16x16x32_bf16 v[100:103], v[148:151], v[182:185], v[100:103]
	v_mfma_f32_16x16x32_bf16 v[96:99], v[156:159], v[182:185], v[96:99]
	v_mfma_f32_16x16x32_bf16 v[84:87], v[148:151], v[190:193], v[84:87]
	v_mfma_f32_16x16x32_bf16 v[80:83], v[156:159], v[190:193], v[80:83]
	v_mfma_f32_16x16x32_bf16 v[68:71], v[148:151], v[198:201], v[68:71]
	v_mfma_f32_16x16x32_bf16 v[64:67], v[156:159], v[198:201], v[64:67]
	s_setprio 2
	s_barrier
	s_mov_b32 m0, s20
	ds_read_b128 v[166:169], v165 offset:16384
	ds_read_b128 v[170:173], v165 offset:17408
	ds_read_b128 v[178:181], v165 offset:18432
	ds_read_b128 v[182:185], v165 offset:19456
	ds_read_b128 v[186:189], v165 offset:20480
	ds_read_b128 v[190:193], v165 offset:21504
	ds_read_b128 v[194:197], v165 offset:22528
	ds_read_b128 v[198:201], v165 offset:23552
	buffer_load_dwordx4 v160, s[48:51], s3 offen lds
	s_mov_b32 m0, s21
	s_add_i32 s80, s3, 0xa0000
	buffer_load_dwordx4 v161, s[48:51], s3 offen lds
	s_mov_b32 m0, s22
	s_nop 0
	buffer_load_dwordx4 v160, s[48:51], s80 offen lds
	s_mov_b32 m0, s23
	s_nop 0
	buffer_load_dwordx4 v161, s[48:51], s80 offen lds
	s_mov_b32 m0, s13
	s_nop 0
	buffer_load_dwordx4 v162, s[44:47], s3 offen lds
	s_mov_b32 m0, s28
	s_nop 0
	buffer_load_dwordx4 v163, s[44:47], s3 offen lds
	s_waitcnt vmcnt(8)
	s_waitcnt lgkmcnt(0)
	s_barrier
	s_setprio 1
	s_waitcnt lgkmcnt(7)
	v_mfma_f32_16x16x32_bf16 v[60:63], v[128:131], v[166:169], v[60:63]
	v_mfma_f32_16x16x32_bf16 v[0:3], v[136:139], v[166:169], v[0:3]
	s_waitcnt lgkmcnt(5)
	v_mfma_f32_16x16x32_bf16 v[48:51], v[128:131], v[178:181], v[48:51]
	v_mfma_f32_16x16x32_bf16 v[44:47], v[136:139], v[178:181], v[44:47]
	s_waitcnt lgkmcnt(3)
	v_mfma_f32_16x16x32_bf16 v[32:35], v[128:131], v[186:189], v[32:35]
	v_mfma_f32_16x16x32_bf16 v[28:31], v[136:139], v[186:189], v[28:31]
	s_waitcnt lgkmcnt(1)
	v_mfma_f32_16x16x32_bf16 v[16:19], v[128:131], v[194:197], v[16:19]
	v_mfma_f32_16x16x32_bf16 v[12:15], v[136:139], v[194:197], v[12:15]
	v_mfma_f32_16x16x32_bf16 v[60:63], v[132:135], v[170:173], v[60:63]
	v_mfma_f32_16x16x32_bf16 v[0:3], v[140:143], v[170:173], v[0:3]
	v_mfma_f32_16x16x32_bf16 v[48:51], v[132:135], v[182:185], v[48:51]
	v_mfma_f32_16x16x32_bf16 v[44:47], v[140:143], v[182:185], v[44:47]
	v_mfma_f32_16x16x32_bf16 v[32:35], v[132:135], v[190:193], v[32:35]
	v_mfma_f32_16x16x32_bf16 v[28:31], v[140:143], v[190:193], v[28:31]
	s_waitcnt lgkmcnt(0)
	v_mfma_f32_16x16x32_bf16 v[16:19], v[132:135], v[198:201], v[16:19]
	v_mfma_f32_16x16x32_bf16 v[12:15], v[140:143], v[198:201], v[12:15]
	s_setprio 2
	s_setprio 1
	v_mfma_f32_16x16x32_bf16 v[56:59], v[144:147], v[166:169], v[56:59]
	v_mfma_f32_16x16x32_bf16 v[52:55], v[152:155], v[166:169], v[52:55]
	v_mfma_f32_16x16x32_bf16 v[40:43], v[144:147], v[178:181], v[40:43]
	v_mfma_f32_16x16x32_bf16 v[36:39], v[152:155], v[178:181], v[36:39]
	v_mfma_f32_16x16x32_bf16 v[24:27], v[144:147], v[186:189], v[24:27]
	v_mfma_f32_16x16x32_bf16 v[20:23], v[152:155], v[186:189], v[20:23]
	v_mfma_f32_16x16x32_bf16 v[8:11], v[144:147], v[194:197], v[8:11]
	v_mfma_f32_16x16x32_bf16 v[4:7], v[152:155], v[194:197], v[4:7]
	v_mfma_f32_16x16x32_bf16 v[56:59], v[148:151], v[170:173], v[56:59]
	v_mfma_f32_16x16x32_bf16 v[52:55], v[156:159], v[170:173], v[52:55]
	v_mfma_f32_16x16x32_bf16 v[40:43], v[148:151], v[182:185], v[40:43]
	v_mfma_f32_16x16x32_bf16 v[36:39], v[156:159], v[182:185], v[36:39]
	v_mfma_f32_16x16x32_bf16 v[24:27], v[148:151], v[190:193], v[24:27]
	v_mfma_f32_16x16x32_bf16 v[20:23], v[156:159], v[190:193], v[20:23]
	v_mfma_f32_16x16x32_bf16 v[8:11], v[148:151], v[198:201], v[8:11]
	v_mfma_f32_16x16x32_bf16 v[4:7], v[156:159], v[198:201], v[4:7]
	s_setprio 2
	s_barrier
	v_add_u32_e32 v140, 0x18000, v164
	v_add_u32_e32 v156, 0x1c000, v164
	ds_read_b128 v[128:131], v140
	ds_read_b128 v[132:135], v140 offset:1024
	ds_read_b128 v[136:139], v140 offset:2048
	ds_read_b128 v[140:143], v140 offset:3072
	ds_read_b128 v[144:147], v156
	ds_read_b128 v[148:151], v156 offset:1024
	ds_read_b128 v[152:155], v156 offset:2048
	ds_read_b128 v[156:159], v156 offset:3072
	s_mov_b32 m0, s29
	ds_read_b128 v[166:169], v165 offset:32768
	ds_read_b128 v[170:173], v165 offset:33792
	ds_read_b128 v[178:181], v165 offset:34816
	ds_read_b128 v[182:185], v165 offset:35840
	ds_read_b128 v[186:189], v165 offset:36864
	ds_read_b128 v[190:193], v165 offset:37888
	ds_read_b128 v[194:197], v165 offset:38912
	ds_read_b128 v[198:201], v165 offset:39936
	buffer_load_dwordx4 v162, s[44:47], s80 offen lds
	s_mov_b32 m0, s30
	s_nop 0
	buffer_load_dwordx4 v163, s[44:47], s80 offen lds
	s_waitcnt vmcnt(8)
	s_waitcnt lgkmcnt(0)
	s_barrier
	s_setprio 1
	s_waitcnt lgkmcnt(7)
	v_mfma_f32_16x16x32_bf16 v[124:127], v[128:131], v[166:169], v[124:127]
	v_mfma_f32_16x16x32_bf16 v[120:123], v[136:139], v[166:169], v[120:123]
	s_waitcnt lgkmcnt(5)
	v_mfma_f32_16x16x32_bf16 v[108:111], v[128:131], v[178:181], v[108:111]
	v_mfma_f32_16x16x32_bf16 v[104:107], v[136:139], v[178:181], v[104:107]
	s_waitcnt lgkmcnt(3)
	v_mfma_f32_16x16x32_bf16 v[92:95], v[128:131], v[186:189], v[92:95]
	v_mfma_f32_16x16x32_bf16 v[88:91], v[136:139], v[186:189], v[88:91]
	s_waitcnt lgkmcnt(1)
	v_mfma_f32_16x16x32_bf16 v[76:79], v[128:131], v[194:197], v[76:79]
	v_mfma_f32_16x16x32_bf16 v[72:75], v[136:139], v[194:197], v[72:75]
	v_mfma_f32_16x16x32_bf16 v[124:127], v[132:135], v[170:173], v[124:127]
	v_mfma_f32_16x16x32_bf16 v[120:123], v[140:143], v[170:173], v[120:123]
	v_mfma_f32_16x16x32_bf16 v[108:111], v[132:135], v[182:185], v[108:111]
	v_mfma_f32_16x16x32_bf16 v[104:107], v[140:143], v[182:185], v[104:107]
	v_mfma_f32_16x16x32_bf16 v[92:95], v[132:135], v[190:193], v[92:95]
	v_mfma_f32_16x16x32_bf16 v[88:91], v[140:143], v[190:193], v[88:91]
	s_waitcnt lgkmcnt(0)
	v_mfma_f32_16x16x32_bf16 v[76:79], v[132:135], v[198:201], v[76:79]
	v_mfma_f32_16x16x32_bf16 v[72:75], v[140:143], v[198:201], v[72:75]
	s_setprio 2
	s_setprio 1
	v_mfma_f32_16x16x32_bf16 v[116:119], v[144:147], v[166:169], v[116:119]
	v_mfma_f32_16x16x32_bf16 v[112:115], v[152:155], v[166:169], v[112:115]
	v_mfma_f32_16x16x32_bf16 v[100:103], v[144:147], v[178:181], v[100:103]
	v_mfma_f32_16x16x32_bf16 v[96:99], v[152:155], v[178:181], v[96:99]
	v_mfma_f32_16x16x32_bf16 v[84:87], v[144:147], v[186:189], v[84:87]
	v_mfma_f32_16x16x32_bf16 v[80:83], v[152:155], v[186:189], v[80:83]
	v_mfma_f32_16x16x32_bf16 v[68:71], v[144:147], v[194:197], v[68:71]
	v_mfma_f32_16x16x32_bf16 v[64:67], v[152:155], v[194:197], v[64:67]
	v_mfma_f32_16x16x32_bf16 v[116:119], v[148:151], v[170:173], v[116:119]
	v_mfma_f32_16x16x32_bf16 v[112:115], v[156:159], v[170:173], v[112:115]
	v_mfma_f32_16x16x32_bf16 v[100:103], v[148:151], v[182:185], v[100:103]
	v_mfma_f32_16x16x32_bf16 v[96:99], v[156:159], v[182:185], v[96:99]
	v_mfma_f32_16x16x32_bf16 v[84:87], v[148:151], v[190:193], v[84:87]
	v_mfma_f32_16x16x32_bf16 v[80:83], v[156:159], v[190:193], v[80:83]
	v_mfma_f32_16x16x32_bf16 v[68:71], v[148:151], v[198:201], v[68:71]
	v_mfma_f32_16x16x32_bf16 v[64:67], v[156:159], v[198:201], v[64:67]
	s_setprio 2
	s_barrier
	s_mov_b32 m0, s31
	ds_read_b128 v[166:169], v165 offset:49152
	ds_read_b128 v[170:173], v165 offset:50176
	ds_read_b128 v[178:181], v165 offset:51200
	ds_read_b128 v[182:185], v165 offset:52224
	ds_read_b128 v[186:189], v165 offset:53248
	ds_read_b128 v[190:193], v165 offset:54272
	ds_read_b128 v[194:197], v165 offset:55296
	ds_read_b128 v[198:201], v165 offset:56320
	buffer_load_dwordx4 v160, s[48:51], s2 offen lds
	s_mov_b32 m0, s33
	s_add_i32 s3, s3, 0xa0080
	buffer_load_dwordx4 v161, s[48:51], s2 offen lds
	s_mov_b32 m0, s62
	s_nop 0
	buffer_load_dwordx4 v160, s[48:51], s3 offen lds
	s_mov_b32 m0, s63
	s_nop 0
	buffer_load_dwordx4 v161, s[48:51], s3 offen lds
	s_mov_b32 m0, s34
	s_nop 0
	buffer_load_dwordx4 v162, s[44:47], s2 offen lds
	s_mov_b32 m0, s35
	s_nop 0
	buffer_load_dwordx4 v163, s[44:47], s2 offen lds
	s_waitcnt vmcnt(8)
	s_waitcnt lgkmcnt(0)
	s_barrier
	s_setprio 1
	s_waitcnt lgkmcnt(7)
	v_mfma_f32_16x16x32_bf16 v[60:63], v[128:131], v[166:169], v[60:63]
	v_mfma_f32_16x16x32_bf16 v[0:3], v[136:139], v[166:169], v[0:3]
	s_waitcnt lgkmcnt(5)
	v_mfma_f32_16x16x32_bf16 v[48:51], v[128:131], v[178:181], v[48:51]
	v_mfma_f32_16x16x32_bf16 v[44:47], v[136:139], v[178:181], v[44:47]
	s_waitcnt lgkmcnt(3)
	v_mfma_f32_16x16x32_bf16 v[32:35], v[128:131], v[186:189], v[32:35]
	v_mfma_f32_16x16x32_bf16 v[28:31], v[136:139], v[186:189], v[28:31]
	s_waitcnt lgkmcnt(1)
	v_mfma_f32_16x16x32_bf16 v[16:19], v[128:131], v[194:197], v[16:19]
	v_mfma_f32_16x16x32_bf16 v[12:15], v[136:139], v[194:197], v[12:15]
	v_mfma_f32_16x16x32_bf16 v[60:63], v[132:135], v[170:173], v[60:63]
	v_mfma_f32_16x16x32_bf16 v[0:3], v[140:143], v[170:173], v[0:3]
	v_mfma_f32_16x16x32_bf16 v[48:51], v[132:135], v[182:185], v[48:51]
	v_mfma_f32_16x16x32_bf16 v[44:47], v[140:143], v[182:185], v[44:47]
	v_mfma_f32_16x16x32_bf16 v[32:35], v[132:135], v[190:193], v[32:35]
	v_mfma_f32_16x16x32_bf16 v[28:31], v[140:143], v[190:193], v[28:31]
	s_waitcnt lgkmcnt(0)
	v_mfma_f32_16x16x32_bf16 v[16:19], v[132:135], v[198:201], v[16:19]
	v_mfma_f32_16x16x32_bf16 v[12:15], v[140:143], v[198:201], v[12:15]
	s_setprio 2
	s_setprio 1
	v_mfma_f32_16x16x32_bf16 v[56:59], v[144:147], v[166:169], v[56:59]
	v_mfma_f32_16x16x32_bf16 v[52:55], v[152:155], v[166:169], v[52:55]
	v_mfma_f32_16x16x32_bf16 v[40:43], v[144:147], v[178:181], v[40:43]
	v_mfma_f32_16x16x32_bf16 v[36:39], v[152:155], v[178:181], v[36:39]
	v_mfma_f32_16x16x32_bf16 v[24:27], v[144:147], v[186:189], v[24:27]
	v_mfma_f32_16x16x32_bf16 v[20:23], v[152:155], v[186:189], v[20:23]
	v_mfma_f32_16x16x32_bf16 v[8:11], v[144:147], v[194:197], v[8:11]
	v_mfma_f32_16x16x32_bf16 v[4:7], v[152:155], v[194:197], v[4:7]
	v_mfma_f32_16x16x32_bf16 v[56:59], v[148:151], v[170:173], v[56:59]
	v_mfma_f32_16x16x32_bf16 v[52:55], v[156:159], v[170:173], v[52:55]
	v_mfma_f32_16x16x32_bf16 v[40:43], v[148:151], v[182:185], v[40:43]
	v_mfma_f32_16x16x32_bf16 v[36:39], v[156:159], v[182:185], v[36:39]
	v_mfma_f32_16x16x32_bf16 v[24:27], v[148:151], v[190:193], v[24:27]
	v_mfma_f32_16x16x32_bf16 v[20:23], v[156:159], v[190:193], v[20:23]
	v_mfma_f32_16x16x32_bf16 v[8:11], v[148:151], v[198:201], v[8:11]
	v_mfma_f32_16x16x32_bf16 v[4:7], v[156:159], v[198:201], v[4:7]
	s_setprio 2
	s_barrier
	s_add_i32 s2, s88, 2
	s_addk_i32 s83, 0x100
	s_cmp_gt_u32 s88, 37
	s_cbranch_scc1 .LBB0_1398
	s_mov_b32 s88, s2
	s_and_b32 s2, s88, 0x7ffffff6
	s_cmp_lg_u32 s2, 16
	s_cbranch_scc0 .LBB0_1395
	s_branch .LBB0_1396

.LBB0_1428:
	v_add_u32_e32 v140, 0x10000, v164
	v_add_u32_e32 v156, 0x14000, v164
	ds_read_b128 v[128:131], v140
	ds_read_b128 v[132:135], v140 offset:1024
	ds_read_b128 v[136:139], v140 offset:2048
	ds_read_b128 v[140:143], v140 offset:3072
	ds_read_b128 v[144:147], v156
	ds_read_b128 v[148:151], v156 offset:1024
	ds_read_b128 v[152:155], v156 offset:2048
	ds_read_b128 v[156:159], v156 offset:3072
	s_add_i32 s2, s83, 0xfff60080
	s_cmp_eq_u32 s88, 38
	s_cselect_b32 s3, 0, s2
	s_cselect_b32 s45, s39, s41
	s_cselect_b32 s44, s38, s40
	s_cselect_b32 s47, s71, s43
	s_cselect_b32 s46, s70, s42
	s_cselect_b32 s49, s73, s53
	s_cselect_b32 s48, s72, s52
	s_cselect_b32 s51, s77, s1
	s_cselect_b32 s50, s76, s0
	s_or_b32 s2, s3, 0x80
	s_mov_b32 m0, s21
	ds_read_b128 v[166:169], v165
	ds_read_b128 v[170:173], v165 offset:1024
	ds_read_b128 v[178:181], v165 offset:2048
	ds_read_b128 v[182:185], v165 offset:3072
	ds_read_b128 v[186:189], v165 offset:4096
	ds_read_b128 v[190:193], v165 offset:5120
	ds_read_b128 v[194:197], v165 offset:6144
	ds_read_b128 v[198:201], v165 offset:7168
	buffer_load_dwordx4 v162, s[40:43], s83 offen lds
	s_mov_b32 m0, s75
	s_nop 0
	buffer_load_dwordx4 v163, s[40:43], s83 offen lds
	s_waitcnt vmcnt(8)
	s_waitcnt lgkmcnt(0)
	s_barrier
	s_setprio 1
	s_waitcnt lgkmcnt(7)
	v_mfma_f32_16x16x32_bf16 v[124:127], v[128:131], v[166:169], v[124:127]
	v_mfma_f32_16x16x32_bf16 v[120:123], v[136:139], v[166:169], v[120:123]
	s_waitcnt lgkmcnt(5)
	v_mfma_f32_16x16x32_bf16 v[108:111], v[128:131], v[178:181], v[108:111]
	v_mfma_f32_16x16x32_bf16 v[104:107], v[136:139], v[178:181], v[104:107]
	s_waitcnt lgkmcnt(3)
	v_mfma_f32_16x16x32_bf16 v[92:95], v[128:131], v[186:189], v[92:95]
	v_mfma_f32_16x16x32_bf16 v[88:91], v[136:139], v[186:189], v[88:91]
	s_waitcnt lgkmcnt(1)
	v_mfma_f32_16x16x32_bf16 v[76:79], v[128:131], v[194:197], v[76:79]
	v_mfma_f32_16x16x32_bf16 v[72:75], v[136:139], v[194:197], v[72:75]
	v_mfma_f32_16x16x32_bf16 v[124:127], v[132:135], v[170:173], v[124:127]
	v_mfma_f32_16x16x32_bf16 v[120:123], v[140:143], v[170:173], v[120:123]
	v_mfma_f32_16x16x32_bf16 v[108:111], v[132:135], v[182:185], v[108:111]
	v_mfma_f32_16x16x32_bf16 v[104:107], v[140:143], v[182:185], v[104:107]
	v_mfma_f32_16x16x32_bf16 v[92:95], v[132:135], v[190:193], v[92:95]
	v_mfma_f32_16x16x32_bf16 v[88:91], v[140:143], v[190:193], v[88:91]
	s_waitcnt lgkmcnt(0)
	v_mfma_f32_16x16x32_bf16 v[76:79], v[132:135], v[198:201], v[76:79]
	v_mfma_f32_16x16x32_bf16 v[72:75], v[140:143], v[198:201], v[72:75]
	s_setprio 2
	s_setprio 1
	v_mfma_f32_16x16x32_bf16 v[116:119], v[144:147], v[166:169], v[116:119]
	v_mfma_f32_16x16x32_bf16 v[112:115], v[152:155], v[166:169], v[112:115]
	v_mfma_f32_16x16x32_bf16 v[100:103], v[144:147], v[178:181], v[100:103]
	v_mfma_f32_16x16x32_bf16 v[96:99], v[152:155], v[178:181], v[96:99]
	v_mfma_f32_16x16x32_bf16 v[84:87], v[144:147], v[186:189], v[84:87]
	v_mfma_f32_16x16x32_bf16 v[80:83], v[152:155], v[186:189], v[80:83]
	v_mfma_f32_16x16x32_bf16 v[68:71], v[144:147], v[194:197], v[68:71]
	v_mfma_f32_16x16x32_bf16 v[64:67], v[152:155], v[194:197], v[64:67]
	v_mfma_f32_16x16x32_bf16 v[116:119], v[148:151], v[170:173], v[116:119]
	v_mfma_f32_16x16x32_bf16 v[112:115], v[156:159], v[170:173], v[112:115]
	v_mfma_f32_16x16x32_bf16 v[100:103], v[148:151], v[182:185], v[100:103]
	v_mfma_f32_16x16x32_bf16 v[96:99], v[156:159], v[182:185], v[96:99]
	v_mfma_f32_16x16x32_bf16 v[84:87], v[148:151], v[190:193], v[84:87]
	v_mfma_f32_16x16x32_bf16 v[80:83], v[156:159], v[190:193], v[80:83]
	v_mfma_f32_16x16x32_bf16 v[68:71], v[148:151], v[198:201], v[68:71]
	v_mfma_f32_16x16x32_bf16 v[64:67], v[156:159], v[198:201], v[64:67]
	s_setprio 2
	s_barrier
	s_mov_b32 m0, s22
	ds_read_b128 v[166:169], v165 offset:16384
	ds_read_b128 v[170:173], v165 offset:17408
	ds_read_b128 v[178:181], v165 offset:18432
	ds_read_b128 v[182:185], v165 offset:19456
	ds_read_b128 v[186:189], v165 offset:20480
	ds_read_b128 v[190:193], v165 offset:21504
	ds_read_b128 v[194:197], v165 offset:22528
	ds_read_b128 v[198:201], v165 offset:23552
	buffer_load_dwordx4 v160, s[48:51], s3 offen lds
	s_mov_b32 m0, s23
	s_add_i32 s80, s3, 0xa0000
	buffer_load_dwordx4 v161, s[48:51], s3 offen lds
	s_mov_b32 m0, s28
	s_nop 0
	buffer_load_dwordx4 v160, s[48:51], s80 offen lds
	s_mov_b32 m0, s29
	s_nop 0
	buffer_load_dwordx4 v161, s[48:51], s80 offen lds
	s_mov_b32 m0, s74
	s_nop 0
	buffer_load_dwordx4 v162, s[44:47], s3 offen lds
	s_mov_b32 m0, s30
	s_nop 0
	buffer_load_dwordx4 v163, s[44:47], s3 offen lds
	s_waitcnt vmcnt(8)
	s_waitcnt lgkmcnt(0)
	s_barrier
	s_setprio 1
	s_waitcnt lgkmcnt(7)
	v_mfma_f32_16x16x32_bf16 v[60:63], v[128:131], v[166:169], v[60:63]
	v_mfma_f32_16x16x32_bf16 v[8:11], v[136:139], v[166:169], v[8:11]
	s_waitcnt lgkmcnt(5)
	v_mfma_f32_16x16x32_bf16 v[48:51], v[128:131], v[178:181], v[48:51]
	v_mfma_f32_16x16x32_bf16 v[44:47], v[136:139], v[178:181], v[44:47]
	s_waitcnt lgkmcnt(3)
	v_mfma_f32_16x16x32_bf16 v[32:35], v[128:131], v[186:189], v[32:35]
	v_mfma_f32_16x16x32_bf16 v[28:31], v[136:139], v[186:189], v[28:31]
	s_waitcnt lgkmcnt(1)
	v_mfma_f32_16x16x32_bf16 v[16:19], v[128:131], v[194:197], v[16:19]
	v_mfma_f32_16x16x32_bf16 v[12:15], v[136:139], v[194:197], v[12:15]
	v_mfma_f32_16x16x32_bf16 v[60:63], v[132:135], v[170:173], v[60:63]
	v_mfma_f32_16x16x32_bf16 v[8:11], v[140:143], v[170:173], v[8:11]
	v_mfma_f32_16x16x32_bf16 v[48:51], v[132:135], v[182:185], v[48:51]
	v_mfma_f32_16x16x32_bf16 v[44:47], v[140:143], v[182:185], v[44:47]
	v_mfma_f32_16x16x32_bf16 v[32:35], v[132:135], v[190:193], v[32:35]
	v_mfma_f32_16x16x32_bf16 v[28:31], v[140:143], v[190:193], v[28:31]
	s_waitcnt lgkmcnt(0)
	v_mfma_f32_16x16x32_bf16 v[16:19], v[132:135], v[198:201], v[16:19]
	v_mfma_f32_16x16x32_bf16 v[12:15], v[140:143], v[198:201], v[12:15]
	s_setprio 2
	s_setprio 1
	v_mfma_f32_16x16x32_bf16 v[56:59], v[144:147], v[166:169], v[56:59]
	v_mfma_f32_16x16x32_bf16 v[52:55], v[152:155], v[166:169], v[52:55]
	v_mfma_f32_16x16x32_bf16 v[40:43], v[144:147], v[178:181], v[40:43]
	v_mfma_f32_16x16x32_bf16 v[36:39], v[152:155], v[178:181], v[36:39]
	v_mfma_f32_16x16x32_bf16 v[24:27], v[144:147], v[186:189], v[24:27]
	v_mfma_f32_16x16x32_bf16 v[20:23], v[152:155], v[186:189], v[20:23]
	v_mfma_f32_16x16x32_bf16 v[4:7], v[144:147], v[194:197], v[4:7]
	v_mfma_f32_16x16x32_bf16 v[0:3], v[152:155], v[194:197], v[0:3]
	v_mfma_f32_16x16x32_bf16 v[56:59], v[148:151], v[170:173], v[56:59]
	v_mfma_f32_16x16x32_bf16 v[52:55], v[156:159], v[170:173], v[52:55]
	v_mfma_f32_16x16x32_bf16 v[40:43], v[148:151], v[182:185], v[40:43]
	v_mfma_f32_16x16x32_bf16 v[36:39], v[156:159], v[182:185], v[36:39]
	v_mfma_f32_16x16x32_bf16 v[24:27], v[148:151], v[190:193], v[24:27]
	v_mfma_f32_16x16x32_bf16 v[20:23], v[156:159], v[190:193], v[20:23]
	v_mfma_f32_16x16x32_bf16 v[4:7], v[148:151], v[198:201], v[4:7]
	v_mfma_f32_16x16x32_bf16 v[0:3], v[156:159], v[198:201], v[0:3]
	s_setprio 2
	s_barrier
	v_add_u32_e32 v140, 0x18000, v164
	v_add_u32_e32 v156, 0x1c000, v164
	ds_read_b128 v[128:131], v140
	ds_read_b128 v[132:135], v140 offset:1024
	ds_read_b128 v[136:139], v140 offset:2048
	ds_read_b128 v[140:143], v140 offset:3072
	ds_read_b128 v[144:147], v156
	ds_read_b128 v[148:151], v156 offset:1024
	ds_read_b128 v[152:155], v156 offset:2048
	ds_read_b128 v[156:159], v156 offset:3072
	s_mov_b32 m0, s31
	ds_read_b128 v[166:169], v165 offset:32768
	ds_read_b128 v[170:173], v165 offset:33792
	ds_read_b128 v[178:181], v165 offset:34816
	ds_read_b128 v[182:185], v165 offset:35840
	ds_read_b128 v[186:189], v165 offset:36864
	ds_read_b128 v[190:193], v165 offset:37888
	ds_read_b128 v[194:197], v165 offset:38912
	ds_read_b128 v[198:201], v165 offset:39936
	buffer_load_dwordx4 v162, s[44:47], s80 offen lds
	s_mov_b32 m0, s33
	s_nop 0
	buffer_load_dwordx4 v163, s[44:47], s80 offen lds
	s_waitcnt vmcnt(8)
	s_waitcnt lgkmcnt(0)
	s_barrier
	s_setprio 1
	s_waitcnt lgkmcnt(7)
	v_mfma_f32_16x16x32_bf16 v[124:127], v[128:131], v[166:169], v[124:127]
	v_mfma_f32_16x16x32_bf16 v[120:123], v[136:139], v[166:169], v[120:123]
	s_waitcnt lgkmcnt(5)
	v_mfma_f32_16x16x32_bf16 v[108:111], v[128:131], v[178:181], v[108:111]
	v_mfma_f32_16x16x32_bf16 v[104:107], v[136:139], v[178:181], v[104:107]
	s_waitcnt lgkmcnt(3)
	v_mfma_f32_16x16x32_bf16 v[92:95], v[128:131], v[186:189], v[92:95]
	v_mfma_f32_16x16x32_bf16 v[88:91], v[136:139], v[186:189], v[88:91]
	s_waitcnt lgkmcnt(1)
	v_mfma_f32_16x16x32_bf16 v[76:79], v[128:131], v[194:197], v[76:79]
	v_mfma_f32_16x16x32_bf16 v[72:75], v[136:139], v[194:197], v[72:75]
	v_mfma_f32_16x16x32_bf16 v[124:127], v[132:135], v[170:173], v[124:127]
	v_mfma_f32_16x16x32_bf16 v[120:123], v[140:143], v[170:173], v[120:123]
	v_mfma_f32_16x16x32_bf16 v[108:111], v[132:135], v[182:185], v[108:111]
	v_mfma_f32_16x16x32_bf16 v[104:107], v[140:143], v[182:185], v[104:107]
	v_mfma_f32_16x16x32_bf16 v[92:95], v[132:135], v[190:193], v[92:95]
	v_mfma_f32_16x16x32_bf16 v[88:91], v[140:143], v[190:193], v[88:91]
	s_waitcnt lgkmcnt(0)
	v_mfma_f32_16x16x32_bf16 v[76:79], v[132:135], v[198:201], v[76:79]
	v_mfma_f32_16x16x32_bf16 v[72:75], v[140:143], v[198:201], v[72:75]
	s_setprio 2
	s_setprio 1
	v_mfma_f32_16x16x32_bf16 v[116:119], v[144:147], v[166:169], v[116:119]
	v_mfma_f32_16x16x32_bf16 v[112:115], v[152:155], v[166:169], v[112:115]
	v_mfma_f32_16x16x32_bf16 v[100:103], v[144:147], v[178:181], v[100:103]
	v_mfma_f32_16x16x32_bf16 v[96:99], v[152:155], v[178:181], v[96:99]
	v_mfma_f32_16x16x32_bf16 v[84:87], v[144:147], v[186:189], v[84:87]
	v_mfma_f32_16x16x32_bf16 v[80:83], v[152:155], v[186:189], v[80:83]
	v_mfma_f32_16x16x32_bf16 v[68:71], v[144:147], v[194:197], v[68:71]
	v_mfma_f32_16x16x32_bf16 v[64:67], v[152:155], v[194:197], v[64:67]
	v_mfma_f32_16x16x32_bf16 v[116:119], v[148:151], v[170:173], v[116:119]
	v_mfma_f32_16x16x32_bf16 v[112:115], v[156:159], v[170:173], v[112:115]
	v_mfma_f32_16x16x32_bf16 v[100:103], v[148:151], v[182:185], v[100:103]
	v_mfma_f32_16x16x32_bf16 v[96:99], v[156:159], v[182:185], v[96:99]
	v_mfma_f32_16x16x32_bf16 v[84:87], v[148:151], v[190:193], v[84:87]
	v_mfma_f32_16x16x32_bf16 v[80:83], v[156:159], v[190:193], v[80:83]
	v_mfma_f32_16x16x32_bf16 v[68:71], v[148:151], v[198:201], v[68:71]
	v_mfma_f32_16x16x32_bf16 v[64:67], v[156:159], v[198:201], v[64:67]
	s_setprio 2
	s_barrier
	s_mov_b32 m0, s34
	ds_read_b128 v[166:169], v165 offset:49152
	ds_read_b128 v[170:173], v165 offset:50176
	ds_read_b128 v[178:181], v165 offset:51200
	ds_read_b128 v[182:185], v165 offset:52224
	ds_read_b128 v[186:189], v165 offset:53248
	ds_read_b128 v[190:193], v165 offset:54272
	ds_read_b128 v[194:197], v165 offset:55296
	ds_read_b128 v[198:201], v165 offset:56320
	buffer_load_dwordx4 v160, s[48:51], s2 offen lds
	s_mov_b32 m0, s35
	s_add_i32 s3, s3, 0xa0080
	buffer_load_dwordx4 v161, s[48:51], s2 offen lds
	s_mov_b32 m0, s64
	s_nop 0
	buffer_load_dwordx4 v160, s[48:51], s3 offen lds
	s_mov_b32 m0, s65
	s_nop 0
	buffer_load_dwordx4 v161, s[48:51], s3 offen lds
	s_mov_b32 m0, s62
	s_nop 0
	buffer_load_dwordx4 v162, s[44:47], s2 offen lds
	s_mov_b32 m0, s63
	s_nop 0
	buffer_load_dwordx4 v163, s[44:47], s2 offen lds
	s_waitcnt vmcnt(8)
	s_waitcnt lgkmcnt(0)
	s_barrier
	s_setprio 1
	s_waitcnt lgkmcnt(7)
	v_mfma_f32_16x16x32_bf16 v[60:63], v[128:131], v[166:169], v[60:63]
	v_mfma_f32_16x16x32_bf16 v[8:11], v[136:139], v[166:169], v[8:11]
	s_waitcnt lgkmcnt(5)
	v_mfma_f32_16x16x32_bf16 v[48:51], v[128:131], v[178:181], v[48:51]
	v_mfma_f32_16x16x32_bf16 v[44:47], v[136:139], v[178:181], v[44:47]
	s_waitcnt lgkmcnt(3)
	v_mfma_f32_16x16x32_bf16 v[32:35], v[128:131], v[186:189], v[32:35]
	v_mfma_f32_16x16x32_bf16 v[28:31], v[136:139], v[186:189], v[28:31]
	s_waitcnt lgkmcnt(1)
	v_mfma_f32_16x16x32_bf16 v[16:19], v[128:131], v[194:197], v[16:19]
	v_mfma_f32_16x16x32_bf16 v[12:15], v[136:139], v[194:197], v[12:15]
	v_mfma_f32_16x16x32_bf16 v[60:63], v[132:135], v[170:173], v[60:63]
	v_mfma_f32_16x16x32_bf16 v[8:11], v[140:143], v[170:173], v[8:11]
	v_mfma_f32_16x16x32_bf16 v[48:51], v[132:135], v[182:185], v[48:51]
	v_mfma_f32_16x16x32_bf16 v[44:47], v[140:143], v[182:185], v[44:47]
	v_mfma_f32_16x16x32_bf16 v[32:35], v[132:135], v[190:193], v[32:35]
	v_mfma_f32_16x16x32_bf16 v[28:31], v[140:143], v[190:193], v[28:31]
	s_waitcnt lgkmcnt(0)
	v_mfma_f32_16x16x32_bf16 v[16:19], v[132:135], v[198:201], v[16:19]
	v_mfma_f32_16x16x32_bf16 v[12:15], v[140:143], v[198:201], v[12:15]
	s_setprio 2
	s_setprio 1
	v_mfma_f32_16x16x32_bf16 v[56:59], v[144:147], v[166:169], v[56:59]
	v_mfma_f32_16x16x32_bf16 v[52:55], v[152:155], v[166:169], v[52:55]
	v_mfma_f32_16x16x32_bf16 v[40:43], v[144:147], v[178:181], v[40:43]
	v_mfma_f32_16x16x32_bf16 v[36:39], v[152:155], v[178:181], v[36:39]
	v_mfma_f32_16x16x32_bf16 v[24:27], v[144:147], v[186:189], v[24:27]
	v_mfma_f32_16x16x32_bf16 v[20:23], v[152:155], v[186:189], v[20:23]
	v_mfma_f32_16x16x32_bf16 v[4:7], v[144:147], v[194:197], v[4:7]
	v_mfma_f32_16x16x32_bf16 v[0:3], v[152:155], v[194:197], v[0:3]
	v_mfma_f32_16x16x32_bf16 v[56:59], v[148:151], v[170:173], v[56:59]
	v_mfma_f32_16x16x32_bf16 v[52:55], v[156:159], v[170:173], v[52:55]
	v_mfma_f32_16x16x32_bf16 v[40:43], v[148:151], v[182:185], v[40:43]
	v_mfma_f32_16x16x32_bf16 v[36:39], v[156:159], v[182:185], v[36:39]
	v_mfma_f32_16x16x32_bf16 v[24:27], v[148:151], v[190:193], v[24:27]
	v_mfma_f32_16x16x32_bf16 v[20:23], v[156:159], v[190:193], v[20:23]
	v_mfma_f32_16x16x32_bf16 v[4:7], v[148:151], v[198:201], v[4:7]
	v_mfma_f32_16x16x32_bf16 v[0:3], v[156:159], v[198:201], v[0:3]
	s_setprio 2
	s_barrier
	s_add_i32 s2, s88, 2
	s_addk_i32 s83, 0x100
	s_cmp_gt_u32 s88, 37
	s_cbranch_scc1 .LBB0_1430
	s_mov_b32 s88, s2
	s_and_b32 s2, s88, 0x7ffffff6
	s_cmp_lg_u32 s2, 16
	s_cbranch_scc0 .LBB0_1427
	s_branch .LBB0_1428

.LBB0_1507:
	v_add_u32_e32 v116, 0x10000, v176
	v_add_u32_e32 v120, 0x14000, v176
	ds_read_b128 v[104:107], v116
	ds_read_b128 v[108:111], v116 offset:1024
	ds_read_b128 v[112:115], v116 offset:2048
	ds_read_b128 v[116:119], v116 offset:3072
	ds_read_b128 v[148:151], v120
	ds_read_b128 v[152:155], v120 offset:1024
	ds_read_b128 v[156:159], v120 offset:2048
	ds_read_b128 v[160:163], v120 offset:3072
	s_add_i32 s21, s13, 0xfffc0080
	s_cmp_eq_u32 s12, 12
	s_cselect_b32 s45, s29, s41
	s_cselect_b32 s44, s28, s40
	s_cselect_b32 s47, s31, s43
	s_cselect_b32 s46, s30, s42
	s_cselect_b32 s21, 0, s21
	s_cselect_b32 s49, s35, s53
	s_cselect_b32 s48, s34, s52
	s_cselect_b32 s51, s39, s5
	s_cselect_b32 s50, s38, s4
	s_mov_b32 m0, s90
	ds_read_b128 v[164:167], v198
	ds_read_b128 v[168:171], v198 offset:1024
	ds_read_b128 v[200:203], v198 offset:2048
	ds_read_b128 v[204:207], v198 offset:3072
	ds_read_b128 v[208:211], v198 offset:4096
	ds_read_b128 v[212:215], v198 offset:5120
	ds_read_b128 v[216:219], v198 offset:6144
	ds_read_b128 v[220:223], v198 offset:7168
	buffer_load_dwordx4 v229, s[40:43], s13 offen lds
	s_mov_b32 m0, s92
	s_nop 0
	buffer_load_dwordx4 v252, s[40:43], s13 offen lds
	s_waitcnt vmcnt(8)
	s_waitcnt lgkmcnt(0)
	s_barrier
	s_setprio 1
	s_waitcnt lgkmcnt(6)
	v_mfma_scale_f32_16x16x128_f8f6f4 v[140:143], v[112:119], v[164:171], v[140:143], v230, v230 op_sel_hi:[0,0,0]
	s_waitcnt lgkmcnt(4)
	v_mfma_scale_f32_16x16x128_f8f6f4 v[128:131], v[104:111], v[200:207], v[128:131], v230, v230 op_sel_hi:[0,0,0]
	v_mfma_scale_f32_16x16x128_f8f6f4 v[124:127], v[112:119], v[200:207], v[124:127], v230, v230 op_sel_hi:[0,0,0]
	v_mfma_scale_f32_16x16x128_f8f6f4 v[120:123], v[104:111], v[164:171], v[144:147], v230, v230 op_sel_hi:[0,0,0]
	s_waitcnt lgkmcnt(2)
	v_mfma_scale_f32_16x16x128_f8f6f4 v[178:181], v[104:111], v[208:215], v[92:95], v230, v230 op_sel_hi:[0,0,0]
	v_mfma_scale_f32_16x16x128_f8f6f4 v[182:185], v[112:119], v[208:215], v[88:91], v230, v230 op_sel_hi:[0,0,0]
	s_waitcnt lgkmcnt(0)
	v_mfma_scale_f32_16x16x128_f8f6f4 v[186:189], v[104:111], v[216:223], v[76:79], v230, v230 op_sel_hi:[0,0,0]
	v_mfma_scale_f32_16x16x128_f8f6f4 v[190:193], v[112:119], v[216:223], v[72:75], v230, v230 op_sel_hi:[0,0,0]
	s_setprio 2
	s_setprio 1
	v_mfma_scale_f32_16x16x128_f8f6f4 v[136:139], v[148:155], v[164:171], v[136:139], v230, v230 op_sel_hi:[0,0,0]
	v_mfma_scale_f32_16x16x128_f8f6f4 v[132:135], v[156:163], v[164:171], v[132:135], v230, v230 op_sel_hi:[0,0,0]
	v_mfma_scale_f32_16x16x128_f8f6f4 v[100:103], v[148:155], v[200:207], v[100:103], v230, v230 op_sel_hi:[0,0,0]
	v_mfma_scale_f32_16x16x128_f8f6f4 v[96:99], v[156:163], v[200:207], v[96:99], v230, v230 op_sel_hi:[0,0,0]
	v_mfma_scale_f32_16x16x128_f8f6f4 v[164:167], v[148:155], v[208:215], v[84:87], v230, v230 op_sel_hi:[0,0,0]
	v_mfma_scale_f32_16x16x128_f8f6f4 v[168:171], v[156:163], v[208:215], v[80:83], v230, v230 op_sel_hi:[0,0,0]
	v_mfma_scale_f32_16x16x128_f8f6f4 v[194:197], v[148:155], v[216:223], v[68:71], v230, v230 op_sel_hi:[0,0,0]
	v_mfma_scale_f32_16x16x128_f8f6f4 v[200:203], v[156:163], v[216:223], v[64:67], v230, v230 op_sel_hi:[0,0,0]
	s_setprio 2
	s_barrier
	s_mov_b32 m0, s63
	s_nop 3
	ds_read_b128 v[64:67], v198 offset:16384
	ds_read_b128 v[68:71], v198 offset:17408
	ds_read_b128 v[72:75], v198 offset:18432
	ds_read_b128 v[76:79], v198 offset:19456
	ds_read_b128 v[80:83], v198 offset:20480
	ds_read_b128 v[84:87], v198 offset:21504
	ds_read_b128 v[88:91], v198 offset:22528
	ds_read_b128 v[92:95], v198 offset:23552
	buffer_load_dwordx4 v199, s[48:51], s21 offen lds
	s_mov_b32 m0, s69
	s_add_i32 s23, s21, 0x40000
	buffer_load_dwordx4 v228, s[48:51], s21 offen lds
	s_mov_b32 m0, s70
	s_nop 0
	buffer_load_dwordx4 v199, s[48:51], s23 offen lds
	s_mov_b32 m0, s71
	s_nop 0
	buffer_load_dwordx4 v228, s[48:51], s23 offen lds
	s_mov_b32 m0, s62
	s_nop 0
	buffer_load_dwordx4 v229, s[44:47], s21 offen lds
	s_mov_b32 m0, s72
	s_nop 0
	buffer_load_dwordx4 v252, s[44:47], s21 offen lds
	s_waitcnt vmcnt(8)
	s_waitcnt lgkmcnt(0)
	s_barrier
	s_setprio 1
	s_waitcnt lgkmcnt(6)
	v_mfma_scale_f32_16x16x128_f8f6f4 v[60:63], v[104:111], v[64:71], v[60:63], v230, v230 op_sel_hi:[0,0,0]
	s_waitcnt lgkmcnt(0)
	v_mfma_scale_f32_16x16x128_f8f6f4 v[16:19], v[104:111], v[88:95], v[16:19], v230, v230 op_sel_hi:[0,0,0]
	v_mfma_scale_f32_16x16x128_f8f6f4 v[204:207], v[112:119], v[64:71], v[8:11], v230, v230 op_sel_hi:[0,0,0]
	v_mfma_scale_f32_16x16x128_f8f6f4 v[208:211], v[104:111], v[72:79], v[48:51], v230, v230 op_sel_hi:[0,0,0]
	v_mfma_scale_f32_16x16x128_f8f6f4 v[212:215], v[112:119], v[72:79], v[44:47], v230, v230 op_sel_hi:[0,0,0]
	v_mfma_scale_f32_16x16x128_f8f6f4 v[216:219], v[104:111], v[80:87], v[32:35], v230, v230 op_sel_hi:[0,0,0]
	v_mfma_scale_f32_16x16x128_f8f6f4 v[220:223], v[112:119], v[80:87], v[28:31], v230, v230 op_sel_hi:[0,0,0]
	v_mfma_scale_f32_16x16x128_f8f6f4 v[224:227], v[112:119], v[88:95], v[12:15], v230, v230 op_sel_hi:[0,0,0]
	s_setprio 2
	s_setprio 1
	v_mfma_scale_f32_16x16x128_f8f6f4 v[56:59], v[148:155], v[64:71], v[56:59], v230, v230 op_sel_hi:[0,0,0]
	v_mfma_scale_f32_16x16x128_f8f6f4 v[52:55], v[156:163], v[64:71], v[52:55], v230, v230 op_sel_hi:[0,0,0]
	v_mfma_scale_f32_16x16x128_f8f6f4 v[232:235], v[148:155], v[72:79], v[40:43], v230, v230 op_sel_hi:[0,0,0]
	v_mfma_scale_f32_16x16x128_f8f6f4 v[236:239], v[156:163], v[72:79], v[36:39], v230, v230 op_sel_hi:[0,0,0]
	v_mfma_scale_f32_16x16x128_f8f6f4 v[240:243], v[148:155], v[80:87], v[24:27], v230, v230 op_sel_hi:[0,0,0]
	v_mfma_scale_f32_16x16x128_f8f6f4 v[244:247], v[156:163], v[80:87], v[20:23], v230, v230 op_sel_hi:[0,0,0]
	v_mfma_scale_f32_16x16x128_f8f6f4 v[248:251], v[148:155], v[88:95], v[4:7], v230, v230 op_sel_hi:[0,0,0]
	v_mfma_scale_f32_16x16x128_f8f6f4 v[172:175], v[156:163], v[88:95], v[0:3], v230, v230 op_sel_hi:[0,0,0]
	s_setprio 2
	s_barrier
	v_add_u32_e32 v8, 0x18000, v176
	s_nop 3
	ds_read_b128 v[0:3], v8
	ds_read_b128 v[4:7], v8 offset:1024
	ds_read_b128 v[20:23], v8 offset:2048
	ds_read_b128 v[24:27], v8 offset:3072
	v_add_u32_e32 v8, 0x1c000, v176
	ds_read_b128 v[104:107], v8
	ds_read_b128 v[108:111], v8 offset:1024
	ds_read_b128 v[112:115], v8 offset:2048
	ds_read_b128 v[116:119], v8 offset:3072
	s_mov_b32 m0, s73
	ds_read_b128 v[8:11], v198 offset:32768
	ds_read_b128 v[12:15], v198 offset:33792
	ds_read_b128 v[28:31], v198 offset:34816
	ds_read_b128 v[32:35], v198 offset:35840
	ds_read_b128 v[36:39], v198 offset:36864
	ds_read_b128 v[40:43], v198 offset:37888
	ds_read_b128 v[44:47], v198 offset:38912
	ds_read_b128 v[48:51], v198 offset:39936
	buffer_load_dwordx4 v229, s[44:47], s23 offen lds
	s_mov_b32 m0, s74
	s_nop 0
	buffer_load_dwordx4 v252, s[44:47], s23 offen lds
	s_waitcnt vmcnt(8)
	s_waitcnt lgkmcnt(0)
	s_barrier
	s_setprio 1
	s_waitcnt lgkmcnt(6)
	v_mfma_scale_f32_16x16x128_f8f6f4 v[144:147], v[0:7], v[8:15], v[120:123], v230, v230 op_sel_hi:[0,0,0]
	v_mfma_scale_f32_16x16x128_f8f6f4 v[140:143], v[20:27], v[8:15], v[140:143], v230, v230 op_sel_hi:[0,0,0]
	s_waitcnt lgkmcnt(4)
	v_mfma_scale_f32_16x16x128_f8f6f4 v[128:131], v[0:7], v[28:35], v[128:131], v230, v230 op_sel_hi:[0,0,0]
	v_mfma_scale_f32_16x16x128_f8f6f4 v[124:127], v[20:27], v[28:35], v[124:127], v230, v230 op_sel_hi:[0,0,0]
	s_waitcnt lgkmcnt(2)
	v_mfma_scale_f32_16x16x128_f8f6f4 v[92:95], v[0:7], v[36:43], v[178:181], v230, v230 op_sel_hi:[0,0,0]
	v_mfma_scale_f32_16x16x128_f8f6f4 v[88:91], v[20:27], v[36:43], v[182:185], v230, v230 op_sel_hi:[0,0,0]
	s_waitcnt lgkmcnt(0)
	v_mfma_scale_f32_16x16x128_f8f6f4 v[76:79], v[0:7], v[44:51], v[186:189], v230, v230 op_sel_hi:[0,0,0]
	v_mfma_scale_f32_16x16x128_f8f6f4 v[72:75], v[20:27], v[44:51], v[190:193], v230, v230 op_sel_hi:[0,0,0]
	s_setprio 2
	s_setprio 1
	v_mfma_scale_f32_16x16x128_f8f6f4 v[136:139], v[104:111], v[8:15], v[136:139], v230, v230 op_sel_hi:[0,0,0]
	v_mfma_scale_f32_16x16x128_f8f6f4 v[132:135], v[112:119], v[8:15], v[132:135], v230, v230 op_sel_hi:[0,0,0]
	v_mfma_scale_f32_16x16x128_f8f6f4 v[100:103], v[104:111], v[28:35], v[100:103], v230, v230 op_sel_hi:[0,0,0]
	v_mfma_scale_f32_16x16x128_f8f6f4 v[96:99], v[112:119], v[28:35], v[96:99], v230, v230 op_sel_hi:[0,0,0]
	v_mfma_scale_f32_16x16x128_f8f6f4 v[84:87], v[104:111], v[36:43], v[164:167], v230, v230 op_sel_hi:[0,0,0]
	v_mfma_scale_f32_16x16x128_f8f6f4 v[80:83], v[112:119], v[36:43], v[168:171], v230, v230 op_sel_hi:[0,0,0]
	v_mfma_scale_f32_16x16x128_f8f6f4 v[68:71], v[104:111], v[44:51], v[194:197], v230, v230 op_sel_hi:[0,0,0]
	v_mfma_scale_f32_16x16x128_f8f6f4 v[64:67], v[112:119], v[44:51], v[200:203], v230, v230 op_sel_hi:[0,0,0]
	s_setprio 2
	s_barrier
	s_mov_b32 m0, s75
	s_or_b32 s23, s21, 0x80
	ds_read_b128 v[36:39], v198 offset:49152
	ds_read_b128 v[40:43], v198 offset:50176
	ds_read_b128 v[148:151], v198 offset:51200
	ds_read_b128 v[152:155], v198 offset:52224
	ds_read_b128 v[156:159], v198 offset:53248
	ds_read_b128 v[160:163], v198 offset:54272
	ds_read_b128 v[164:167], v198 offset:55296
	ds_read_b128 v[168:171], v198 offset:56320
	buffer_load_dwordx4 v199, s[48:51], s23 offen lds
	s_mov_b32 m0, s76
	s_add_i32 s21, s21, 0x40080
	buffer_load_dwordx4 v228, s[48:51], s23 offen lds
	s_mov_b32 m0, s82
	s_nop 0
	buffer_load_dwordx4 v199, s[48:51], s21 offen lds
	s_mov_b32 m0, s83
	s_nop 0
	buffer_load_dwordx4 v228, s[48:51], s21 offen lds
	s_mov_b32 m0, s77
	s_nop 0
	buffer_load_dwordx4 v229, s[44:47], s23 offen lds
	s_mov_b32 m0, s80
	s_nop 0
	buffer_load_dwordx4 v252, s[44:47], s23 offen lds
	s_waitcnt vmcnt(8)
	s_waitcnt lgkmcnt(0)
	s_barrier
	s_setprio 1
	s_waitcnt lgkmcnt(6)
	v_mfma_scale_f32_16x16x128_f8f6f4 v[60:63], v[0:7], v[36:43], v[60:63], v230, v230 op_sel_hi:[0,0,0]
	v_mfma_scale_f32_16x16x128_f8f6f4 v[8:11], v[20:27], v[36:43], v[204:207], v230, v230 op_sel_hi:[0,0,0]
	s_waitcnt lgkmcnt(4)
	v_mfma_scale_f32_16x16x128_f8f6f4 v[48:51], v[0:7], v[148:155], v[208:211], v230, v230 op_sel_hi:[0,0,0]
	v_mfma_scale_f32_16x16x128_f8f6f4 v[44:47], v[20:27], v[148:155], v[212:215], v230, v230 op_sel_hi:[0,0,0]
	s_waitcnt lgkmcnt(2)
	v_mfma_scale_f32_16x16x128_f8f6f4 v[32:35], v[0:7], v[156:163], v[216:219], v230, v230 op_sel_hi:[0,0,0]
	v_mfma_scale_f32_16x16x128_f8f6f4 v[28:31], v[20:27], v[156:163], v[220:223], v230, v230 op_sel_hi:[0,0,0]
	s_waitcnt lgkmcnt(0)
	v_mfma_scale_f32_16x16x128_f8f6f4 v[16:19], v[0:7], v[164:171], v[16:19], v230, v230 op_sel_hi:[0,0,0]
	v_mfma_scale_f32_16x16x128_f8f6f4 v[12:15], v[20:27], v[164:171], v[224:227], v230, v230 op_sel_hi:[0,0,0]
	s_setprio 2
	s_setprio 1
	v_mfma_scale_f32_16x16x128_f8f6f4 v[56:59], v[104:111], v[36:43], v[56:59], v230, v230 op_sel_hi:[0,0,0]
	v_mfma_scale_f32_16x16x128_f8f6f4 v[52:55], v[112:119], v[36:43], v[52:55], v230, v230 op_sel_hi:[0,0,0]
	v_mfma_scale_f32_16x16x128_f8f6f4 v[40:43], v[104:111], v[148:155], v[232:235], v230, v230 op_sel_hi:[0,0,0]
	v_mfma_scale_f32_16x16x128_f8f6f4 v[36:39], v[112:119], v[148:155], v[236:239], v230, v230 op_sel_hi:[0,0,0]
	v_mfma_scale_f32_16x16x128_f8f6f4 v[24:27], v[104:111], v[156:163], v[240:243], v230, v230 op_sel_hi:[0,0,0]
	v_mfma_scale_f32_16x16x128_f8f6f4 v[20:23], v[112:119], v[156:163], v[244:247], v230, v230 op_sel_hi:[0,0,0]
	v_mfma_scale_f32_16x16x128_f8f6f4 v[4:7], v[104:111], v[164:171], v[248:251], v230, v230 op_sel_hi:[0,0,0]
	v_mfma_scale_f32_16x16x128_f8f6f4 v[0:3], v[112:119], v[164:171], v[172:175], v230, v230 op_sel_hi:[0,0,0]
	s_setprio 2
	s_barrier
	s_add_i32 s12, s12, 2
	s_addk_i32 s13, 0x100
	s_cmp_gt_u32 s12, 13
	s_cbranch_scc0 .LBB0_1507
	s_and_b64 vcc, exec, s[18:19]
	s_cbranch_vccz .LBB0_1510
	s_barrier

.LBB0_1539:
	v_add_u32_e32 v124, 0x10000, v174
	v_add_u32_e32 v156, 0x14000, v174
	ds_read_b128 v[104:107], v124
	ds_read_b128 v[116:119], v124 offset:1024
	ds_read_b128 v[120:123], v124 offset:2048
	ds_read_b128 v[124:127], v124 offset:3072
	ds_read_b128 v[128:131], v156
	ds_read_b128 v[136:139], v156 offset:1024
	ds_read_b128 v[152:155], v156 offset:2048
	ds_read_b128 v[156:159], v156 offset:3072
	s_add_i32 s19, s13, 0xfff80080
	s_cmp_eq_u32 s12, 28
	s_cselect_b32 s45, s23, s41
	s_cselect_b32 s44, s22, s40
	s_cselect_b32 s47, s29, s43
	s_cselect_b32 s46, s28, s42
	s_cselect_b32 s19, 0, s19
	s_cselect_b32 s49, s31, s53
	s_cselect_b32 s48, s30, s52
	s_cselect_b32 s51, s35, s5
	s_cselect_b32 s50, s34, s4
	s_mov_b32 m0, s92
	ds_read_b128 v[160:163], v175
	ds_read_b128 v[164:167], v175 offset:1024
	ds_read_b128 v[178:181], v175 offset:2048
	ds_read_b128 v[182:185], v175 offset:3072
	ds_read_b128 v[186:189], v175 offset:4096
	ds_read_b128 v[190:193], v175 offset:5120
	ds_read_b128 v[194:197], v175 offset:6144
	ds_read_b128 v[198:201], v175 offset:7168
	buffer_load_dwordx4 v172, s[40:43], s13 offen lds
	s_mov_b32 m0, s94
	s_nop 0
	buffer_load_dwordx4 v173, s[40:43], s13 offen lds
	s_waitcnt vmcnt(8)
	s_waitcnt lgkmcnt(0)
	s_barrier
	s_setprio 1
	s_waitcnt lgkmcnt(7)
	v_mfma_f32_16x16x32_bf16 v[148:151], v[104:107], v[160:163], v[148:151]
	v_mfma_f32_16x16x32_bf16 v[144:147], v[120:123], v[160:163], v[144:147]
	s_waitcnt lgkmcnt(5)
	v_mfma_f32_16x16x32_bf16 v[112:115], v[104:107], v[178:181], v[112:115]
	v_mfma_f32_16x16x32_bf16 v[108:111], v[120:123], v[178:181], v[108:111]
	s_waitcnt lgkmcnt(3)
	v_mfma_f32_16x16x32_bf16 v[92:95], v[104:107], v[186:189], v[92:95]
	v_mfma_f32_16x16x32_bf16 v[88:91], v[120:123], v[186:189], v[88:91]
	s_waitcnt lgkmcnt(1)
	v_mfma_f32_16x16x32_bf16 v[76:79], v[104:107], v[194:197], v[76:79]
	v_mfma_f32_16x16x32_bf16 v[72:75], v[120:123], v[194:197], v[72:75]
	v_mfma_f32_16x16x32_bf16 v[148:151], v[116:119], v[164:167], v[148:151]
	v_mfma_f32_16x16x32_bf16 v[144:147], v[124:127], v[164:167], v[144:147]
	v_mfma_f32_16x16x32_bf16 v[112:115], v[116:119], v[182:185], v[112:115]
	v_mfma_f32_16x16x32_bf16 v[108:111], v[124:127], v[182:185], v[108:111]
	v_mfma_f32_16x16x32_bf16 v[92:95], v[116:119], v[190:193], v[92:95]
	v_mfma_f32_16x16x32_bf16 v[88:91], v[124:127], v[190:193], v[88:91]
	s_waitcnt lgkmcnt(0)
	v_mfma_f32_16x16x32_bf16 v[76:79], v[116:119], v[198:201], v[76:79]
	v_mfma_f32_16x16x32_bf16 v[72:75], v[124:127], v[198:201], v[72:75]
	s_setprio 2
	s_setprio 1
	v_mfma_f32_16x16x32_bf16 v[140:143], v[128:131], v[160:163], v[140:143]
	v_mfma_f32_16x16x32_bf16 v[132:135], v[152:155], v[160:163], v[132:135]
	v_mfma_f32_16x16x32_bf16 v[100:103], v[128:131], v[178:181], v[100:103]
	v_mfma_f32_16x16x32_bf16 v[96:99], v[152:155], v[178:181], v[96:99]
	v_mfma_f32_16x16x32_bf16 v[84:87], v[128:131], v[186:189], v[84:87]
	v_mfma_f32_16x16x32_bf16 v[80:83], v[152:155], v[186:189], v[80:83]
	v_mfma_f32_16x16x32_bf16 v[68:71], v[128:131], v[194:197], v[68:71]
	v_mfma_f32_16x16x32_bf16 v[64:67], v[152:155], v[194:197], v[64:67]
	v_mfma_f32_16x16x32_bf16 v[140:143], v[136:139], v[164:167], v[140:143]
	v_mfma_f32_16x16x32_bf16 v[132:135], v[156:159], v[164:167], v[132:135]
	v_mfma_f32_16x16x32_bf16 v[100:103], v[136:139], v[182:185], v[100:103]
	v_mfma_f32_16x16x32_bf16 v[96:99], v[156:159], v[182:185], v[96:99]
	v_mfma_f32_16x16x32_bf16 v[84:87], v[136:139], v[190:193], v[84:87]
	v_mfma_f32_16x16x32_bf16 v[80:83], v[156:159], v[190:193], v[80:83]
	v_mfma_f32_16x16x32_bf16 v[68:71], v[136:139], v[198:201], v[68:71]
	v_mfma_f32_16x16x32_bf16 v[64:67], v[156:159], v[198:201], v[64:67]
	s_setprio 2
	s_barrier
	s_mov_b32 m0, s61
	ds_read_b128 v[160:163], v175 offset:16384
	ds_read_b128 v[164:167], v175 offset:17408
	ds_read_b128 v[178:181], v175 offset:18432
	ds_read_b128 v[182:185], v175 offset:19456
	ds_read_b128 v[186:189], v175 offset:20480
	ds_read_b128 v[190:193], v175 offset:21504
	ds_read_b128 v[194:197], v175 offset:22528
	ds_read_b128 v[198:201], v175 offset:23552
	buffer_load_dwordx4 v170, s[48:51], s19 offen lds
	s_mov_b32 m0, s69
	s_add_i32 s21, s19, 0x80000
	buffer_load_dwordx4 v171, s[48:51], s19 offen lds
	s_mov_b32 m0, s70
	s_nop 0
	buffer_load_dwordx4 v170, s[48:51], s21 offen lds
	s_mov_b32 m0, s71
	s_nop 0
	buffer_load_dwordx4 v171, s[48:51], s21 offen lds
	s_mov_b32 m0, s59
	s_nop 0
	buffer_load_dwordx4 v172, s[44:47], s19 offen lds
	s_mov_b32 m0, s72
	s_nop 0
	buffer_load_dwordx4 v173, s[44:47], s19 offen lds
	s_waitcnt vmcnt(8)
	s_waitcnt lgkmcnt(0)
	s_barrier
	s_setprio 1
	s_waitcnt lgkmcnt(7)
	v_mfma_f32_16x16x32_bf16 v[60:63], v[104:107], v[160:163], v[60:63]
	v_mfma_f32_16x16x32_bf16 v[48:51], v[120:123], v[160:163], v[48:51]
	s_waitcnt lgkmcnt(5)
	v_mfma_f32_16x16x32_bf16 v[44:47], v[104:107], v[178:181], v[44:47]
	v_mfma_f32_16x16x32_bf16 v[40:43], v[120:123], v[178:181], v[40:43]
	s_waitcnt lgkmcnt(3)
	v_mfma_f32_16x16x32_bf16 v[28:31], v[104:107], v[186:189], v[28:31]
	v_mfma_f32_16x16x32_bf16 v[24:27], v[120:123], v[186:189], v[24:27]
	s_waitcnt lgkmcnt(1)
	v_mfma_f32_16x16x32_bf16 v[12:15], v[104:107], v[194:197], v[12:15]
	v_mfma_f32_16x16x32_bf16 v[8:11], v[120:123], v[194:197], v[8:11]
	v_mfma_f32_16x16x32_bf16 v[60:63], v[116:119], v[164:167], v[60:63]
	v_mfma_f32_16x16x32_bf16 v[48:51], v[124:127], v[164:167], v[48:51]
	v_mfma_f32_16x16x32_bf16 v[44:47], v[116:119], v[182:185], v[44:47]
	v_mfma_f32_16x16x32_bf16 v[40:43], v[124:127], v[182:185], v[40:43]
	v_mfma_f32_16x16x32_bf16 v[28:31], v[116:119], v[190:193], v[28:31]
	v_mfma_f32_16x16x32_bf16 v[24:27], v[124:127], v[190:193], v[24:27]
	s_waitcnt lgkmcnt(0)
	v_mfma_f32_16x16x32_bf16 v[12:15], v[116:119], v[198:201], v[12:15]
	v_mfma_f32_16x16x32_bf16 v[8:11], v[124:127], v[198:201], v[8:11]
	s_setprio 2
	s_setprio 1
	v_mfma_f32_16x16x32_bf16 v[56:59], v[128:131], v[160:163], v[56:59]
	v_mfma_f32_16x16x32_bf16 v[52:55], v[152:155], v[160:163], v[52:55]
	v_mfma_f32_16x16x32_bf16 v[36:39], v[128:131], v[178:181], v[36:39]
	v_mfma_f32_16x16x32_bf16 v[32:35], v[152:155], v[178:181], v[32:35]
	v_mfma_f32_16x16x32_bf16 v[20:23], v[128:131], v[186:189], v[20:23]
	v_mfma_f32_16x16x32_bf16 v[16:19], v[152:155], v[186:189], v[16:19]
	v_mfma_f32_16x16x32_bf16 v[4:7], v[128:131], v[194:197], v[4:7]
	v_mfma_f32_16x16x32_bf16 v[0:3], v[152:155], v[194:197], v[0:3]
	v_mfma_f32_16x16x32_bf16 v[56:59], v[136:139], v[164:167], v[56:59]
	v_mfma_f32_16x16x32_bf16 v[52:55], v[156:159], v[164:167], v[52:55]
	v_mfma_f32_16x16x32_bf16 v[36:39], v[136:139], v[182:185], v[36:39]
	v_mfma_f32_16x16x32_bf16 v[32:35], v[156:159], v[182:185], v[32:35]
	v_mfma_f32_16x16x32_bf16 v[20:23], v[136:139], v[190:193], v[20:23]
	v_mfma_f32_16x16x32_bf16 v[16:19], v[156:159], v[190:193], v[16:19]
	v_mfma_f32_16x16x32_bf16 v[4:7], v[136:139], v[198:201], v[4:7]
	v_mfma_f32_16x16x32_bf16 v[0:3], v[156:159], v[198:201], v[0:3]
	s_setprio 2
	s_barrier
	v_add_u32_e32 v124, 0x18000, v174
	v_add_u32_e32 v156, 0x1c000, v174
	ds_read_b128 v[104:107], v124
	ds_read_b128 v[116:119], v124 offset:1024
	ds_read_b128 v[120:123], v124 offset:2048
	ds_read_b128 v[124:127], v124 offset:3072
	ds_read_b128 v[128:131], v156
	ds_read_b128 v[136:139], v156 offset:1024
	ds_read_b128 v[152:155], v156 offset:2048
	ds_read_b128 v[156:159], v156 offset:3072
	s_mov_b32 m0, s73
	ds_read_b128 v[160:163], v175 offset:32768
	ds_read_b128 v[164:167], v175 offset:33792
	ds_read_b128 v[178:181], v175 offset:34816
	ds_read_b128 v[182:185], v175 offset:35840
	ds_read_b128 v[186:189], v175 offset:36864
	ds_read_b128 v[190:193], v175 offset:37888
	ds_read_b128 v[194:197], v175 offset:38912
	ds_read_b128 v[198:201], v175 offset:39936
	buffer_load_dwordx4 v172, s[44:47], s21 offen lds
	s_mov_b32 m0, s74
	s_nop 0
	buffer_load_dwordx4 v173, s[44:47], s21 offen lds
	s_waitcnt vmcnt(8)
	s_waitcnt lgkmcnt(0)
	s_barrier
	s_setprio 1
	s_waitcnt lgkmcnt(7)
	v_mfma_f32_16x16x32_bf16 v[148:151], v[104:107], v[160:163], v[148:151]
	v_mfma_f32_16x16x32_bf16 v[144:147], v[120:123], v[160:163], v[144:147]
	s_waitcnt lgkmcnt(5)
	v_mfma_f32_16x16x32_bf16 v[112:115], v[104:107], v[178:181], v[112:115]
	v_mfma_f32_16x16x32_bf16 v[108:111], v[120:123], v[178:181], v[108:111]
	s_waitcnt lgkmcnt(3)
	v_mfma_f32_16x16x32_bf16 v[92:95], v[104:107], v[186:189], v[92:95]
	v_mfma_f32_16x16x32_bf16 v[88:91], v[120:123], v[186:189], v[88:91]
	s_waitcnt lgkmcnt(1)
	v_mfma_f32_16x16x32_bf16 v[76:79], v[104:107], v[194:197], v[76:79]
	v_mfma_f32_16x16x32_bf16 v[72:75], v[120:123], v[194:197], v[72:75]
	v_mfma_f32_16x16x32_bf16 v[148:151], v[116:119], v[164:167], v[148:151]
	v_mfma_f32_16x16x32_bf16 v[144:147], v[124:127], v[164:167], v[144:147]
	v_mfma_f32_16x16x32_bf16 v[112:115], v[116:119], v[182:185], v[112:115]
	v_mfma_f32_16x16x32_bf16 v[108:111], v[124:127], v[182:185], v[108:111]
	v_mfma_f32_16x16x32_bf16 v[92:95], v[116:119], v[190:193], v[92:95]
	v_mfma_f32_16x16x32_bf16 v[88:91], v[124:127], v[190:193], v[88:91]
	s_waitcnt lgkmcnt(0)
	v_mfma_f32_16x16x32_bf16 v[76:79], v[116:119], v[198:201], v[76:79]
	v_mfma_f32_16x16x32_bf16 v[72:75], v[124:127], v[198:201], v[72:75]
	s_setprio 2
	s_setprio 1
	v_mfma_f32_16x16x32_bf16 v[140:143], v[128:131], v[160:163], v[140:143]
	v_mfma_f32_16x16x32_bf16 v[132:135], v[152:155], v[160:163], v[132:135]
	v_mfma_f32_16x16x32_bf16 v[100:103], v[128:131], v[178:181], v[100:103]
	v_mfma_f32_16x16x32_bf16 v[96:99], v[152:155], v[178:181], v[96:99]
	v_mfma_f32_16x16x32_bf16 v[84:87], v[128:131], v[186:189], v[84:87]
	v_mfma_f32_16x16x32_bf16 v[80:83], v[152:155], v[186:189], v[80:83]
	v_mfma_f32_16x16x32_bf16 v[68:71], v[128:131], v[194:197], v[68:71]
	v_mfma_f32_16x16x32_bf16 v[64:67], v[152:155], v[194:197], v[64:67]
	v_mfma_f32_16x16x32_bf16 v[140:143], v[136:139], v[164:167], v[140:143]
	v_mfma_f32_16x16x32_bf16 v[132:135], v[156:159], v[164:167], v[132:135]
	v_mfma_f32_16x16x32_bf16 v[100:103], v[136:139], v[182:185], v[100:103]
	v_mfma_f32_16x16x32_bf16 v[96:99], v[156:159], v[182:185], v[96:99]
	v_mfma_f32_16x16x32_bf16 v[84:87], v[136:139], v[190:193], v[84:87]
	v_mfma_f32_16x16x32_bf16 v[80:83], v[156:159], v[190:193], v[80:83]
	v_mfma_f32_16x16x32_bf16 v[68:71], v[136:139], v[198:201], v[68:71]
	v_mfma_f32_16x16x32_bf16 v[64:67], v[156:159], v[198:201], v[64:67]
	s_setprio 2
	s_barrier
	s_mov_b32 m0, s75
	s_or_b32 s21, s19, 0x80
	ds_read_b128 v[160:163], v175 offset:49152
	ds_read_b128 v[164:167], v175 offset:50176
	ds_read_b128 v[178:181], v175 offset:51200
	ds_read_b128 v[182:185], v175 offset:52224
	ds_read_b128 v[186:189], v175 offset:53248
	ds_read_b128 v[190:193], v175 offset:54272
	ds_read_b128 v[194:197], v175 offset:55296
	ds_read_b128 v[198:201], v175 offset:56320
	buffer_load_dwordx4 v170, s[48:51], s21 offen lds
	s_mov_b32 m0, s76
	s_add_i32 s19, s19, 0x80080
	buffer_load_dwordx4 v171, s[48:51], s21 offen lds
	s_mov_b32 m0, s83
	s_nop 0
	buffer_load_dwordx4 v170, s[48:51], s19 offen lds
	s_mov_b32 m0, s88
	s_nop 0
	buffer_load_dwordx4 v171, s[48:51], s19 offen lds
	s_mov_b32 m0, s77
	s_nop 0
	buffer_load_dwordx4 v172, s[44:47], s21 offen lds
	s_mov_b32 m0, s82
	s_nop 0
	buffer_load_dwordx4 v173, s[44:47], s21 offen lds
	s_waitcnt vmcnt(8)
	s_waitcnt lgkmcnt(0)
	s_barrier
	s_setprio 1
	s_waitcnt lgkmcnt(7)
	v_mfma_f32_16x16x32_bf16 v[60:63], v[104:107], v[160:163], v[60:63]
	v_mfma_f32_16x16x32_bf16 v[48:51], v[120:123], v[160:163], v[48:51]
	s_waitcnt lgkmcnt(5)
	v_mfma_f32_16x16x32_bf16 v[44:47], v[104:107], v[178:181], v[44:47]
	v_mfma_f32_16x16x32_bf16 v[40:43], v[120:123], v[178:181], v[40:43]
	s_waitcnt lgkmcnt(3)
	v_mfma_f32_16x16x32_bf16 v[28:31], v[104:107], v[186:189], v[28:31]
	v_mfma_f32_16x16x32_bf16 v[24:27], v[120:123], v[186:189], v[24:27]
	s_waitcnt lgkmcnt(1)
	v_mfma_f32_16x16x32_bf16 v[12:15], v[104:107], v[194:197], v[12:15]
	v_mfma_f32_16x16x32_bf16 v[8:11], v[120:123], v[194:197], v[8:11]
	v_mfma_f32_16x16x32_bf16 v[60:63], v[116:119], v[164:167], v[60:63]
	v_mfma_f32_16x16x32_bf16 v[48:51], v[124:127], v[164:167], v[48:51]
	v_mfma_f32_16x16x32_bf16 v[44:47], v[116:119], v[182:185], v[44:47]
	v_mfma_f32_16x16x32_bf16 v[40:43], v[124:127], v[182:185], v[40:43]
	v_mfma_f32_16x16x32_bf16 v[28:31], v[116:119], v[190:193], v[28:31]
	v_mfma_f32_16x16x32_bf16 v[24:27], v[124:127], v[190:193], v[24:27]
	s_waitcnt lgkmcnt(0)
	v_mfma_f32_16x16x32_bf16 v[12:15], v[116:119], v[198:201], v[12:15]
	v_mfma_f32_16x16x32_bf16 v[8:11], v[124:127], v[198:201], v[8:11]
	s_setprio 2
	s_setprio 1
	v_mfma_f32_16x16x32_bf16 v[56:59], v[128:131], v[160:163], v[56:59]
	v_mfma_f32_16x16x32_bf16 v[52:55], v[152:155], v[160:163], v[52:55]
	v_mfma_f32_16x16x32_bf16 v[36:39], v[128:131], v[178:181], v[36:39]
	v_mfma_f32_16x16x32_bf16 v[32:35], v[152:155], v[178:181], v[32:35]
	v_mfma_f32_16x16x32_bf16 v[20:23], v[128:131], v[186:189], v[20:23]
	v_mfma_f32_16x16x32_bf16 v[16:19], v[152:155], v[186:189], v[16:19]
	v_mfma_f32_16x16x32_bf16 v[4:7], v[128:131], v[194:197], v[4:7]
	v_mfma_f32_16x16x32_bf16 v[0:3], v[152:155], v[194:197], v[0:3]
	v_mfma_f32_16x16x32_bf16 v[56:59], v[136:139], v[164:167], v[56:59]
	v_mfma_f32_16x16x32_bf16 v[52:55], v[156:159], v[164:167], v[52:55]
	v_mfma_f32_16x16x32_bf16 v[36:39], v[136:139], v[182:185], v[36:39]
	v_mfma_f32_16x16x32_bf16 v[32:35], v[156:159], v[182:185], v[32:35]
	v_mfma_f32_16x16x32_bf16 v[20:23], v[136:139], v[190:193], v[20:23]
	v_mfma_f32_16x16x32_bf16 v[16:19], v[156:159], v[190:193], v[16:19]
	v_mfma_f32_16x16x32_bf16 v[4:7], v[136:139], v[198:201], v[4:7]
	v_mfma_f32_16x16x32_bf16 v[0:3], v[156:159], v[198:201], v[0:3]
	s_setprio 2
	s_barrier
	s_add_i32 s12, s12, 2
	s_addk_i32 s13, 0x100
	s_cmp_gt_u32 s12, 29
	s_cbranch_scc0 .LBB0_1539
	s_and_b64 vcc, exec, s[8:9]
	s_cbranch_vccz .LBB0_1542
	s_barrier

.LBB0_1723:
	s_nop 0
	v_add_u32_e32 v64, 0x10000, v138
	ds_read_b128 v[140:143], v64
	ds_read_b128 v[144:147], v64 offset:1024
	ds_read_b128 v[148:151], v64 offset:2048
	ds_read_b128 v[152:155], v64 offset:3072
	v_add_u32_e32 v64, 0x14000, v138
	ds_read_b128 v[156:159], v64
	ds_read_b128 v[160:163], v64 offset:1024
	ds_read_b128 v[164:167], v64 offset:2048
	ds_read_b128 v[168:171], v64 offset:3072
	s_cmp_eq_u32 s12, 12
	s_cselect_b64 s[4:5], -1, 0
	s_and_b64 s[48:49], s[4:5], exec
	s_cselect_b32 s31, 0, s13
	s_cselect_b32 s49, s35, s45
	s_cselect_b32 s48, s34, s44
	s_cselect_b32 s51, s43, s47
	s_cselect_b32 s50, s42, s46
	s_cselect_b32 s56, s62, s40
	s_cselect_b32 s57, s63, s41
	s_cselect_b32 s58, s64, s66
	s_cselect_b32 s59, s65, s67
	s_or_b32 vcc_lo, s31, 0x80
	s_add_i32 vcc_hi, s13, 0xffffff80
	ds_read_b128 v[198:201], v139
	ds_read_b128 v[202:205], v139 offset:1024
	ds_read_b128 v[206:209], v139 offset:2048
	ds_read_b128 v[210:213], v139 offset:3072
	ds_read_b128 v[214:217], v139 offset:4096
	ds_read_b128 v[218:221], v139 offset:5120
	ds_read_b128 v[222:225], v139 offset:6144
	ds_read_b128 v[226:229], v139 offset:7168
	v_mbcnt_lo_u32_b32 v64, -1, 0
	v_mbcnt_hi_u32_b32 v64, -1, v64
	s_mov_b32 m0, s93
	v_lshl_add_u32 v64, v64, 4, s71
	ds_read_b64 v[64:65], v64 offset:8
	s_waitcnt lgkmcnt(0)
	buffer_load_dwordx4 v64, s[44:47], vcc_hi offen lds
	s_mov_b32 m0, s96
	s_nop 0
	buffer_load_dwordx4 v65, s[44:47], vcc_hi offen lds
	s_waitcnt vmcnt(8)
	s_waitcnt lgkmcnt(0)
	s_barrier
	s_setprio 1
	v_mfma_scale_f32_16x16x128_f8f6f4 v[128:131], v[148:155], v[198:205], v[128:131], v230, v230 op_sel_hi:[0,0,0]
	v_mfma_scale_f32_16x16x128_f8f6f4 v[108:111], v[140:147], v[206:213], v[108:111], v230, v230 op_sel_hi:[0,0,0]
	v_mfma_scale_f32_16x16x128_f8f6f4 v[104:107], v[148:155], v[206:213], v[104:107], v230, v230 op_sel_hi:[0,0,0]
	v_mfma_scale_f32_16x16x128_f8f6f4 v[112:115], v[140:147], v[198:205], v[124:127], v230, v230 op_sel_hi:[0,0,0]
	v_mfma_scale_f32_16x16x128_f8f6f4 v[132:135], v[140:147], v[214:221], v[92:95], v230, v230 op_sel_hi:[0,0,0]
	v_mfma_scale_f32_16x16x128_f8f6f4 v[172:175], v[148:155], v[214:221], v[88:91], v230, v230 op_sel_hi:[0,0,0]
	v_mfma_scale_f32_16x16x128_f8f6f4 v[178:181], v[140:147], v[222:229], v[76:79], v230, v230 op_sel_hi:[0,0,0]
	v_mfma_scale_f32_16x16x128_f8f6f4 v[182:185], v[148:155], v[222:229], v[72:75], v230, v230 op_sel_hi:[0,0,0]
	s_setprio 2
	s_setprio 1
	v_mfma_scale_f32_16x16x128_f8f6f4 v[120:123], v[156:163], v[198:205], v[120:123], v230, v230 op_sel_hi:[0,0,0]
	v_mfma_scale_f32_16x16x128_f8f6f4 v[116:119], v[164:171], v[198:205], v[116:119], v230, v230 op_sel_hi:[0,0,0]
	v_mfma_scale_f32_16x16x128_f8f6f4 v[100:103], v[156:163], v[206:213], v[100:103], v230, v230 op_sel_hi:[0,0,0]
	v_mfma_scale_f32_16x16x128_f8f6f4 v[96:99], v[164:171], v[206:213], v[96:99], v230, v230 op_sel_hi:[0,0,0]
	v_mfma_scale_f32_16x16x128_f8f6f4 v[186:189], v[156:163], v[214:221], v[84:87], v230, v230 op_sel_hi:[0,0,0]
	v_mfma_scale_f32_16x16x128_f8f6f4 v[190:193], v[164:171], v[214:221], v[80:83], v230, v230 op_sel_hi:[0,0,0]
	v_mfma_scale_f32_16x16x128_f8f6f4 v[194:197], v[156:163], v[222:229], v[68:71], v230, v230 op_sel_hi:[0,0,0]
	v_mfma_scale_f32_16x16x128_f8f6f4 v[198:201], v[164:171], v[222:229], v[24:27], v230, v230 op_sel_hi:[0,0,0]
	s_setprio 2
	s_barrier
	s_mov_b32 m0, s74
	s_add_i32 vcc_hi, s31, 0x40000
	s_and_b64 s[4:5], s[38:39], s[4:5]
	ds_read_b128 v[64:67], v139 offset:16384
	ds_read_b128 v[68:71], v139 offset:17408
	ds_read_b128 v[72:75], v139 offset:18432
	ds_read_b128 v[76:79], v139 offset:19456
	ds_read_b128 v[80:83], v139 offset:20480
	ds_read_b128 v[84:87], v139 offset:21504
	ds_read_b128 v[88:91], v139 offset:22528
	ds_read_b128 v[92:95], v139 offset:23552
	buffer_load_dwordx4 v136, s[56:59], s31 offen lds
	s_mov_b32 m0, s75
	s_and_b64 s[4:5], s[4:5], exec
	buffer_load_dwordx4 v137, s[56:59], s31 offen lds
	s_mov_b32 m0, s76
	s_mov_b32 s4, 0x24000
	buffer_load_dwordx4 v136, s[56:59], vcc_hi offen lds
	s_mov_b32 m0, s77
	s_cselect_b32 s4, s4, 0x20500
	buffer_load_dwordx4 v137, s[56:59], vcc_hi offen lds
	v_mbcnt_lo_u32_b32 v24, -1, 0
	v_mbcnt_hi_u32_b32 v24, -1, v24
	s_add_i32 s4, s70, s4
	v_lshl_add_u32 v24, v24, 4, s4
	ds_read_b64 v[24:25], v24
	s_mov_b32 m0, s70
	s_waitcnt lgkmcnt(0)
	buffer_load_dwordx4 v24, s[48:51], s31 offen lds
	s_mov_b32 m0, s78
	s_nop 0
	buffer_load_dwordx4 v25, s[48:51], s31 offen lds
	s_waitcnt vmcnt(8)
	s_waitcnt lgkmcnt(0)
	s_barrier
	s_setprio 1
	v_mfma_scale_f32_16x16x128_f8f6f4 v[60:63], v[140:147], v[64:71], v[60:63], v230, v230 op_sel_hi:[0,0,0]
	v_mfma_scale_f32_16x16x128_f8f6f4 v[0:3], v[148:155], v[64:71], v[0:3], v230, v230 op_sel_hi:[0,0,0]
	v_mfma_scale_f32_16x16x128_f8f6f4 v[12:15], v[140:147], v[88:95], v[12:15], v230, v230 op_sel_hi:[0,0,0]
	v_mfma_scale_f32_16x16x128_f8f6f4 v[206:209], v[140:147], v[72:79], v[44:47], v230, v230 op_sel_hi:[0,0,0]
	v_mfma_scale_f32_16x16x128_f8f6f4 v[210:213], v[148:155], v[72:79], v[48:51], v230, v230 op_sel_hi:[0,0,0]
	v_mfma_scale_f32_16x16x128_f8f6f4 v[214:217], v[140:147], v[80:87], v[28:31], v230, v230 op_sel_hi:[0,0,0]
	v_mfma_scale_f32_16x16x128_f8f6f4 v[218:221], v[148:155], v[80:87], v[32:35], v230, v230 op_sel_hi:[0,0,0]
	v_mfma_scale_f32_16x16x128_f8f6f4 v[222:225], v[148:155], v[88:95], v[16:19], v230, v230 op_sel_hi:[0,0,0]
	s_setprio 2
	s_setprio 1
	v_mfma_scale_f32_16x16x128_f8f6f4 v[56:59], v[164:171], v[64:71], v[56:59], v230, v230 op_sel_hi:[0,0,0]
	v_mfma_scale_f32_16x16x128_f8f6f4 v[244:247], v[164:171], v[80:87], v[244:247], v230, v230 op_sel_hi:[0,0,0]
	v_mfma_scale_f32_16x16x128_f8f6f4 v[226:229], v[156:163], v[64:71], v[52:55], v230, v230 op_sel_hi:[0,0,0]
	v_mfma_scale_f32_16x16x128_f8f6f4 v[232:235], v[156:163], v[72:79], v[36:39], v230, v230 op_sel_hi:[0,0,0]
	v_mfma_scale_f32_16x16x128_f8f6f4 v[236:239], v[164:171], v[72:79], v[40:43], v230, v230 op_sel_hi:[0,0,0]
	v_mfma_scale_f32_16x16x128_f8f6f4 v[240:243], v[156:163], v[80:87], v[20:23], v230, v230 op_sel_hi:[0,0,0]
	v_mfma_scale_f32_16x16x128_f8f6f4 v[248:251], v[156:163], v[88:95], v[4:7], v230, v230 op_sel_hi:[0,0,0]
	v_mfma_scale_f32_16x16x128_f8f6f4 v[64:67], v[164:171], v[88:95], v[8:11], v230, v230 op_sel_hi:[0,0,0]
	s_setprio 2
	s_barrier
	s_nop 2
	v_add_u32_e32 v20, 0x18000, v138
	v_add_u32_e32 v24, 0x1c000, v138
	ds_read_b128 v[4:7], v20
	ds_read_b128 v[8:11], v20 offset:1024
	ds_read_b128 v[16:19], v20 offset:2048
	ds_read_b128 v[20:23], v20 offset:3072
	ds_read_b128 v[140:143], v24
	ds_read_b128 v[144:147], v24 offset:1024
	ds_read_b128 v[148:151], v24 offset:2048
	ds_read_b128 v[152:155], v24 offset:3072
	ds_read_b128 v[24:27], v139 offset:32768
	ds_read_b128 v[28:31], v139 offset:33792
	ds_read_b128 v[32:35], v139 offset:34816
	ds_read_b128 v[36:39], v139 offset:35840
	ds_read_b128 v[40:43], v139 offset:36864
	ds_read_b128 v[44:47], v139 offset:37888
	ds_read_b128 v[48:51], v139 offset:38912
	ds_read_b128 v[52:55], v139 offset:39936
	v_mbcnt_lo_u32_b32 v68, -1, 0
	v_mbcnt_hi_u32_b32 v68, -1, v68
	s_mov_b32 m0, s79
	v_lshl_add_u32 v68, v68, 4, s4
	ds_read_b64 v[68:69], v68 offset:8
	s_waitcnt lgkmcnt(0)
	buffer_load_dwordx4 v68, s[48:51], s31 offen lds
	s_mov_b32 m0, s80
	s_nop 0
	buffer_load_dwordx4 v69, s[48:51], s31 offen lds
	s_waitcnt vmcnt(8)
	s_waitcnt lgkmcnt(0)
	s_barrier
	s_setprio 1
	v_mfma_scale_f32_16x16x128_f8f6f4 v[124:127], v[4:11], v[24:31], v[112:115], v230, v230 op_sel_hi:[0,0,0]
	v_mfma_scale_f32_16x16x128_f8f6f4 v[128:131], v[16:23], v[24:31], v[128:131], v230, v230 op_sel_hi:[0,0,0]
	v_mfma_scale_f32_16x16x128_f8f6f4 v[108:111], v[4:11], v[32:39], v[108:111], v230, v230 op_sel_hi:[0,0,0]
	v_mfma_scale_f32_16x16x128_f8f6f4 v[104:107], v[16:23], v[32:39], v[104:107], v230, v230 op_sel_hi:[0,0,0]
	v_mfma_scale_f32_16x16x128_f8f6f4 v[92:95], v[4:11], v[40:47], v[132:135], v230, v230 op_sel_hi:[0,0,0]
	v_mfma_scale_f32_16x16x128_f8f6f4 v[88:91], v[16:23], v[40:47], v[172:175], v230, v230 op_sel_hi:[0,0,0]
	v_mfma_scale_f32_16x16x128_f8f6f4 v[76:79], v[4:11], v[48:55], v[178:181], v230, v230 op_sel_hi:[0,0,0]
	v_mfma_scale_f32_16x16x128_f8f6f4 v[72:75], v[16:23], v[48:55], v[182:185], v230, v230 op_sel_hi:[0,0,0]
	s_setprio 2
	s_setprio 1
	v_mfma_scale_f32_16x16x128_f8f6f4 v[120:123], v[140:147], v[24:31], v[120:123], v230, v230 op_sel_hi:[0,0,0]
	v_mfma_scale_f32_16x16x128_f8f6f4 v[116:119], v[148:155], v[24:31], v[116:119], v230, v230 op_sel_hi:[0,0,0]
	v_mfma_scale_f32_16x16x128_f8f6f4 v[100:103], v[140:147], v[32:39], v[100:103], v230, v230 op_sel_hi:[0,0,0]
	v_mfma_scale_f32_16x16x128_f8f6f4 v[96:99], v[148:155], v[32:39], v[96:99], v230, v230 op_sel_hi:[0,0,0]
	v_mfma_scale_f32_16x16x128_f8f6f4 v[84:87], v[140:147], v[40:47], v[186:189], v230, v230 op_sel_hi:[0,0,0]
	v_mfma_scale_f32_16x16x128_f8f6f4 v[80:83], v[148:155], v[40:47], v[190:193], v230, v230 op_sel_hi:[0,0,0]
	v_mfma_scale_f32_16x16x128_f8f6f4 v[68:71], v[140:147], v[48:55], v[194:197], v230, v230 op_sel_hi:[0,0,0]
	v_mfma_scale_f32_16x16x128_f8f6f4 v[24:27], v[148:155], v[48:55], v[198:201], v230, v230 op_sel_hi:[0,0,0]
	s_setprio 2
	s_barrier
	s_mov_b32 m0, s83
	ds_read_b128 v[36:39], v139 offset:49152
	ds_read_b128 v[40:43], v139 offset:50176
	ds_read_b128 v[156:159], v139 offset:51200
	ds_read_b128 v[160:163], v139 offset:52224
	ds_read_b128 v[164:167], v139 offset:53248
	ds_read_b128 v[168:171], v139 offset:54272
	ds_read_b128 v[198:201], v139 offset:55296
	ds_read_b128 v[202:205], v139 offset:56320
	buffer_load_dwordx4 v136, s[56:59], vcc_lo offen lds
	s_mov_b32 m0, s88
	s_add_i32 s31, s31, 0x40080
	buffer_load_dwordx4 v137, s[56:59], vcc_lo offen lds
	s_mov_b32 m0, s91
	s_nop 0
	buffer_load_dwordx4 v136, s[56:59], s31 offen lds
	s_mov_b32 m0, s92
	s_nop 0
	buffer_load_dwordx4 v137, s[56:59], s31 offen lds
	v_mbcnt_lo_u32_b32 v28, -1, 0
	v_mbcnt_hi_u32_b32 v28, -1, v28
	s_mov_b32 m0, s89
	v_lshl_add_u32 v28, v28, 4, s4
	ds_read_b64 v[28:29], v28
	s_waitcnt lgkmcnt(0)
	buffer_load_dwordx4 v28, s[48:51], vcc_lo offen lds
	s_mov_b32 m0, s90
	s_nop 0
	buffer_load_dwordx4 v29, s[48:51], vcc_lo offen lds
	s_waitcnt vmcnt(8)
	s_waitcnt lgkmcnt(0)
	s_barrier
	s_setprio 1
	v_mfma_scale_f32_16x16x128_f8f6f4 v[60:63], v[4:11], v[36:43], v[60:63], v230, v230 op_sel_hi:[0,0,0]
	v_mfma_scale_f32_16x16x128_f8f6f4 v[0:3], v[16:23], v[36:43], v[0:3], v230, v230 op_sel_hi:[0,0,0]
	v_mfma_scale_f32_16x16x128_f8f6f4 v[44:47], v[4:11], v[156:163], v[206:209], v230, v230 op_sel_hi:[0,0,0]
	v_mfma_scale_f32_16x16x128_f8f6f4 v[48:51], v[16:23], v[156:163], v[210:213], v230, v230 op_sel_hi:[0,0,0]
	v_mfma_scale_f32_16x16x128_f8f6f4 v[28:31], v[4:11], v[164:171], v[214:217], v230, v230 op_sel_hi:[0,0,0]
	v_mfma_scale_f32_16x16x128_f8f6f4 v[32:35], v[16:23], v[164:171], v[218:221], v230, v230 op_sel_hi:[0,0,0]
	v_mfma_scale_f32_16x16x128_f8f6f4 v[12:15], v[4:11], v[198:205], v[12:15], v230, v230 op_sel_hi:[0,0,0]
	v_mfma_scale_f32_16x16x128_f8f6f4 v[16:19], v[16:23], v[198:205], v[222:225], v230, v230 op_sel_hi:[0,0,0]
	s_setprio 2
	s_setprio 1
	v_mfma_scale_f32_16x16x128_f8f6f4 v[52:55], v[140:147], v[36:43], v[226:229], v230, v230 op_sel_hi:[0,0,0]
	v_mfma_scale_f32_16x16x128_f8f6f4 v[56:59], v[148:155], v[36:43], v[56:59], v230, v230 op_sel_hi:[0,0,0]
	v_mfma_scale_f32_16x16x128_f8f6f4 v[36:39], v[140:147], v[156:163], v[232:235], v230, v230 op_sel_hi:[0,0,0]
	v_mfma_scale_f32_16x16x128_f8f6f4 v[40:43], v[148:155], v[156:163], v[236:239], v230, v230 op_sel_hi:[0,0,0]
	v_mfma_scale_f32_16x16x128_f8f6f4 v[20:23], v[140:147], v[164:171], v[240:243], v230, v230 op_sel_hi:[0,0,0]
	v_mfma_scale_f32_16x16x128_f8f6f4 v[244:247], v[148:155], v[164:171], v[244:247], v230, v230 op_sel_hi:[0,0,0]
	v_mfma_scale_f32_16x16x128_f8f6f4 v[4:7], v[140:147], v[198:205], v[248:251], v230, v230 op_sel_hi:[0,0,0]
	v_mfma_scale_f32_16x16x128_f8f6f4 v[8:11], v[148:155], v[198:205], v[64:67], v230, v230 op_sel_hi:[0,0,0]
	s_setprio 2
	s_barrier
	s_add_i32 s12, s12, 2
	s_addk_i32 s13, 0x100
	s_cmp_gt_u32 s12, 13
	s_cbranch_scc0 .LBB0_1723
	s_mov_b64 s[4:5], 0
	s_and_b64 vcc, exec, s[38:39]
	s_cbranch_vccz .LBB0_1731
	v_readlane_b32 s4, v255, 9
	v_mov_b32_e32 v222, v176
	s_nop 0
	v_mov_b32_e32 v64, s4
	ds_read_b32 v64, v64
	s_add_i32 s4, s3, 2
	s_mul_i32 s3, s4, s72
	s_mul_hi_u32 s5, s4, s33
	s_add_i32 s5, s5, s3
	s_waitcnt lgkmcnt(0)
	v_readfirstlane_b32 s3, v64
	s_mul_i32 s4, s4, s33
	s_mul_i32 s31, s3, 44
	s_add_u32 s12, s4, s61
	s_addc_u32 s13, s5, s73
	s_ashr_i32 s38, s31, 31
	v_mov_b32_e32 v64, s31
	v_mov_b32_e32 v65, s38
	v_cmp_ge_i64_e32 vcc, s[12:13], v[64:65]
	s_mov_b64 s[4:5], 0
	s_cbranch_vccnz .LBB0_1732
	s_lshr_b32 s4, s38, 29
	s_add_i32 s4, s31, s4
	s_ashr_i32 s38, s4, 3
	s_and_b32 s4, s4, -8
	s_sub_i32 s39, s31, s4
	s_ashr_i32 s4, s12, 31
	s_lshr_b32 s4, s4, 29
	s_add_i32 s13, s12, s4
	s_and_b32 s4, s13, -8
	s_sub_i32 s12, s12, s4
	s_add_i32 s29, s38, 1
	s_cmp_ge_i32 s12, s39
	s_mov_b64 s[4:5], -1
	s_cbranch_scc0 .LBB0_1728
	s_sub_i32 s5, s12, s39
	s_mul_i32 s4, s29, s39
	s_mul_i32 s5, s5, s38
	s_add_i32 s31, s5, s4
	s_mov_b64 s[4:5], 0

.LBB0_1825:
	v_add_u32_e32 v128, 0x10000, v134
	ds_read_b128 v[136:139], v128
	ds_read_b128 v[140:143], v128 offset:1024
	ds_read_b128 v[144:147], v128 offset:2048
	ds_read_b128 v[148:151], v128 offset:3072
	v_add_u32_e32 v128, 0x14000, v134
	ds_read_b128 v[152:155], v128
	ds_read_b128 v[156:159], v128 offset:1024
	ds_read_b128 v[160:163], v128 offset:2048
	ds_read_b128 v[164:167], v128 offset:3072
	s_add_i32 s31, s13, 0xfff50080
	s_cmp_eq_u32 s12, 40
	s_cselect_b32 s45, s19, s41
	s_cselect_b32 s44, s18, s40
	s_cselect_b32 s47, s21, s43
	s_cselect_b32 s46, s20, s42
	s_cselect_b32 s31, 0, s31
	s_cselect_b32 s49, s23, s53
	s_cselect_b32 s48, s22, s52
	s_cselect_b32 s51, s29, s5
	s_cselect_b32 s50, s28, s4
	s_mov_b32 m0, s77
	ds_read_b128 v[168:171], v135
	ds_read_b128 v[172:175], v135 offset:1024
	ds_read_b128 v[198:201], v135 offset:2048
	ds_read_b128 v[202:205], v135 offset:3072
	ds_read_b128 v[206:209], v135 offset:4096
	ds_read_b128 v[210:213], v135 offset:5120
	ds_read_b128 v[214:217], v135 offset:6144
	ds_read_b128 v[218:221], v135 offset:7168
	buffer_load_dwordx4 v132, s[40:43], s13 offen lds
	s_mov_b32 m0, s79
	s_nop 0
	buffer_load_dwordx4 v133, s[40:43], s13 offen lds
	s_waitcnt vmcnt(8)
	s_waitcnt lgkmcnt(0)
	s_barrier
	s_setprio 1
	s_waitcnt lgkmcnt(6)
	v_mfma_scale_f32_16x16x128_f8f6f4 v[124:127], v[136:143], v[168:175], v[124:127], v230, v230 op_sel_hi:[0,0,0]
	v_mfma_scale_f32_16x16x128_f8f6f4 v[120:123], v[144:151], v[168:175], v[120:123], v230, v230 op_sel_hi:[0,0,0]
	s_waitcnt lgkmcnt(4)
	v_mfma_scale_f32_16x16x128_f8f6f4 v[108:111], v[136:143], v[198:205], v[108:111], v230, v230 op_sel_hi:[0,0,0]
	v_mfma_scale_f32_16x16x128_f8f6f4 v[104:107], v[144:151], v[198:205], v[104:107], v230, v230 op_sel_hi:[0,0,0]
	s_waitcnt lgkmcnt(2)
	v_mfma_scale_f32_16x16x128_f8f6f4 v[178:181], v[136:143], v[206:213], v[92:95], v230, v230 op_sel_hi:[0,0,0]
	v_mfma_scale_f32_16x16x128_f8f6f4 v[182:185], v[144:151], v[206:213], v[88:91], v230, v230 op_sel_hi:[0,0,0]
	s_waitcnt lgkmcnt(0)
	v_mfma_scale_f32_16x16x128_f8f6f4 v[186:189], v[136:143], v[214:221], v[76:79], v230, v230 op_sel_hi:[0,0,0]
	v_mfma_scale_f32_16x16x128_f8f6f4 v[190:193], v[144:151], v[214:221], v[72:75], v230, v230 op_sel_hi:[0,0,0]
	s_setprio 2
	s_setprio 1
	v_mfma_scale_f32_16x16x128_f8f6f4 v[116:119], v[152:159], v[168:175], v[116:119], v230, v230 op_sel_hi:[0,0,0]
	v_mfma_scale_f32_16x16x128_f8f6f4 v[112:115], v[160:167], v[168:175], v[112:115], v230, v230 op_sel_hi:[0,0,0]
	v_mfma_scale_f32_16x16x128_f8f6f4 v[100:103], v[152:159], v[198:205], v[100:103], v230, v230 op_sel_hi:[0,0,0]
	v_mfma_scale_f32_16x16x128_f8f6f4 v[96:99], v[160:167], v[198:205], v[96:99], v230, v230 op_sel_hi:[0,0,0]
	v_mfma_scale_f32_16x16x128_f8f6f4 v[168:171], v[152:159], v[206:213], v[84:87], v230, v230 op_sel_hi:[0,0,0]
	v_mfma_scale_f32_16x16x128_f8f6f4 v[172:175], v[160:167], v[206:213], v[80:83], v230, v230 op_sel_hi:[0,0,0]
	v_mfma_scale_f32_16x16x128_f8f6f4 v[194:197], v[152:159], v[214:221], v[68:71], v230, v230 op_sel_hi:[0,0,0]
	v_mfma_scale_f32_16x16x128_f8f6f4 v[198:201], v[160:167], v[214:221], v[64:67], v230, v230 op_sel_hi:[0,0,0]
	s_setprio 2
	s_barrier
	s_mov_b32 m0, s62
	s_nop 3
	ds_read_b128 v[64:67], v135 offset:16384
	ds_read_b128 v[68:71], v135 offset:17408
	ds_read_b128 v[72:75], v135 offset:18432
	ds_read_b128 v[76:79], v135 offset:19456
	ds_read_b128 v[80:83], v135 offset:20480
	ds_read_b128 v[84:87], v135 offset:21504
	ds_read_b128 v[88:91], v135 offset:22528
	ds_read_b128 v[92:95], v135 offset:23552
	buffer_load_dwordx4 v130, s[48:51], s31 offen lds
	s_mov_b32 m0, s63
	s_add_i32 s38, s31, 0xb0000
	buffer_load_dwordx4 v131, s[48:51], s31 offen lds
	s_mov_b32 m0, s64
	s_nop 0
	buffer_load_dwordx4 v130, s[48:51], s38 offen lds
	s_mov_b32 m0, s65
	s_nop 0
	buffer_load_dwordx4 v131, s[48:51], s38 offen lds
	s_mov_b32 m0, s61
	s_nop 0
	buffer_load_dwordx4 v132, s[44:47], s31 offen lds
	s_mov_b32 m0, s66
	s_nop 0
	buffer_load_dwordx4 v133, s[44:47], s31 offen lds
	s_waitcnt vmcnt(8)
	s_waitcnt lgkmcnt(0)
	s_barrier
	s_setprio 1
	s_waitcnt lgkmcnt(6)
	v_mfma_scale_f32_16x16x128_f8f6f4 v[60:63], v[136:143], v[64:71], v[60:63], v230, v230 op_sel_hi:[0,0,0]
	v_mfma_scale_f32_16x16x128_f8f6f4 v[0:3], v[144:151], v[64:71], v[0:3], v230, v230 op_sel_hi:[0,0,0]
	s_waitcnt lgkmcnt(4)
	v_mfma_scale_f32_16x16x128_f8f6f4 v[202:205], v[136:143], v[72:79], v[48:51], v230, v230 op_sel_hi:[0,0,0]
	v_mfma_scale_f32_16x16x128_f8f6f4 v[206:209], v[144:151], v[72:79], v[44:47], v230, v230 op_sel_hi:[0,0,0]
	s_waitcnt lgkmcnt(2)
	v_mfma_scale_f32_16x16x128_f8f6f4 v[210:213], v[136:143], v[80:87], v[32:35], v230, v230 op_sel_hi:[0,0,0]
	v_mfma_scale_f32_16x16x128_f8f6f4 v[214:217], v[144:151], v[80:87], v[28:31], v230, v230 op_sel_hi:[0,0,0]
	s_waitcnt lgkmcnt(0)
	v_mfma_scale_f32_16x16x128_f8f6f4 v[218:221], v[136:143], v[88:95], v[16:19], v230, v230 op_sel_hi:[0,0,0]
	v_mfma_scale_f32_16x16x128_f8f6f4 v[222:225], v[144:151], v[88:95], v[12:15], v230, v230 op_sel_hi:[0,0,0]
	s_setprio 2
	s_setprio 1
	v_mfma_scale_f32_16x16x128_f8f6f4 v[56:59], v[152:159], v[64:71], v[56:59], v230, v230 op_sel_hi:[0,0,0]
	v_mfma_scale_f32_16x16x128_f8f6f4 v[52:55], v[160:167], v[64:71], v[52:55], v230, v230 op_sel_hi:[0,0,0]
	v_mfma_scale_f32_16x16x128_f8f6f4 v[226:229], v[152:159], v[72:79], v[40:43], v230, v230 op_sel_hi:[0,0,0]
	v_mfma_scale_f32_16x16x128_f8f6f4 v[232:235], v[160:167], v[72:79], v[36:39], v230, v230 op_sel_hi:[0,0,0]
	v_mfma_scale_f32_16x16x128_f8f6f4 v[236:239], v[152:159], v[80:87], v[24:27], v230, v230 op_sel_hi:[0,0,0]
	v_mfma_scale_f32_16x16x128_f8f6f4 v[240:243], v[160:167], v[80:87], v[20:23], v230, v230 op_sel_hi:[0,0,0]
	v_mfma_scale_f32_16x16x128_f8f6f4 v[244:247], v[152:159], v[88:95], v[8:11], v230, v230 op_sel_hi:[0,0,0]
	v_mfma_scale_f32_16x16x128_f8f6f4 v[248:251], v[160:167], v[88:95], v[4:7], v230, v230 op_sel_hi:[0,0,0]
	s_setprio 2
	s_barrier
	v_add_u32_e32 v12, 0x18000, v134
	s_nop 3
	ds_read_b128 v[4:7], v12
	ds_read_b128 v[8:11], v12 offset:1024
	ds_read_b128 v[20:23], v12 offset:2048
	ds_read_b128 v[24:27], v12 offset:3072
	v_add_u32_e32 v12, 0x1c000, v134
	ds_read_b128 v[136:139], v12
	ds_read_b128 v[140:143], v12 offset:1024
	ds_read_b128 v[144:147], v12 offset:2048
	ds_read_b128 v[148:151], v12 offset:3072
	s_mov_b32 m0, s67
	ds_read_b128 v[12:15], v135 offset:32768
	ds_read_b128 v[16:19], v135 offset:33792
	ds_read_b128 v[28:31], v135 offset:34816
	ds_read_b128 v[32:35], v135 offset:35840
	ds_read_b128 v[36:39], v135 offset:36864
	ds_read_b128 v[40:43], v135 offset:37888
	ds_read_b128 v[44:47], v135 offset:38912
	ds_read_b128 v[48:51], v135 offset:39936
	buffer_load_dwordx4 v132, s[44:47], s38 offen lds
	s_mov_b32 m0, s68
	s_nop 0
	buffer_load_dwordx4 v133, s[44:47], s38 offen lds
	s_waitcnt vmcnt(8)
	s_waitcnt lgkmcnt(0)
	s_barrier
	s_setprio 1
	s_waitcnt lgkmcnt(6)
	v_mfma_scale_f32_16x16x128_f8f6f4 v[124:127], v[4:11], v[12:19], v[124:127], v230, v230 op_sel_hi:[0,0,0]
	v_mfma_scale_f32_16x16x128_f8f6f4 v[120:123], v[20:27], v[12:19], v[120:123], v230, v230 op_sel_hi:[0,0,0]
	s_waitcnt lgkmcnt(4)
	v_mfma_scale_f32_16x16x128_f8f6f4 v[108:111], v[4:11], v[28:35], v[108:111], v230, v230 op_sel_hi:[0,0,0]
	v_mfma_scale_f32_16x16x128_f8f6f4 v[104:107], v[20:27], v[28:35], v[104:107], v230, v230 op_sel_hi:[0,0,0]
	s_waitcnt lgkmcnt(2)
	v_mfma_scale_f32_16x16x128_f8f6f4 v[92:95], v[4:11], v[36:43], v[178:181], v230, v230 op_sel_hi:[0,0,0]
	v_mfma_scale_f32_16x16x128_f8f6f4 v[88:91], v[20:27], v[36:43], v[182:185], v230, v230 op_sel_hi:[0,0,0]
	s_waitcnt lgkmcnt(0)
	v_mfma_scale_f32_16x16x128_f8f6f4 v[76:79], v[4:11], v[44:51], v[186:189], v230, v230 op_sel_hi:[0,0,0]
	v_mfma_scale_f32_16x16x128_f8f6f4 v[72:75], v[20:27], v[44:51], v[190:193], v230, v230 op_sel_hi:[0,0,0]
	s_setprio 2
	s_setprio 1
	v_mfma_scale_f32_16x16x128_f8f6f4 v[116:119], v[136:143], v[12:19], v[116:119], v230, v230 op_sel_hi:[0,0,0]
	v_mfma_scale_f32_16x16x128_f8f6f4 v[112:115], v[144:151], v[12:19], v[112:115], v230, v230 op_sel_hi:[0,0,0]
	v_mfma_scale_f32_16x16x128_f8f6f4 v[100:103], v[136:143], v[28:35], v[100:103], v230, v230 op_sel_hi:[0,0,0]
	v_mfma_scale_f32_16x16x128_f8f6f4 v[96:99], v[144:151], v[28:35], v[96:99], v230, v230 op_sel_hi:[0,0,0]
	v_mfma_scale_f32_16x16x128_f8f6f4 v[84:87], v[136:143], v[36:43], v[168:171], v230, v230 op_sel_hi:[0,0,0]
	v_mfma_scale_f32_16x16x128_f8f6f4 v[80:83], v[144:151], v[36:43], v[172:175], v230, v230 op_sel_hi:[0,0,0]
	v_mfma_scale_f32_16x16x128_f8f6f4 v[68:71], v[136:143], v[44:51], v[194:197], v230, v230 op_sel_hi:[0,0,0]
	v_mfma_scale_f32_16x16x128_f8f6f4 v[64:67], v[144:151], v[44:51], v[198:201], v230, v230 op_sel_hi:[0,0,0]
	s_setprio 2
	s_barrier
	s_mov_b32 m0, s69
	s_or_b32 s38, s31, 0x80
	ds_read_b128 v[36:39], v135 offset:49152
	ds_read_b128 v[40:43], v135 offset:50176
	ds_read_b128 v[152:155], v135 offset:51200
	ds_read_b128 v[156:159], v135 offset:52224
	ds_read_b128 v[160:163], v135 offset:53248
	ds_read_b128 v[164:167], v135 offset:54272
	ds_read_b128 v[168:171], v135 offset:55296
	ds_read_b128 v[172:175], v135 offset:56320
	buffer_load_dwordx4 v130, s[48:51], s38 offen lds
	s_mov_b32 m0, s70
	s_add_i32 s31, s31, 0xb0080
	buffer_load_dwordx4 v131, s[48:51], s38 offen lds
	s_mov_b32 m0, s73
	s_nop 0
	buffer_load_dwordx4 v130, s[48:51], s31 offen lds
	s_mov_b32 m0, s74
	s_nop 0
	buffer_load_dwordx4 v131, s[48:51], s31 offen lds
	s_mov_b32 m0, s71
	s_nop 0
	buffer_load_dwordx4 v132, s[44:47], s38 offen lds
	s_mov_b32 m0, s72
	s_nop 0
	buffer_load_dwordx4 v133, s[44:47], s38 offen lds
	s_waitcnt vmcnt(8)
	s_waitcnt lgkmcnt(0)
	s_barrier
	s_setprio 1
	s_waitcnt lgkmcnt(6)
	v_mfma_scale_f32_16x16x128_f8f6f4 v[60:63], v[4:11], v[36:43], v[60:63], v230, v230 op_sel_hi:[0,0,0]
	v_mfma_scale_f32_16x16x128_f8f6f4 v[0:3], v[20:27], v[36:43], v[0:3], v230, v230 op_sel_hi:[0,0,0]
	s_waitcnt lgkmcnt(4)
	v_mfma_scale_f32_16x16x128_f8f6f4 v[48:51], v[4:11], v[152:159], v[202:205], v230, v230 op_sel_hi:[0,0,0]
	v_mfma_scale_f32_16x16x128_f8f6f4 v[44:47], v[20:27], v[152:159], v[206:209], v230, v230 op_sel_hi:[0,0,0]
	s_waitcnt lgkmcnt(2)
	v_mfma_scale_f32_16x16x128_f8f6f4 v[32:35], v[4:11], v[160:167], v[210:213], v230, v230 op_sel_hi:[0,0,0]
	v_mfma_scale_f32_16x16x128_f8f6f4 v[28:31], v[20:27], v[160:167], v[214:217], v230, v230 op_sel_hi:[0,0,0]
	s_waitcnt lgkmcnt(0)
	v_mfma_scale_f32_16x16x128_f8f6f4 v[16:19], v[4:11], v[168:175], v[218:221], v230, v230 op_sel_hi:[0,0,0]
	v_mfma_scale_f32_16x16x128_f8f6f4 v[12:15], v[20:27], v[168:175], v[222:225], v230, v230 op_sel_hi:[0,0,0]
	s_setprio 2
	s_setprio 1
	v_mfma_scale_f32_16x16x128_f8f6f4 v[56:59], v[136:143], v[36:43], v[56:59], v230, v230 op_sel_hi:[0,0,0]
	v_mfma_scale_f32_16x16x128_f8f6f4 v[52:55], v[144:151], v[36:43], v[52:55], v230, v230 op_sel_hi:[0,0,0]
	v_mfma_scale_f32_16x16x128_f8f6f4 v[40:43], v[136:143], v[152:159], v[226:229], v230, v230 op_sel_hi:[0,0,0]
	v_mfma_scale_f32_16x16x128_f8f6f4 v[36:39], v[144:151], v[152:159], v[232:235], v230, v230 op_sel_hi:[0,0,0]
	v_mfma_scale_f32_16x16x128_f8f6f4 v[24:27], v[136:143], v[160:167], v[236:239], v230, v230 op_sel_hi:[0,0,0]
	v_mfma_scale_f32_16x16x128_f8f6f4 v[20:23], v[144:151], v[160:167], v[240:243], v230, v230 op_sel_hi:[0,0,0]
	v_mfma_scale_f32_16x16x128_f8f6f4 v[8:11], v[136:143], v[168:175], v[244:247], v230, v230 op_sel_hi:[0,0,0]
	v_mfma_scale_f32_16x16x128_f8f6f4 v[4:7], v[144:151], v[168:175], v[248:251], v230, v230 op_sel_hi:[0,0,0]
	s_setprio 2
	s_barrier
	s_add_i32 s12, s12, 2
	s_addk_i32 s13, 0x100
	s_cmp_gt_u32 s12, 41
	s_cbranch_scc0 .LBB0_1825
	s_and_b64 vcc, exec, s[8:9]
	s_cbranch_vccz .LBB0_1828
	s_barrier

.LBB0_1950:
	v_add_u32_e32 v132, 0x10000, v138
	ds_read_b128 v[128:131], v132
	ds_read_b128 v[140:143], v132 offset:1024
	ds_read_b128 v[144:147], v132 offset:2048
	ds_read_b128 v[148:151], v132 offset:3072
	v_add_u32_e32 v132, 0x14000, v138
	ds_read_b128 v[152:155], v132
	ds_read_b128 v[156:159], v132 offset:1024
	ds_read_b128 v[160:163], v132 offset:2048
	ds_read_b128 v[164:167], v132 offset:3072
	s_add_i32 s48, s29, 0xfff80080
	s_cmp_eq_u32 s23, 28
	s_cselect_b32 s41, s31, s45
	s_cselect_b32 s40, s30, s44
	s_cselect_b32 s43, s35, s47
	s_cselect_b32 s42, s34, s46
	s_cselect_b32 s93, 0, s48
	s_cselect_b32 s49, s57, s53
	s_cselect_b32 s48, s56, s52
	s_cselect_b32 s51, s59, s13
	s_cselect_b32 s50, s58, s12
	s_mov_b32 m0, s88
	ds_read_b128 v[168:171], v139
	ds_read_b128 v[172:175], v139 offset:1024
	ds_read_b128 v[178:181], v139 offset:2048
	ds_read_b128 v[182:185], v139 offset:3072
	ds_read_b128 v[186:189], v139 offset:4096
	ds_read_b128 v[190:193], v139 offset:5120
	ds_read_b128 v[194:197], v139 offset:6144
	ds_read_b128 v[198:201], v139 offset:7168
	buffer_load_dwordx4 v136, s[44:47], s29 offen lds
	s_mov_b32 m0, s90
	s_nop 0
	buffer_load_dwordx4 v137, s[44:47], s29 offen lds
	s_waitcnt vmcnt(8)
	s_waitcnt lgkmcnt(0)
	s_barrier
	s_setprio 1
	s_waitcnt lgkmcnt(7)
	v_mfma_f32_16x16x32_bf16 v[124:127], v[128:131], v[168:171], v[124:127]
	v_mfma_f32_16x16x32_bf16 v[120:123], v[144:147], v[168:171], v[120:123]
	s_waitcnt lgkmcnt(5)
	v_mfma_f32_16x16x32_bf16 v[108:111], v[128:131], v[178:181], v[108:111]
	v_mfma_f32_16x16x32_bf16 v[104:107], v[144:147], v[178:181], v[104:107]
	s_waitcnt lgkmcnt(3)
	v_mfma_f32_16x16x32_bf16 v[92:95], v[128:131], v[186:189], v[92:95]
	v_mfma_f32_16x16x32_bf16 v[88:91], v[144:147], v[186:189], v[88:91]
	s_waitcnt lgkmcnt(1)
	v_mfma_f32_16x16x32_bf16 v[76:79], v[128:131], v[194:197], v[76:79]
	v_mfma_f32_16x16x32_bf16 v[72:75], v[144:147], v[194:197], v[72:75]
	v_mfma_f32_16x16x32_bf16 v[124:127], v[140:143], v[172:175], v[124:127]
	v_mfma_f32_16x16x32_bf16 v[120:123], v[148:151], v[172:175], v[120:123]
	v_mfma_f32_16x16x32_bf16 v[108:111], v[140:143], v[182:185], v[108:111]
	v_mfma_f32_16x16x32_bf16 v[104:107], v[148:151], v[182:185], v[104:107]
	v_mfma_f32_16x16x32_bf16 v[92:95], v[140:143], v[190:193], v[92:95]
	v_mfma_f32_16x16x32_bf16 v[88:91], v[148:151], v[190:193], v[88:91]
	s_waitcnt lgkmcnt(0)
	v_mfma_f32_16x16x32_bf16 v[76:79], v[140:143], v[198:201], v[76:79]
	v_mfma_f32_16x16x32_bf16 v[72:75], v[148:151], v[198:201], v[72:75]
	s_setprio 2
	s_setprio 1
	v_mfma_f32_16x16x32_bf16 v[116:119], v[152:155], v[168:171], v[116:119]
	v_mfma_f32_16x16x32_bf16 v[112:115], v[160:163], v[168:171], v[112:115]
	v_mfma_f32_16x16x32_bf16 v[100:103], v[152:155], v[178:181], v[100:103]
	v_mfma_f32_16x16x32_bf16 v[96:99], v[160:163], v[178:181], v[96:99]
	v_mfma_f32_16x16x32_bf16 v[84:87], v[152:155], v[186:189], v[84:87]
	v_mfma_f32_16x16x32_bf16 v[80:83], v[160:163], v[186:189], v[80:83]
	v_mfma_f32_16x16x32_bf16 v[68:71], v[152:155], v[194:197], v[68:71]
	v_mfma_f32_16x16x32_bf16 v[64:67], v[160:163], v[194:197], v[64:67]
	v_mfma_f32_16x16x32_bf16 v[116:119], v[156:159], v[172:175], v[116:119]
	v_mfma_f32_16x16x32_bf16 v[112:115], v[164:167], v[172:175], v[112:115]
	v_mfma_f32_16x16x32_bf16 v[100:103], v[156:159], v[182:185], v[100:103]
	v_mfma_f32_16x16x32_bf16 v[96:99], v[164:167], v[182:185], v[96:99]
	v_mfma_f32_16x16x32_bf16 v[84:87], v[156:159], v[190:193], v[84:87]
	v_mfma_f32_16x16x32_bf16 v[80:83], v[164:167], v[190:193], v[80:83]
	v_mfma_f32_16x16x32_bf16 v[68:71], v[156:159], v[198:201], v[68:71]
	v_mfma_f32_16x16x32_bf16 v[64:67], v[164:167], v[198:201], v[64:67]
	s_setprio 2
	s_barrier
	s_mov_b32 m0, s69
	ds_read_b128 v[168:171], v139 offset:16384
	ds_read_b128 v[172:175], v139 offset:17408
	ds_read_b128 v[178:181], v139 offset:18432
	ds_read_b128 v[182:185], v139 offset:19456
	ds_read_b128 v[186:189], v139 offset:20480
	ds_read_b128 v[190:193], v139 offset:21504
	ds_read_b128 v[194:197], v139 offset:22528
	ds_read_b128 v[198:201], v139 offset:23552
	buffer_load_dwordx4 v134, s[48:51], s93 offen lds
	s_mov_b32 m0, s70
	s_add_i32 s94, s93, 0x80000
	buffer_load_dwordx4 v135, s[48:51], s93 offen lds
	s_mov_b32 m0, s71
	s_nop 0
	buffer_load_dwordx4 v134, s[48:51], s94 offen lds
	s_mov_b32 m0, s72
	s_nop 0
	buffer_load_dwordx4 v135, s[48:51], s94 offen lds
	s_mov_b32 m0, s68
	s_nop 0
	buffer_load_dwordx4 v136, s[40:43], s93 offen lds
	s_mov_b32 m0, s73
	s_nop 0
	buffer_load_dwordx4 v137, s[40:43], s93 offen lds
	s_waitcnt vmcnt(8)
	s_waitcnt lgkmcnt(0)
	s_barrier
	s_setprio 1
	s_waitcnt lgkmcnt(7)
	v_mfma_f32_16x16x32_bf16 v[60:63], v[128:131], v[168:171], v[60:63]
	v_mfma_f32_16x16x32_bf16 v[0:3], v[144:147], v[168:171], v[0:3]
	s_waitcnt lgkmcnt(5)
	v_mfma_f32_16x16x32_bf16 v[44:47], v[128:131], v[178:181], v[44:47]
	v_mfma_f32_16x16x32_bf16 v[48:51], v[144:147], v[178:181], v[48:51]
	s_waitcnt lgkmcnt(3)
	v_mfma_f32_16x16x32_bf16 v[28:31], v[128:131], v[186:189], v[28:31]
	v_mfma_f32_16x16x32_bf16 v[32:35], v[144:147], v[186:189], v[32:35]
	s_waitcnt lgkmcnt(1)
	v_mfma_f32_16x16x32_bf16 v[12:15], v[128:131], v[194:197], v[12:15]
	v_mfma_f32_16x16x32_bf16 v[16:19], v[144:147], v[194:197], v[16:19]
	v_mfma_f32_16x16x32_bf16 v[60:63], v[140:143], v[172:175], v[60:63]
	v_mfma_f32_16x16x32_bf16 v[0:3], v[148:151], v[172:175], v[0:3]
	v_mfma_f32_16x16x32_bf16 v[44:47], v[140:143], v[182:185], v[44:47]
	v_mfma_f32_16x16x32_bf16 v[48:51], v[148:151], v[182:185], v[48:51]
	v_mfma_f32_16x16x32_bf16 v[28:31], v[140:143], v[190:193], v[28:31]
	v_mfma_f32_16x16x32_bf16 v[32:35], v[148:151], v[190:193], v[32:35]
	s_waitcnt lgkmcnt(0)
	v_mfma_f32_16x16x32_bf16 v[12:15], v[140:143], v[198:201], v[12:15]
	v_mfma_f32_16x16x32_bf16 v[16:19], v[148:151], v[198:201], v[16:19]
	s_setprio 2
	s_setprio 1
	v_mfma_f32_16x16x32_bf16 v[52:55], v[152:155], v[168:171], v[52:55]
	v_mfma_f32_16x16x32_bf16 v[56:59], v[160:163], v[168:171], v[56:59]
	v_mfma_f32_16x16x32_bf16 v[36:39], v[152:155], v[178:181], v[36:39]
	v_mfma_f32_16x16x32_bf16 v[40:43], v[160:163], v[178:181], v[40:43]
	v_mfma_f32_16x16x32_bf16 v[20:23], v[152:155], v[186:189], v[20:23]
	v_mfma_f32_16x16x32_bf16 v[24:27], v[160:163], v[186:189], v[24:27]
	v_mfma_f32_16x16x32_bf16 v[4:7], v[152:155], v[194:197], v[4:7]
	v_mfma_f32_16x16x32_bf16 v[8:11], v[160:163], v[194:197], v[8:11]
	v_mfma_f32_16x16x32_bf16 v[52:55], v[156:159], v[172:175], v[52:55]
	v_mfma_f32_16x16x32_bf16 v[56:59], v[164:167], v[172:175], v[56:59]
	v_mfma_f32_16x16x32_bf16 v[36:39], v[156:159], v[182:185], v[36:39]
	v_mfma_f32_16x16x32_bf16 v[40:43], v[164:167], v[182:185], v[40:43]
	v_mfma_f32_16x16x32_bf16 v[20:23], v[156:159], v[190:193], v[20:23]
	v_mfma_f32_16x16x32_bf16 v[24:27], v[164:167], v[190:193], v[24:27]
	v_mfma_f32_16x16x32_bf16 v[4:7], v[156:159], v[198:201], v[4:7]
	v_mfma_f32_16x16x32_bf16 v[8:11], v[164:167], v[198:201], v[8:11]
	s_setprio 2
	s_barrier
	v_add_u32_e32 v132, 0x18000, v138
	ds_read_b128 v[128:131], v132
	ds_read_b128 v[140:143], v132 offset:1024
	ds_read_b128 v[144:147], v132 offset:2048
	ds_read_b128 v[148:151], v132 offset:3072
	v_add_u32_e32 v132, 0x1c000, v138
	ds_read_b128 v[152:155], v132
	ds_read_b128 v[156:159], v132 offset:1024
	ds_read_b128 v[160:163], v132 offset:2048
	ds_read_b128 v[164:167], v132 offset:3072
	s_mov_b32 m0, s74
	ds_read_b128 v[168:171], v139 offset:32768
	ds_read_b128 v[172:175], v139 offset:33792
	ds_read_b128 v[178:181], v139 offset:34816
	ds_read_b128 v[182:185], v139 offset:35840
	ds_read_b128 v[186:189], v139 offset:36864
	ds_read_b128 v[190:193], v139 offset:37888
	ds_read_b128 v[194:197], v139 offset:38912
	ds_read_b128 v[198:201], v139 offset:39936
	buffer_load_dwordx4 v136, s[40:43], s94 offen lds
	s_mov_b32 m0, s75
	s_nop 0
	buffer_load_dwordx4 v137, s[40:43], s94 offen lds
	s_waitcnt vmcnt(8)
	s_waitcnt lgkmcnt(0)
	s_barrier
	s_setprio 1
	s_waitcnt lgkmcnt(7)
	v_mfma_f32_16x16x32_bf16 v[124:127], v[128:131], v[168:171], v[124:127]
	v_mfma_f32_16x16x32_bf16 v[120:123], v[144:147], v[168:171], v[120:123]
	s_waitcnt lgkmcnt(5)
	v_mfma_f32_16x16x32_bf16 v[108:111], v[128:131], v[178:181], v[108:111]
	v_mfma_f32_16x16x32_bf16 v[104:107], v[144:147], v[178:181], v[104:107]
	s_waitcnt lgkmcnt(3)
	v_mfma_f32_16x16x32_bf16 v[92:95], v[128:131], v[186:189], v[92:95]
	v_mfma_f32_16x16x32_bf16 v[88:91], v[144:147], v[186:189], v[88:91]
	s_waitcnt lgkmcnt(1)
	v_mfma_f32_16x16x32_bf16 v[76:79], v[128:131], v[194:197], v[76:79]
	v_mfma_f32_16x16x32_bf16 v[72:75], v[144:147], v[194:197], v[72:75]
	v_mfma_f32_16x16x32_bf16 v[124:127], v[140:143], v[172:175], v[124:127]
	v_mfma_f32_16x16x32_bf16 v[120:123], v[148:151], v[172:175], v[120:123]
	v_mfma_f32_16x16x32_bf16 v[108:111], v[140:143], v[182:185], v[108:111]
	v_mfma_f32_16x16x32_bf16 v[104:107], v[148:151], v[182:185], v[104:107]
	v_mfma_f32_16x16x32_bf16 v[92:95], v[140:143], v[190:193], v[92:95]
	v_mfma_f32_16x16x32_bf16 v[88:91], v[148:151], v[190:193], v[88:91]
	s_waitcnt lgkmcnt(0)
	v_mfma_f32_16x16x32_bf16 v[76:79], v[140:143], v[198:201], v[76:79]
	v_mfma_f32_16x16x32_bf16 v[72:75], v[148:151], v[198:201], v[72:75]
	s_setprio 2
	s_setprio 1
	v_mfma_f32_16x16x32_bf16 v[116:119], v[152:155], v[168:171], v[116:119]
	v_mfma_f32_16x16x32_bf16 v[112:115], v[160:163], v[168:171], v[112:115]
	v_mfma_f32_16x16x32_bf16 v[100:103], v[152:155], v[178:181], v[100:103]
	v_mfma_f32_16x16x32_bf16 v[96:99], v[160:163], v[178:181], v[96:99]
	v_mfma_f32_16x16x32_bf16 v[84:87], v[152:155], v[186:189], v[84:87]
	v_mfma_f32_16x16x32_bf16 v[80:83], v[160:163], v[186:189], v[80:83]
	v_mfma_f32_16x16x32_bf16 v[68:71], v[152:155], v[194:197], v[68:71]
	v_mfma_f32_16x16x32_bf16 v[64:67], v[160:163], v[194:197], v[64:67]
	v_mfma_f32_16x16x32_bf16 v[116:119], v[156:159], v[172:175], v[116:119]
	v_mfma_f32_16x16x32_bf16 v[112:115], v[164:167], v[172:175], v[112:115]
	v_mfma_f32_16x16x32_bf16 v[100:103], v[156:159], v[182:185], v[100:103]
	v_mfma_f32_16x16x32_bf16 v[96:99], v[164:167], v[182:185], v[96:99]
	v_mfma_f32_16x16x32_bf16 v[84:87], v[156:159], v[190:193], v[84:87]
	v_mfma_f32_16x16x32_bf16 v[80:83], v[164:167], v[190:193], v[80:83]
	v_mfma_f32_16x16x32_bf16 v[68:71], v[156:159], v[198:201], v[68:71]
	v_mfma_f32_16x16x32_bf16 v[64:67], v[164:167], v[198:201], v[64:67]
	s_setprio 2
	s_barrier
	s_mov_b32 m0, s76
	s_or_b32 s94, s93, 0x80
	ds_read_b128 v[168:171], v139 offset:49152
	ds_read_b128 v[172:175], v139 offset:50176
	ds_read_b128 v[178:181], v139 offset:51200
	ds_read_b128 v[182:185], v139 offset:52224
	ds_read_b128 v[186:189], v139 offset:53248
	ds_read_b128 v[190:193], v139 offset:54272
	ds_read_b128 v[194:197], v139 offset:55296
	ds_read_b128 v[198:201], v139 offset:56320
	buffer_load_dwordx4 v134, s[48:51], s94 offen lds
	s_mov_b32 m0, s77
	s_add_i32 s93, s93, 0x80080
	buffer_load_dwordx4 v135, s[48:51], s94 offen lds
	s_mov_b32 m0, s80
	s_nop 0
	buffer_load_dwordx4 v134, s[48:51], s93 offen lds
	s_mov_b32 m0, s82
	s_nop 0
	buffer_load_dwordx4 v135, s[48:51], s93 offen lds
	s_mov_b32 m0, s78
	s_nop 0
	buffer_load_dwordx4 v136, s[40:43], s94 offen lds
	s_mov_b32 m0, s79
	s_nop 0
	buffer_load_dwordx4 v137, s[40:43], s94 offen lds
	s_waitcnt vmcnt(8)
	s_waitcnt lgkmcnt(0)
	s_barrier
	s_setprio 1
	s_waitcnt lgkmcnt(7)
	v_mfma_f32_16x16x32_bf16 v[60:63], v[128:131], v[168:171], v[60:63]
	v_mfma_f32_16x16x32_bf16 v[0:3], v[144:147], v[168:171], v[0:3]
	s_waitcnt lgkmcnt(5)
	v_mfma_f32_16x16x32_bf16 v[44:47], v[128:131], v[178:181], v[44:47]
	v_mfma_f32_16x16x32_bf16 v[48:51], v[144:147], v[178:181], v[48:51]
	s_waitcnt lgkmcnt(3)
	v_mfma_f32_16x16x32_bf16 v[28:31], v[128:131], v[186:189], v[28:31]
	v_mfma_f32_16x16x32_bf16 v[32:35], v[144:147], v[186:189], v[32:35]
	s_waitcnt lgkmcnt(1)
	v_mfma_f32_16x16x32_bf16 v[12:15], v[128:131], v[194:197], v[12:15]
	v_mfma_f32_16x16x32_bf16 v[16:19], v[144:147], v[194:197], v[16:19]
	v_mfma_f32_16x16x32_bf16 v[60:63], v[140:143], v[172:175], v[60:63]
	v_mfma_f32_16x16x32_bf16 v[0:3], v[148:151], v[172:175], v[0:3]
	v_mfma_f32_16x16x32_bf16 v[44:47], v[140:143], v[182:185], v[44:47]
	v_mfma_f32_16x16x32_bf16 v[48:51], v[148:151], v[182:185], v[48:51]
	v_mfma_f32_16x16x32_bf16 v[28:31], v[140:143], v[190:193], v[28:31]
	v_mfma_f32_16x16x32_bf16 v[32:35], v[148:151], v[190:193], v[32:35]
	s_waitcnt lgkmcnt(0)
	v_mfma_f32_16x16x32_bf16 v[12:15], v[140:143], v[198:201], v[12:15]
	v_mfma_f32_16x16x32_bf16 v[16:19], v[148:151], v[198:201], v[16:19]
	s_setprio 2
	s_setprio 1
	v_mfma_f32_16x16x32_bf16 v[52:55], v[152:155], v[168:171], v[52:55]
	v_mfma_f32_16x16x32_bf16 v[56:59], v[160:163], v[168:171], v[56:59]
	v_mfma_f32_16x16x32_bf16 v[36:39], v[152:155], v[178:181], v[36:39]
	v_mfma_f32_16x16x32_bf16 v[40:43], v[160:163], v[178:181], v[40:43]
	v_mfma_f32_16x16x32_bf16 v[20:23], v[152:155], v[186:189], v[20:23]
	v_mfma_f32_16x16x32_bf16 v[24:27], v[160:163], v[186:189], v[24:27]
	v_mfma_f32_16x16x32_bf16 v[4:7], v[152:155], v[194:197], v[4:7]
	v_mfma_f32_16x16x32_bf16 v[8:11], v[160:163], v[194:197], v[8:11]
	v_mfma_f32_16x16x32_bf16 v[52:55], v[156:159], v[172:175], v[52:55]
	v_mfma_f32_16x16x32_bf16 v[56:59], v[164:167], v[172:175], v[56:59]
	v_mfma_f32_16x16x32_bf16 v[36:39], v[156:159], v[182:185], v[36:39]
	v_mfma_f32_16x16x32_bf16 v[40:43], v[164:167], v[182:185], v[40:43]
	v_mfma_f32_16x16x32_bf16 v[20:23], v[156:159], v[190:193], v[20:23]
	v_mfma_f32_16x16x32_bf16 v[24:27], v[164:167], v[190:193], v[24:27]
	v_mfma_f32_16x16x32_bf16 v[4:7], v[156:159], v[198:201], v[4:7]
	v_mfma_f32_16x16x32_bf16 v[8:11], v[164:167], v[198:201], v[8:11]
	s_setprio 2
	s_barrier
	s_add_i32 s23, s23, 2
	s_addk_i32 s29, 0x100
	s_cmp_gt_u32 s23, 29
	s_cbranch_scc0 .LBB0_1950
	s_and_b64 vcc, exec, s[20:21]
	s_cbranch_vccz .LBB0_1953
	s_barrier

.LBB0_2033:
	v_add_u32_e32 v124, 0x10000, v199
	v_add_u32_e32 v156, 0x14000, v199
	ds_read_b128 v[96:99], v124
	ds_read_b128 v[108:111], v124 offset:1024
	ds_read_b128 v[120:123], v124 offset:2048
	ds_read_b128 v[124:127], v124 offset:3072
	ds_read_b128 v[128:131], v156
	ds_read_b128 v[132:135], v156 offset:1024
	ds_read_b128 v[152:155], v156 offset:2048
	ds_read_b128 v[156:159], v156 offset:3072
	s_add_i32 s48, s13, 0xffe9c080
	s_cmpk_eq_i32 s12, 0x54
	s_cselect_b32 s41, s23, s45
	s_cselect_b32 s40, s22, s44
	s_cselect_b32 s43, s29, s47
	s_cselect_b32 s42, s28, s46
	s_cselect_b32 s57, 0, s48
	s_cselect_b32 s49, s31, s53
	s_cselect_b32 s48, s30, s52
	s_cselect_b32 s51, s35, s5
	s_cselect_b32 s50, s34, s4
	s_mov_b32 m0, s83
	ds_read_b128 v[160:163], v200
	ds_read_b128 v[164:167], v200 offset:1024
	ds_read_b128 v[168:171], v200 offset:2048
	ds_read_b128 v[178:181], v200 offset:3072
	ds_read_b128 v[182:185], v200 offset:4096
	ds_read_b128 v[186:189], v200 offset:5120
	ds_read_b128 v[190:193], v200 offset:6144
	ds_read_b128 v[194:197], v200 offset:7168
	buffer_load_dwordx4 v176, s[44:47], s13 offen lds
	s_mov_b32 m0, s89
	s_nop 0
	buffer_load_dwordx4 v198, s[44:47], s13 offen lds
	s_waitcnt vmcnt(8)
	s_waitcnt lgkmcnt(0)
	s_barrier
	s_setprio 1
	s_waitcnt lgkmcnt(7)
	v_mfma_f32_16x16x32_bf16 v[148:151], v[96:99], v[160:163], v[148:151]
	v_mfma_f32_16x16x32_bf16 v[144:147], v[120:123], v[160:163], v[144:147]
	s_waitcnt lgkmcnt(5)
	v_mfma_f32_16x16x32_bf16 v[116:119], v[96:99], v[168:171], v[116:119]
	v_mfma_f32_16x16x32_bf16 v[112:115], v[120:123], v[168:171], v[112:115]
	s_waitcnt lgkmcnt(3)
	v_mfma_f32_16x16x32_bf16 v[92:95], v[96:99], v[182:185], v[92:95]
	v_mfma_f32_16x16x32_bf16 v[88:91], v[120:123], v[182:185], v[88:91]
	s_waitcnt lgkmcnt(1)
	v_mfma_f32_16x16x32_bf16 v[76:79], v[96:99], v[190:193], v[76:79]
	v_mfma_f32_16x16x32_bf16 v[72:75], v[120:123], v[190:193], v[72:75]
	v_mfma_f32_16x16x32_bf16 v[148:151], v[108:111], v[164:167], v[148:151]
	v_mfma_f32_16x16x32_bf16 v[144:147], v[124:127], v[164:167], v[144:147]
	v_mfma_f32_16x16x32_bf16 v[116:119], v[108:111], v[178:181], v[116:119]
	v_mfma_f32_16x16x32_bf16 v[112:115], v[124:127], v[178:181], v[112:115]
	v_mfma_f32_16x16x32_bf16 v[92:95], v[108:111], v[186:189], v[92:95]
	v_mfma_f32_16x16x32_bf16 v[88:91], v[124:127], v[186:189], v[88:91]
	s_waitcnt lgkmcnt(0)
	v_mfma_f32_16x16x32_bf16 v[76:79], v[108:111], v[194:197], v[76:79]
	v_mfma_f32_16x16x32_bf16 v[72:75], v[124:127], v[194:197], v[72:75]
	s_setprio 2
	s_setprio 1
	v_mfma_f32_16x16x32_bf16 v[140:143], v[128:131], v[160:163], v[140:143]
	v_mfma_f32_16x16x32_bf16 v[136:139], v[152:155], v[160:163], v[136:139]
	v_mfma_f32_16x16x32_bf16 v[104:107], v[128:131], v[168:171], v[104:107]
	v_mfma_f32_16x16x32_bf16 v[100:103], v[152:155], v[168:171], v[100:103]
	v_mfma_f32_16x16x32_bf16 v[84:87], v[128:131], v[182:185], v[84:87]
	v_mfma_f32_16x16x32_bf16 v[80:83], v[152:155], v[182:185], v[80:83]
	v_mfma_f32_16x16x32_bf16 v[68:71], v[128:131], v[190:193], v[68:71]
	v_mfma_f32_16x16x32_bf16 v[64:67], v[152:155], v[190:193], v[64:67]
	v_mfma_f32_16x16x32_bf16 v[140:143], v[132:135], v[164:167], v[140:143]
	v_mfma_f32_16x16x32_bf16 v[136:139], v[156:159], v[164:167], v[136:139]
	v_mfma_f32_16x16x32_bf16 v[104:107], v[132:135], v[178:181], v[104:107]
	v_mfma_f32_16x16x32_bf16 v[100:103], v[156:159], v[178:181], v[100:103]
	v_mfma_f32_16x16x32_bf16 v[84:87], v[132:135], v[186:189], v[84:87]
	v_mfma_f32_16x16x32_bf16 v[80:83], v[156:159], v[186:189], v[80:83]
	v_mfma_f32_16x16x32_bf16 v[68:71], v[132:135], v[194:197], v[68:71]
	v_mfma_f32_16x16x32_bf16 v[64:67], v[156:159], v[194:197], v[64:67]
	s_setprio 2
	s_barrier
	s_mov_b32 m0, s65
	ds_read_b128 v[160:163], v200 offset:16384
	ds_read_b128 v[164:167], v200 offset:17408
	ds_read_b128 v[168:171], v200 offset:18432
	ds_read_b128 v[178:181], v200 offset:19456
	ds_read_b128 v[182:185], v200 offset:20480
	ds_read_b128 v[186:189], v200 offset:21504
	ds_read_b128 v[190:193], v200 offset:22528
	ds_read_b128 v[194:197], v200 offset:23552
	buffer_load_dwordx4 v174, s[48:51], s57 offen lds
	s_mov_b32 m0, s66
	s_add_i32 s95, s57, 0x164000
	buffer_load_dwordx4 v175, s[48:51], s57 offen lds
	s_mov_b32 m0, s67
	s_nop 0
	buffer_load_dwordx4 v174, s[48:51], s95 offen lds
	s_mov_b32 m0, s68
	s_nop 0
	buffer_load_dwordx4 v175, s[48:51], s95 offen lds
	s_mov_b32 m0, s64
	s_nop 0
	buffer_load_dwordx4 v176, s[40:43], s57 offen lds
	s_mov_b32 m0, s69
	s_nop 0
	buffer_load_dwordx4 v198, s[40:43], s57 offen lds
	s_waitcnt vmcnt(8)
	s_waitcnt lgkmcnt(0)
	s_barrier
	s_setprio 1
	s_waitcnt lgkmcnt(7)
	v_mfma_f32_16x16x32_bf16 v[60:63], v[96:99], v[160:163], v[60:63]
	v_mfma_f32_16x16x32_bf16 v[48:51], v[120:123], v[160:163], v[48:51]
	s_waitcnt lgkmcnt(5)
	v_mfma_f32_16x16x32_bf16 v[44:47], v[96:99], v[168:171], v[44:47]
	v_mfma_f32_16x16x32_bf16 v[40:43], v[120:123], v[168:171], v[40:43]
	s_waitcnt lgkmcnt(3)
	v_mfma_f32_16x16x32_bf16 v[28:31], v[96:99], v[182:185], v[28:31]
	v_mfma_f32_16x16x32_bf16 v[24:27], v[120:123], v[182:185], v[24:27]
	s_waitcnt lgkmcnt(1)
	v_mfma_f32_16x16x32_bf16 v[12:15], v[96:99], v[190:193], v[12:15]
	v_mfma_f32_16x16x32_bf16 v[8:11], v[120:123], v[190:193], v[8:11]
	v_mfma_f32_16x16x32_bf16 v[60:63], v[108:111], v[164:167], v[60:63]
	v_mfma_f32_16x16x32_bf16 v[48:51], v[124:127], v[164:167], v[48:51]
	v_mfma_f32_16x16x32_bf16 v[44:47], v[108:111], v[178:181], v[44:47]
	v_mfma_f32_16x16x32_bf16 v[40:43], v[124:127], v[178:181], v[40:43]
	v_mfma_f32_16x16x32_bf16 v[28:31], v[108:111], v[186:189], v[28:31]
	v_mfma_f32_16x16x32_bf16 v[24:27], v[124:127], v[186:189], v[24:27]
	s_waitcnt lgkmcnt(0)
	v_mfma_f32_16x16x32_bf16 v[12:15], v[108:111], v[194:197], v[12:15]
	v_mfma_f32_16x16x32_bf16 v[8:11], v[124:127], v[194:197], v[8:11]
	s_setprio 2
	s_setprio 1
	v_mfma_f32_16x16x32_bf16 v[56:59], v[128:131], v[160:163], v[56:59]
	v_mfma_f32_16x16x32_bf16 v[52:55], v[152:155], v[160:163], v[52:55]
	v_mfma_f32_16x16x32_bf16 v[36:39], v[128:131], v[168:171], v[36:39]
	v_mfma_f32_16x16x32_bf16 v[32:35], v[152:155], v[168:171], v[32:35]
	v_mfma_f32_16x16x32_bf16 v[20:23], v[128:131], v[182:185], v[20:23]
	v_mfma_f32_16x16x32_bf16 v[16:19], v[152:155], v[182:185], v[16:19]
	v_mfma_f32_16x16x32_bf16 v[4:7], v[128:131], v[190:193], v[4:7]
	v_mfma_f32_16x16x32_bf16 v[0:3], v[152:155], v[190:193], v[0:3]
	v_mfma_f32_16x16x32_bf16 v[56:59], v[132:135], v[164:167], v[56:59]
	v_mfma_f32_16x16x32_bf16 v[52:55], v[156:159], v[164:167], v[52:55]
	v_mfma_f32_16x16x32_bf16 v[36:39], v[132:135], v[178:181], v[36:39]
	v_mfma_f32_16x16x32_bf16 v[32:35], v[156:159], v[178:181], v[32:35]
	v_mfma_f32_16x16x32_bf16 v[20:23], v[132:135], v[186:189], v[20:23]
	v_mfma_f32_16x16x32_bf16 v[16:19], v[156:159], v[186:189], v[16:19]
	v_mfma_f32_16x16x32_bf16 v[4:7], v[132:135], v[194:197], v[4:7]
	v_mfma_f32_16x16x32_bf16 v[0:3], v[156:159], v[194:197], v[0:3]
	s_setprio 2
	s_barrier
	v_add_u32_e32 v124, 0x18000, v199
	v_add_u32_e32 v156, 0x1c000, v199
	ds_read_b128 v[96:99], v124
	ds_read_b128 v[108:111], v124 offset:1024
	ds_read_b128 v[120:123], v124 offset:2048
	ds_read_b128 v[124:127], v124 offset:3072
	ds_read_b128 v[128:131], v156
	ds_read_b128 v[132:135], v156 offset:1024
	ds_read_b128 v[152:155], v156 offset:2048
	ds_read_b128 v[156:159], v156 offset:3072
	s_mov_b32 m0, s70
	ds_read_b128 v[160:163], v200 offset:32768
	ds_read_b128 v[164:167], v200 offset:33792
	ds_read_b128 v[168:171], v200 offset:34816
	ds_read_b128 v[178:181], v200 offset:35840
	ds_read_b128 v[182:185], v200 offset:36864
	ds_read_b128 v[186:189], v200 offset:37888
	ds_read_b128 v[190:193], v200 offset:38912
	ds_read_b128 v[194:197], v200 offset:39936
	buffer_load_dwordx4 v176, s[40:43], s95 offen lds
	s_mov_b32 m0, s71
	s_nop 0
	buffer_load_dwordx4 v198, s[40:43], s95 offen lds
	s_waitcnt vmcnt(8)
	s_waitcnt lgkmcnt(0)
	s_barrier
	s_setprio 1
	s_waitcnt lgkmcnt(7)
	v_mfma_f32_16x16x32_bf16 v[148:151], v[96:99], v[160:163], v[148:151]
	v_mfma_f32_16x16x32_bf16 v[144:147], v[120:123], v[160:163], v[144:147]
	s_waitcnt lgkmcnt(5)
	v_mfma_f32_16x16x32_bf16 v[116:119], v[96:99], v[168:171], v[116:119]
	v_mfma_f32_16x16x32_bf16 v[112:115], v[120:123], v[168:171], v[112:115]
	s_waitcnt lgkmcnt(3)
	v_mfma_f32_16x16x32_bf16 v[92:95], v[96:99], v[182:185], v[92:95]
	v_mfma_f32_16x16x32_bf16 v[88:91], v[120:123], v[182:185], v[88:91]
	s_waitcnt lgkmcnt(1)
	v_mfma_f32_16x16x32_bf16 v[76:79], v[96:99], v[190:193], v[76:79]
	v_mfma_f32_16x16x32_bf16 v[72:75], v[120:123], v[190:193], v[72:75]
	v_mfma_f32_16x16x32_bf16 v[148:151], v[108:111], v[164:167], v[148:151]
	v_mfma_f32_16x16x32_bf16 v[144:147], v[124:127], v[164:167], v[144:147]
	v_mfma_f32_16x16x32_bf16 v[116:119], v[108:111], v[178:181], v[116:119]
	v_mfma_f32_16x16x32_bf16 v[112:115], v[124:127], v[178:181], v[112:115]
	v_mfma_f32_16x16x32_bf16 v[92:95], v[108:111], v[186:189], v[92:95]
	v_mfma_f32_16x16x32_bf16 v[88:91], v[124:127], v[186:189], v[88:91]
	s_waitcnt lgkmcnt(0)
	v_mfma_f32_16x16x32_bf16 v[76:79], v[108:111], v[194:197], v[76:79]
	v_mfma_f32_16x16x32_bf16 v[72:75], v[124:127], v[194:197], v[72:75]
	s_setprio 2
	s_setprio 1
	v_mfma_f32_16x16x32_bf16 v[140:143], v[128:131], v[160:163], v[140:143]
	v_mfma_f32_16x16x32_bf16 v[136:139], v[152:155], v[160:163], v[136:139]
	v_mfma_f32_16x16x32_bf16 v[104:107], v[128:131], v[168:171], v[104:107]
	v_mfma_f32_16x16x32_bf16 v[100:103], v[152:155], v[168:171], v[100:103]
	v_mfma_f32_16x16x32_bf16 v[84:87], v[128:131], v[182:185], v[84:87]
	v_mfma_f32_16x16x32_bf16 v[80:83], v[152:155], v[182:185], v[80:83]
	v_mfma_f32_16x16x32_bf16 v[68:71], v[128:131], v[190:193], v[68:71]
	v_mfma_f32_16x16x32_bf16 v[64:67], v[152:155], v[190:193], v[64:67]
	v_mfma_f32_16x16x32_bf16 v[140:143], v[132:135], v[164:167], v[140:143]
	v_mfma_f32_16x16x32_bf16 v[136:139], v[156:159], v[164:167], v[136:139]
	v_mfma_f32_16x16x32_bf16 v[104:107], v[132:135], v[178:181], v[104:107]
	v_mfma_f32_16x16x32_bf16 v[100:103], v[156:159], v[178:181], v[100:103]
	v_mfma_f32_16x16x32_bf16 v[84:87], v[132:135], v[186:189], v[84:87]
	v_mfma_f32_16x16x32_bf16 v[80:83], v[156:159], v[186:189], v[80:83]
	v_mfma_f32_16x16x32_bf16 v[68:71], v[132:135], v[194:197], v[68:71]
	v_mfma_f32_16x16x32_bf16 v[64:67], v[156:159], v[194:197], v[64:67]
	s_setprio 2
	s_barrier
	s_mov_b32 m0, s72
	s_or_b32 s95, s57, 0x80
	ds_read_b128 v[160:163], v200 offset:49152
	ds_read_b128 v[164:167], v200 offset:50176
	ds_read_b128 v[168:171], v200 offset:51200
	ds_read_b128 v[178:181], v200 offset:52224
	ds_read_b128 v[182:185], v200 offset:53248
	ds_read_b128 v[186:189], v200 offset:54272
	ds_read_b128 v[190:193], v200 offset:55296
	ds_read_b128 v[194:197], v200 offset:56320
	buffer_load_dwordx4 v174, s[48:51], s95 offen lds
	s_mov_b32 m0, s73
	s_add_i32 s57, s57, 0x164080
	buffer_load_dwordx4 v175, s[48:51], s95 offen lds
	s_mov_b32 m0, s76
	s_nop 0
	buffer_load_dwordx4 v174, s[48:51], s57 offen lds
	s_mov_b32 m0, s77
	s_nop 0
	buffer_load_dwordx4 v175, s[48:51], s57 offen lds
	s_mov_b32 m0, s74
	s_nop 0
	buffer_load_dwordx4 v176, s[40:43], s95 offen lds
	s_mov_b32 m0, s75
	s_nop 0
	buffer_load_dwordx4 v198, s[40:43], s95 offen lds
	s_waitcnt vmcnt(8)
	s_waitcnt lgkmcnt(0)
	s_barrier
	s_setprio 1
	s_waitcnt lgkmcnt(7)
	v_mfma_f32_16x16x32_bf16 v[60:63], v[96:99], v[160:163], v[60:63]
	v_mfma_f32_16x16x32_bf16 v[48:51], v[120:123], v[160:163], v[48:51]
	s_waitcnt lgkmcnt(5)
	v_mfma_f32_16x16x32_bf16 v[44:47], v[96:99], v[168:171], v[44:47]
	v_mfma_f32_16x16x32_bf16 v[40:43], v[120:123], v[168:171], v[40:43]
	s_waitcnt lgkmcnt(3)
	v_mfma_f32_16x16x32_bf16 v[28:31], v[96:99], v[182:185], v[28:31]
	v_mfma_f32_16x16x32_bf16 v[24:27], v[120:123], v[182:185], v[24:27]
	s_waitcnt lgkmcnt(1)
	v_mfma_f32_16x16x32_bf16 v[12:15], v[96:99], v[190:193], v[12:15]
	v_mfma_f32_16x16x32_bf16 v[8:11], v[120:123], v[190:193], v[8:11]
	v_mfma_f32_16x16x32_bf16 v[60:63], v[108:111], v[164:167], v[60:63]
	v_mfma_f32_16x16x32_bf16 v[48:51], v[124:127], v[164:167], v[48:51]
	v_mfma_f32_16x16x32_bf16 v[44:47], v[108:111], v[178:181], v[44:47]
	v_mfma_f32_16x16x32_bf16 v[40:43], v[124:127], v[178:181], v[40:43]
	v_mfma_f32_16x16x32_bf16 v[28:31], v[108:111], v[186:189], v[28:31]
	v_mfma_f32_16x16x32_bf16 v[24:27], v[124:127], v[186:189], v[24:27]
	s_waitcnt lgkmcnt(0)
	v_mfma_f32_16x16x32_bf16 v[12:15], v[108:111], v[194:197], v[12:15]
	v_mfma_f32_16x16x32_bf16 v[8:11], v[124:127], v[194:197], v[8:11]
	s_setprio 2
	s_setprio 1
	v_mfma_f32_16x16x32_bf16 v[56:59], v[128:131], v[160:163], v[56:59]
	v_mfma_f32_16x16x32_bf16 v[52:55], v[152:155], v[160:163], v[52:55]
	v_mfma_f32_16x16x32_bf16 v[36:39], v[128:131], v[168:171], v[36:39]
	v_mfma_f32_16x16x32_bf16 v[32:35], v[152:155], v[168:171], v[32:35]
	v_mfma_f32_16x16x32_bf16 v[20:23], v[128:131], v[182:185], v[20:23]
	v_mfma_f32_16x16x32_bf16 v[16:19], v[152:155], v[182:185], v[16:19]
	v_mfma_f32_16x16x32_bf16 v[4:7], v[128:131], v[190:193], v[4:7]
	v_mfma_f32_16x16x32_bf16 v[0:3], v[152:155], v[190:193], v[0:3]
	v_mfma_f32_16x16x32_bf16 v[56:59], v[132:135], v[164:167], v[56:59]
	v_mfma_f32_16x16x32_bf16 v[52:55], v[156:159], v[164:167], v[52:55]
	v_mfma_f32_16x16x32_bf16 v[36:39], v[132:135], v[178:181], v[36:39]
	v_mfma_f32_16x16x32_bf16 v[32:35], v[156:159], v[178:181], v[32:35]
	v_mfma_f32_16x16x32_bf16 v[20:23], v[132:135], v[186:189], v[20:23]
	v_mfma_f32_16x16x32_bf16 v[16:19], v[156:159], v[186:189], v[16:19]
	v_mfma_f32_16x16x32_bf16 v[4:7], v[132:135], v[194:197], v[4:7]
	v_mfma_f32_16x16x32_bf16 v[0:3], v[156:159], v[194:197], v[0:3]
	s_setprio 2
	s_barrier
	s_add_i32 s12, s12, 2
	s_addk_i32 s13, 0x100
	s_cmpk_gt_u32 s12, 0x55
	s_cbranch_scc0 .LBB0_2033
	s_and_b64 vcc, exec, s[20:21]
	s_cbranch_vccz .LBB0_2036
	s_barrier
